# v55 stack + workspace aliasing: Y, XG, YE reuse the dead in-proj buffer; next-layer HN reuses the dead expert-H buffer; fp8 HN reuses the dead CAT buffer (fewer dirty lines to write back)
# baseline (speedup 1.0000x reference)
; #define GAS __attribute__((address_space(1)))
; #define LAS __attribute__((address_space(3)))
; __device__ __forceinline__ unsigned pk2(float lo, float hi) { const m_f32x2 v = {lo, hi}; return __builtin_bit_cast(unsigned, __builtin_convertvector(v, m_bf16x2)); }
; __device__ __forceinline__ float rsq(float x) { return __builtin_amdgcn_rsqf(x); }
; __device__ __forceinline__ void prologue2(Frame& F) {
;     ...
;     for (int m = gw; m < M; m += NGW) { const int b = m >> 12; f32x4 v[4]; row_load(INP(F, I_X) + (size_t)m * DM, lane, v);
;         const LAS f32x4* Bv = (const LAS f32x4*)(PV + b * 2048); const float rstd = rsq(row_ss(v, lane) * (1.0f / DM) + EPS); GAS v2u* orow = (GAS v2u*)((GAS bf16*)(F.ws + WS_HN) + (size_t)m * DM);
; #pragma unroll
;         for (int j = 0; j < 4; ++j) { const int c4 = lane + 64 * j; const f32x4 o4 = v[j] * rstd * Bv[c4] + Bv[256 + c4]; v2u o; o.x = pk2(o4[0], o4[1]); o.y = pk2(o4[2], o4[3]); orow[c4] = o; } }
.LBB0_130:
	s_or_b64 exec, exec, s[0:1]
	s_lshl_b32 s0, s38, 3
	s_add_i32 s0, s89, s0
	s_lshl_b32 s4, s33, 3
	s_cmpk_gt_i32 s0, 0x3fff
	s_waitcnt lgkmcnt(0)
	s_barrier
	s_cbranch_scc1 .LBB0_133
	s_add_i32 s1, 0, 0x20000
	v_mov_b32_e32 v1, s1
	s_ashr_i32 s1, s0, 31
	ds_read_b64 v[2:3], v1
	s_lshl_b64 s[2:3], s[0:1], 11
	s_add_u32 s2, s58, s2
	v_lshlrev_b32_e32 v4, 3, v186
	v_mov_b32_e32 v5, 0
	s_addc_u32 s3, s59, s3
	v_lshlrev_b32_e32 v7, 4, v186
	v_lshl_add_u64 v[4:5], s[2:3], 0, v[4:5]
	s_mov_b64 s[2:3], 0x18400000
	s_ashr_i32 s5, s4, 31
	s_lshl_b64 s[6:7], s[0:1], 12
	v_add_u32_e32 v1, 0, v7
	v_lshl_add_u64 v[4:5], v[4:5], 0, s[2:3]
	s_lshl_b64 s[2:3], s[4:5], 11
	v_or_b32_e32 v8, s6, v7
	v_mov_b32_e32 v9, s7
	s_lshl_b64 s[6:7], s[4:5], 12
	v_mov_b32_e32 v7, 0x358637bd
	s_mov_b32 s1, s0

; #define PG8_STAGE(bufoff, gbase, voff) do { _Pragma("unroll") for (int _i = 0; _i < 2; ++_i) \
;         __builtin_amdgcn_global_load_lds((const unsigned*)((const char*)(gbase) + (voff)[_i]), (PG8_LAS unsigned*)(lds + (bufoff) + ldsw + _i * 8192), 16, 0, 0); } while (0)
; #define PG8_WAIT_V(n) asm volatile("s_waitcnt vmcnt(" #n ")" ::: "memory")
; #define PG8_BAR __builtin_amdgcn_s_barrier()
; template <class Epi, class Sched, bool ALIGN_EPI = false, bool SP2 = false, bool F8 = false, bool BTILED = false, bool ATILED = false>
; __device__ __forceinline__ void gemm_phase(PG8_LAS unsigned char* lds, const Gemm g, const Sched& S, const Epi& E) {
;     ...
;     const char* cA = (const char*)g.A + (size_t)cur.pm * tstep; const char* cB = (const char*)g.Bt + (size_t)cur.pn * tstep;
;     S.a_ready(cur);
;     if constexpr (SP2) {
;         PG8_STAGE(PG8_SB(0, 0), cB, voffB); PG8_STAGE(PG8_SB(0, 1), cB + hstepB, voffB); PG8_STAGE(PG8_SA(0, 0), cA, voffA); PG8_STAGE(PG8_SA(0, 1), cA + hstepA, voffA);
;         if (wr == 1) PG8_BAR;
;         PG8_WAIT_V(2); PG8_BAR;
;         PG8_STAGE(PG8_SB(1, 0), cB + kstepB, voffB); PG8_STAGE(PG8_SA(1, 0), cA + kstepA, voffA); PG8_STAGE(PG8_SB(1, 1), cB + hstepB + kstepB, voffB);
;         PG8_WAIT_V(6); PG8_BAR;
;     } else {
;         PG8_STAGE(PG8_SB(0, 0), cB, voffB); PG8_STAGE(PG8_SA(0, 0), cA, voffA); PG8_STAGE(PG8_SB(0, 1), cB + hstepB, voffB); PG8_STAGE(PG8_SA(0, 1), cA + hstepA, voffA);
;         if (wr == 1) PG8_BAR;
;         PG8_WAIT_V(4); PG8_BAR;
;         PG8_STAGE(PG8_SB(1, 0), cB + kstepB, voffB); PG8_STAGE(PG8_SA(1, 0), cA + kstepA, voffA); PG8_STAGE(PG8_SB(1, 1), cB + hstepB + kstepB, voffB);
;         PG8_WAIT_V(6); PG8_BAR;
; __global__ void __launch_bounds__(NTHR, 2) fwd_kernel(Args args) {
;     ...
;             pg8::Gemm g{(const pg8::bf16_t*)(F.ws + WS_HN), (const pg8::bf16_t*)(F.ws + WS_WIN) + (size_t)l * NPROJ * DM, M, NPROJ, DM};
;             pg8::StaticOrder S; S.init(M, NPROJ, F.G, (int)blockIdx.x);
;             pg8::EpiBf16<0> E{(pg8::bf16_t*)(F.ws + WS_PROJ), NPROJ, nullptr, 0, 0, 1.f};
;             pg8::gemm_phase<pg8::EpiBf16<0>, pg8::StaticOrder, true, true>(F.lds, g, S, E);
.LBB0_287:
	s_mul_i32 s0, s54, 10
	s_add_i32 s2, s0, 2
	s_cmp_le_i32 s86, s2
	v_writelane_b32 v255, s0, 2
	s_cselect_b64 s[0:1], -1, 0
	s_cmp_lt_i32 s2, s87
	s_cselect_b64 s[2:3], -1, 0
	s_and_b64 s[0:1], s[0:1], s[2:3]
	s_andn2_b64 vcc, exec, s[0:1]
	s_cbranch_vccnz .LBB0_329
	v_readlane_b32 s2, v254, 8
	v_readlane_b32 s3, v254, 9
	v_mov_b32_e32 v1, v0
	v_writelane_b32 v254, s2, 8
	v_mov_b32_e32 v10, v0
	s_nop 0
	v_writelane_b32 v254, s3, 9
	s_nop 0
	v_readlane_b32 s2, v254, 59
	v_readlane_b32 s27, v254, 2
	v_readlane_b32 s3, v254, 60
	s_and_b64 vcc, exec, s[2:3]
	v_readfirstlane_b32 s26, v1
	v_readfirstlane_b32 s4, v10
	s_cbranch_vccnz .LBB0_304
	v_lshlrev_b32_e32 v2, 4, v10
	v_add_u32_e32 v3, 0x2000, v2
	v_ashrrev_i32_e32 v4, 31, v3
	v_lshrrev_b32_e32 v4, 22, v4
	v_add_u32_e32 v4, v3, v4
	v_ashrrev_i32_e32 v11, 10, v4
	v_mul_i32_i24_e32 v4, 0x400, v11
	v_sub_u32_e32 v3, v3, v4
	v_lshrrev_b32_e32 v4, 4, v3
	v_bitop3_b32 v3, v4, v3, 32 bitop3:0x6c
	v_ashrrev_i32_e32 v4, 31, v3
	s_mul_i32 s94, s54, 0x280000
	s_add_u32 s28, s58, 0x18400000
	v_lshrrev_b32_e32 v4, 26, v4
	s_addc_u32 s29, s59, 0
	s_lshl_b64 s[2:3], s[94:95], 1
	v_add_u32_e32 v4, v3, v4
	v_lshlrev_b32_e32 v5, 3, v11
	s_add_u32 s2, s58, s2
	v_ashrrev_i32_e32 v12, 6, v4
	v_and_b32_e32 v5, -16, v5
	s_addc_u32 s3, s59, s3
	v_add_u32_e32 v5, v12, v5
	s_add_u32 s30, s2, 0x1600000
	s_waitcnt vmcnt(0)
	v_and_b32_e32 v6, 3, v12
	s_mov_b32 s2, 0x1fffe0
	v_lshrrev_b32_e32 v7, 2, v5
	v_lshlrev_b32_e32 v8, 1, v5
	v_and_b32_e32 v4, 0xc0, v4
	v_and_or_b32 v6, v5, s2, v6
	v_and_b32_e32 v7, 4, v7
	v_and_b32_e32 v8, 24, v8
	v_sub_u32_e32 v3, v3, v4
	v_or3_b32 v6, v6, v7, v8
	v_lshlrev_b32_e32 v7, 5, v11
	v_ashrrev_i16_sdwa v3, v224, sext(v3) dst_sel:DWORD dst_unused:UNUSED_PAD src0_sel:DWORD src1_sel:BYTE_0
	v_and_b32_e32 v7, 32, v7
	v_bfe_i32 v13, v3, 0, 16
	v_add_lshl_u32 v3, v7, v13, 1
	v_lshl_add_u32 v130, v6, 11, v3
	v_lshl_add_u32 v132, v5, 11, v3
	v_bfe_i32 v3, v10, 27, 1
	v_lshrrev_b32_e32 v3, 22, v3
	v_add_u32_e32 v3, v2, v3
	v_and_b32_e32 v3, 0xfffffc00, v3
	v_sub_u32_e32 v2, v2, v3
	v_lshrrev_b32_e32 v3, 4, v2
	v_ashrrev_i32_e32 v4, 31, v10
	v_bitop3_b32 v2, v3, v2, 32 bitop3:0x6c
	v_lshrrev_b32_e32 v4, 26, v4
	v_ashrrev_i32_e32 v3, 31, v2
	v_add_u32_e32 v4, v10, v4
	v_lshrrev_b32_e32 v3, 26, v3
	v_ashrrev_i32_e32 v15, 6, v4
	v_add_u32_e32 v3, v2, v3
	v_lshlrev_b32_e32 v4, 3, v15
	v_ashrrev_i32_e32 v14, 6, v3
	v_and_b32_e32 v4, -16, v4
	v_add_u32_e32 v4, v14, v4
	v_and_b32_e32 v5, 3, v14
	v_lshrrev_b32_e32 v6, 2, v4
	v_lshlrev_b32_e32 v7, 1, v4
	v_and_b32_e32 v3, 0xc0, v3
	s_addc_u32 s31, s3, 0
	s_ashr_i32 s12, s4, 6
	v_and_or_b32 v5, v4, s2, v5
	v_and_b32_e32 v6, 4, v6
	v_and_b32_e32 v7, 24, v7
	v_sub_u32_e32 v2, v2, v3
	s_ashr_i32 s5, s4, 8
	s_lshl_b32 s34, s12, 10
	v_or3_b32 v5, v5, v6, v7
	v_lshlrev_b32_e32 v6, 5, v15
	v_ashrrev_i16_sdwa v2, v224, sext(v2) dst_sel:DWORD dst_unused:UNUSED_PAD src0_sel:DWORD src1_sel:BYTE_0
	v_readlane_b32 s2, v254, 24
	v_and_b32_e32 v6, 32, v6
	v_bfe_i32 v16, v2, 0, 16
	v_readlane_b32 s3, v254, 25
	s_add_u32 s22, s30, s2
	v_add_lshl_u32 v2, v6, v16, 1
	s_addc_u32 s23, s31, s3
	s_add_i32 s35, s34, 0
	v_lshl_add_u32 v182, v5, 11, v2
	s_add_i32 m0, s35, 0x10000
	v_lshl_add_u32 v134, v4, 11, v2
	global_load_lds_dwordx4 v182, s[22:23]
	s_add_i32 m0, s35, 0x12000
	s_add_u32 s2, s22, 0x40000
	global_load_lds_dwordx4 v130, s[22:23]
	s_addc_u32 s3, s23, 0
	s_add_i32 m0, s35, 0x14000
	v_mov_b32_e32 v131, v183
	global_load_lds_dwordx4 v182, s[2:3]
	s_add_i32 m0, s35, 0x16000
	v_mov_b32_e32 v135, v183
	global_load_lds_dwordx4 v130, s[2:3]
	v_readlane_b32 s2, v254, 51
	v_readlane_b32 s3, v254, 52
	s_add_u32 s2, s28, s2
	s_addc_u32 s3, s29, s3
	s_add_i32 s36, s35, 0x2000
	s_mov_b32 m0, s35
	s_add_u32 s8, s2, 0x40000
	global_load_lds_dwordx4 v134, s[2:3]
	s_mov_b32 m0, s36
	s_addc_u32 s9, s3, 0
	s_add_i32 s37, s35, 0x4000
	global_load_lds_dwordx4 v132, s[2:3]
	s_mov_b32 m0, s37
	s_add_i32 s38, s35, 0x6000
	global_load_lds_dwordx4 v134, s[8:9]
	s_mov_b32 m0, s38
	v_mov_b32_e32 v133, v183
	global_load_lds_dwordx4 v132, s[8:9]
	s_cmp_eq_u32 s5, 1
	v_lshl_add_u64 v[8:9], s[22:23], 0, v[182:183]
	v_lshl_add_u64 v[6:7], s[22:23], 0, v[130:131]
	v_lshl_add_u64 v[2:3], s[2:3], 0, v[134:135]
	s_cselect_b64 s[8:9], -1, 0
	s_cmp_lg_u32 s5, 1
	v_lshl_add_u64 v[4:5], s[2:3], 0, v[132:133]
	s_cbranch_scc1 .LBB0_291
	s_barrier

; __global__ void __launch_bounds__(NTHR, 2) fwd_kernel(Args args) {
;     ...
;             pg8::Gemm g{(const pg8::bf16_t*)(F.ws + WS_CAT), (const pg8::bf16_t*)(F.ws + WS_WOUT) + (size_t)l * DM * DM, M, DM, DM};
;             pg8::StaticOrder S; S.init(M, DM, F.G, (int)blockIdx.x);
;             pg8::EpiBf16Row E{(pg8::bf16_t*)(F.ws + WS_Y), DM, nullptr, 1.0f};
;             pg8::gemm_phase<pg8::EpiBf16Row, pg8::StaticOrder, true, true>(F.lds, g, S, E);
.LBB0_1068:
	s_add_u32 s8, s58, 0x4400000
	s_addc_u32 s9, s59, 0
	s_lshl_b32 s10, s10, 5
	s_and_b32 s13, s10, 0x60
	s_add_i32 m0, s31, 0x18000
	v_lshl_add_u64 v[8:9], v[8:9], 0, s[90:91]
	s_lshl_b32 s12, s5, 13
	s_lshl_b32 s14, s13, 7
	s_waitcnt vmcnt(2)
	s_barrier
	global_load_lds_dwordx4 v[8:9], off
	v_lshl_add_u64 v[6:7], v[6:7], 0, s[90:91]
	s_add_i32 m0, s31, 0x1a000
	s_add_i32 s37, s31, 0x8000
	s_add_i32 s38, s31, 0xa000
	global_load_lds_dwordx4 v[6:7], off
	v_lshl_add_u64 v[2:3], v[2:3], 0, s[90:91]
	s_mov_b32 m0, s37
	s_add_u32 s10, s20, 0x40080
	global_load_lds_dwordx4 v[2:3], off
	v_lshl_add_u64 v[2:3], v[4:5], 0, s[90:91]
	s_mov_b32 m0, s38
	s_addc_u32 s11, s21, 0
	global_load_lds_dwordx4 v[2:3], off
	s_add_i32 m0, s31, 0x1c000
	v_lshl_add_u64 v[2:3], s[10:11], 0, v[182:183]
	global_load_lds_dwordx4 v[2:3], off
	v_lshl_add_u64 v[2:3], s[10:11], 0, v[130:131]
	s_add_i32 m0, s31, 0x1e000
	s_cmpk_lt_u32 s4, 0x100
	global_load_lds_dwordx4 v[2:3], off
	v_lshrrev_b32_e32 v3, 1, v10
	v_and_b32_e32 v3, 24, v3
	v_and_b32_e32 v2, 15, v10
	v_lshlrev_b32_e32 v4, 1, v3
	v_lshl_or_b32 v142, s5, 6, v2
	v_lshl_or_b32 v2, v2, 6, v4
	v_lshlrev_b32_e32 v4, 2, v10
	v_and_b32_e32 v4, 32, v4
	v_bitop3_b32 v5, v2, s12, v4 bitop3:0xde
	v_bitop3_b32 v143, v2, s14, v4 bitop3:0xde
	v_lshlrev_b32_e32 v2, 14, v15
	v_and_b32_e32 v2, 0xffff8000, v2
	v_or_b32_e32 v144, s13, v3
	v_lshl_add_u32 v2, v14, 11, v2
	v_and_b32_e32 v3, 1, v15
	v_lshl_or_b32 v2, v3, 6, v2
	v_lshl_add_u32 v136, v16, 1, v2
	v_lshlrev_b32_e32 v2, 14, v11
	v_and_b32_e32 v2, 0xffff8000, v2
	s_waitcnt vmcnt(6)
	v_lshl_add_u32 v2, v12, 11, v2
	v_and_b32_e32 v3, 1, v11
	v_lshl_or_b32 v2, v3, 6, v2
	v_readlane_b32 s4, v254, 53
	s_cselect_b64 s[10:11], -1, 0
	s_ashr_i32 s39, s25, 31
	v_mov_b32_e32 v137, v183
	v_lshl_add_u32 v138, v13, 1, v2
	v_mov_b32_e32 v139, v183
	s_mov_b32 s40, 0
	v_add_u32_e32 v145, 0, v5
	v_readlane_b32 s41, v254, 27
	s_mov_b32 s42, s4
	s_barrier
	v_readlane_b32 s5, v254, 54
	s_branch .LBB0_1071

; #define GAS __attribute__((address_space(1)))
; __device__ __forceinline__ void phase_post_mix(Frame& F, int l) {
;     ...
;     const int gw = F.vcu * NWAVES + F.wave, NGW = F.G * NWAVES, lane = F.lane;
;     const GAS float* xin = INP(F, I_X); const GAS bf16* xr = (const GAS bf16*)(F.ws + WS_XR); const GAS bf16* Y = (const GAS bf16*)(F.ws + WS_Y);
;     for (int m0 = gw; m0 < M; m0 += 4 * NGW) {
;         int mm[4]; f32x4 xx[4][4];
; #pragma unroll
;         for (int q = 0; q < 4; ++q) mm[q] = (m0 + q * NGW < M) ? m0 + q * NGW : m0;
; #pragma unroll
;         for (int q = 0; q < 4; q += 2) { f32x4 ya[4], yb[4];
;             roww_load_bf16(Y + (size_t)mm[q] * DM, lane, ya); roww_load_bf16(Y + (size_t)mm[q + 1] * DM, lane, yb);
;             if (l == 0) { roww_load(xin + (size_t)mm[q] * DM, lane, xx[q]); roww_load(xin + (size_t)mm[q + 1] * DM, lane, xx[q + 1]); }
;             else { roww_load_bf16(xr + (size_t)mm[q] * DM, lane, xx[q]); roww_load_bf16(xr + (size_t)mm[q + 1] * DM, lane, xx[q + 1]); }
;             post_mix_front(F, l, mm[q], ya, xx[q], PV); post_mix_front(F, l, mm[q + 1], yb, xx[q + 1], PV); }
.LBB0_1216:
	s_or_b64 exec, exec, s[2:3]
	s_ashr_i32 s89, s9, 6
	s_lshl_b32 s2, s8, 3
	s_add_i32 s14, s89, s2
	v_and_b32_e32 v186, 63, v8
	s_cmpk_gt_i32 s14, 0x3fff
	s_waitcnt lgkmcnt(0)
	s_barrier
	s_cbranch_scc1 .LBB0_1236
	s_movk_i32 s2, 0x110
	v_lshlrev_b32_e32 v10, 4, v186
	v_mov_b32_e32 v11, v183
	v_mad_u32_u24 v1, v186, s2, 0
	v_lshl_add_u64 v[6:7], s[80:81], 0, v[10:11]
	s_mov_b64 s[2:3], 0xac00000
	v_lshlrev_b32_e32 v182, 5, v186
	v_lshl_add_u64 v[6:7], v[6:7], 0, s[2:3]
	s_add_i32 s2, 0, 0x11000
	s_ashr_i32 s15, s14, 31
	s_lshl_b32 s38, s22, 3
	v_lshl_add_u64 v[4:5], s[80:81], 0, v[182:183]
	s_mov_b64 s[4:5], 0x4400000
	s_lshl_b32 s16, s22, 5
	v_and_b32_e32 v9, 8, v8
	v_and_b32_e32 v11, 4, v8
	v_and_b32_e32 v8, 3, v8
	v_add_u32_e32 v96, s2, v10
	s_lshl_b64 s[2:3], s[14:15], 10
	v_lshl_add_u64 v[2:3], v[4:5], 0, s[4:5]
	s_mov_b64 s[4:5], 0x27400000
	v_cmp_eq_u32_e64 s[8:9], 0, v8
	v_lshlrev_b32_e32 v8, 12, v186
	s_add_u32 s2, s2, 0xac00000
	v_lshl_add_u64 v[4:5], v[4:5], 0, s[4:5]
	v_cmp_eq_u32_e64 s[4:5], 0, v9
	v_and_b32_e32 v8, 0x3c000, v8
	v_mov_b32_e32 v9, v183
	s_addc_u32 s3, s3, 0
	v_cmp_eq_u32_e64 s[6:7], 0, v11
	v_lshl_add_u64 v[8:9], s[80:81], 0, v[8:9]
	v_or_b32_e32 v10, s2, v10
	v_mov_b32_e32 v11, s3
	s_ashr_i32 s17, s16, 31
	s_lshl_b64 s[2:3], s[14:15], 11
	v_lshl_add_u64 v[8:9], v[8:9], 0, s[96:97]
	s_lshl_b64 s[18:19], s[16:17], 10
	v_or_b32_e32 v12, s2, v182
	v_mov_b32_e32 v13, s3
	s_lshl_b64 s[20:21], s[16:17], 11
	s_lshl_b32 s15, s22, 4
	s_mul_i32 s17, s22, 24
	s_branch .LBB0_1220

; #define GAS __attribute__((address_space(1)))
; #define LAS __attribute__((address_space(3)))
; __device__ __forceinline__ float rsq(float x) { return __builtin_amdgcn_rsqf(x); }
; __device__ __forceinline__ void post_mix_front(Frame& F, int l, int m, const f32x4 (&y)[4], f32x4 (&x)[4], const LAS float* PV) {
;     const int lane = F.lane, b = m >> 12; const LAS f32x4* A = (const LAS f32x4*)(PV + b * 3072); const LAS f32x4* Bv = A + 256; const LAS f32x4* Cv = A + 512;
;     const float rstd = rsq(row_ss(y, lane) * (1.0f / DM) + EPS);
; #pragma unroll
;     for (int j = 0; j < 4; ++j) { const int c4 = lane + 64 * j; x[j] = x[j] + A[c4] * (y[j] * rstd); }
;     roww_store_bf16((GAS bf16*)(F.ws + WS_XR) + (size_t)m * DM, lane, x);
;     const float rstd2 = rsq(row_ss(x, lane) * (1.0f / DM) + EPS);
; __device__ __forceinline__ void phase_post_mix(Frame& F, int l) {
;     ...
;         for (int q = 0; q < 4; q += 2) { f32x4 ya[4], yb[4];
;             roww_load_bf16(Y + (size_t)mm[q] * DM, lane, ya); roww_load_bf16(Y + (size_t)mm[q + 1] * DM, lane, yb);
;             if (l == 0) { roww_load(xin + (size_t)mm[q] * DM, lane, xx[q]); roww_load(xin + (size_t)mm[q + 1] * DM, lane, xx[q + 1]); }
;             else { roww_load_bf16(xr + (size_t)mm[q] * DM, lane, xx[q]); roww_load_bf16(xr + (size_t)mm[q + 1] * DM, lane, xx[q + 1]); }
;             post_mix_front(F, l, mm[q], ya, xx[q], PV); post_mix_front(F, l, mm[q + 1], yb, xx[q + 1], PV); }
.LBB0_1220:
	v_lshl_add_u64 v[28:29], s[80:81], 0, v[12:13]
	s_mov_b32 s2, 0x27400000
	v_add_co_u32_e32 v14, vcc, s2, v28
	s_mov_b64 s[2:3], 0x27400000
	v_lshl_add_u64 v[20:21], v[28:29], 0, s[2:3]
	s_add_i32 s2, s38, s14
	s_cmpk_lt_i32 s2, 0x4000
	s_cselect_b32 s26, s2, s14
	s_add_i32 s2, s15, s14
	s_cmpk_lt_i32 s2, 0x4000
	v_addc_co_u32_e32 v15, vcc, 0, v29, vcc
	s_cselect_b32 s24, s2, s14
	s_add_i32 s2, s17, s14
	v_add_co_u32_e32 v24, vcc, 0x4400000, v28
	s_mov_b64 s[22:23], 0x4400000
	s_cmpk_lt_i32 s2, 0x4000
	v_addc_co_u32_e32 v25, vcc, 0, v29, vcc
	v_lshl_add_u64 v[28:29], v[28:29], 0, s[22:23]
	s_cselect_b32 s22, s2, s14
	s_ashr_i32 s27, s26, 31
	s_lshl_b64 s[2:3], s[26:27], 11
	global_load_dwordx4 v[24:27], v[24:25], off
	v_lshl_add_u64 v[30:31], v[4:5], 0, s[2:3]
	global_load_dwordx4 v[32:35], v[28:29], off offset:16
	v_lshl_add_u64 v[28:29], v[2:3], 0, s[2:3]
	global_load_dwordx4 v[16:19], v[14:15], off
	s_ashr_i32 s28, s14, 12
	global_load_dwordx4 v[20:23], v[20:21], off offset:16
	s_nop 0
	global_load_dwordx4 v[36:39], v[28:29], off
	global_load_dwordx4 v[40:43], v[28:29], off offset:16
	global_load_dwordx4 v[52:55], v[30:31], off
	global_load_dwordx4 v[64:67], v[30:31], off offset:16
	s_mul_i32 s2, s28, 0x3000
	v_add_u32_e32 v92, s2, v96
	ds_read_b128 v[68:71], v92
	s_ashr_i32 s30, s26, 12
	s_mul_i32 s2, s30, 0x3000
	s_ashr_i32 s25, s24, 31
	s_ashr_i32 s23, s22, 31
	s_lshl_b64 s[34:35], s[22:23], 11
	s_ashr_i32 s36, s22, 12
	s_waitcnt vmcnt(0)
	v_lshlrev_b32_e32 v80, 16, v24
	v_and_b32_e32 v81, 0xffff0000, v24
	v_lshlrev_b32_e32 v24, 16, v25
	v_and_b32_e32 v25, 0xffff0000, v25
	v_lshlrev_b32_e32 v88, 16, v33
	v_and_b32_e32 v89, 0xffff0000, v33
	v_lshlrev_b32_e32 v50, 16, v38
	v_and_b32_e32 v51, 0xffff0000, v38
	v_lshlrev_b32_e32 v46, 16, v39
	v_and_b32_e32 v47, 0xffff0000, v39
	v_lshlrev_b32_e32 v38, 16, v40
	v_and_b32_e32 v39, 0xffff0000, v40
	v_mul_f32_e32 v33, v81, v81
	v_mul_f32_e32 v40, v25, v25
	v_and_b32_e32 v83, 0xffff0000, v26
	v_and_b32_e32 v85, 0xffff0000, v27
	v_fmac_f32_e32 v33, v80, v80
	v_fmac_f32_e32 v40, v24, v24
	v_lshlrev_b32_e32 v82, 16, v26
	v_lshlrev_b32_e32 v84, 16, v27
	v_lshlrev_b32_e32 v58, 16, v36
	v_and_b32_e32 v59, 0xffff0000, v36
	v_lshlrev_b32_e32 v56, 16, v37
	v_and_b32_e32 v57, 0xffff0000, v37
	v_lshlrev_b32_e32 v36, 16, v41
	v_and_b32_e32 v37, 0xffff0000, v41
	v_add_f32_e32 v33, v33, v40
	v_mul_f32_e32 v40, v83, v83
	v_mul_f32_e32 v41, v85, v85
	v_fmac_f32_e32 v40, v82, v82
	v_fmac_f32_e32 v41, v84, v84
	v_and_b32_e32 v87, 0xffff0000, v32
	v_add_f32_e32 v40, v40, v41
	v_lshlrev_b32_e32 v86, 16, v32
	v_add_f32_e32 v33, v33, v40
	v_mul_f32_e32 v40, v87, v87
	v_mul_f32_e32 v41, v89, v89
	v_fmac_f32_e32 v40, v86, v86
	v_fmac_f32_e32 v41, v88, v88
	v_lshlrev_b32_e32 v90, 16, v34
	v_and_b32_e32 v91, 0xffff0000, v34
	v_lshlrev_b32_e32 v34, 16, v35
	v_and_b32_e32 v35, 0xffff0000, v35
	v_add_f32_e32 v40, v40, v41
	v_add_f32_e32 v33, v33, v40
	v_mul_f32_e32 v40, v91, v91
	v_mul_f32_e32 v41, v35, v35
	v_fmac_f32_e32 v40, v90, v90
	v_fmac_f32_e32 v41, v34, v34
	v_add_f32_e32 v40, v40, v41
	v_add_f32_e32 v33, v40, v33
	v_lshlrev_b32_e32 v48, 16, v18
	v_and_b32_e32 v49, 0xffff0000, v18
	v_add_f32_dpp v33, v33, v33 quad_perm:[1,0,3,2] row_mask:0xf bank_mask:0xf bound_ctrl:1
	v_lshlrev_b32_e32 v72, 16, v19
	v_and_b32_e32 v73, 0xffff0000, v19
	v_add_f32_dpp v33, v33, v33 quad_perm:[2,3,0,1] row_mask:0xf bank_mask:0xf bound_ctrl:1
	v_lshlrev_b32_e32 v76, 16, v22
	v_and_b32_e32 v77, 0xffff0000, v22
	v_add_f32_dpp v33, v33, v33 row_half_mirror row_mask:0xf bank_mask:0xf bound_ctrl:1
	v_lshlrev_b32_e32 v78, 16, v23
	v_and_b32_e32 v79, 0xffff0000, v23
	v_add_f32_dpp v33, v33, v33 row_mirror row_mask:0xf bank_mask:0xf bound_ctrl:1
	v_mov_b32_e32 v40, v33
	s_nop 1
	v_permlane16_swap_b32_e32 v33, v40
	v_add_f32_e32 v33, v33, v40
	v_mov_b32_e32 v40, v33
	s_nop 1
	v_permlane32_swap_b32_e32 v33, v40
	v_add_f32_e32 v33, v33, v40
	v_fmamk_f32 v33, v33, 0x3a800000, v225
	v_rsq_f32_e32 v40, v33
	v_lshlrev_b32_e32 v22, 16, v42
	v_and_b32_e32 v23, 0xffff0000, v42
	v_lshlrev_b32_e32 v18, 16, v43
	v_and_b32_e32 v19, 0xffff0000, v43
	v_lshlrev_b32_e32 v42, 16, v64
	v_and_b32_e32 v43, 0xffff0000, v64
	v_lshlrev_b32_e32 v44, 16, v65
	v_and_b32_e32 v45, 0xffff0000, v65
	v_lshlrev_b32_e32 v26, 16, v66
	v_and_b32_e32 v27, 0xffff0000, v66
	v_lshlrev_b32_e32 v32, 16, v67
	v_and_b32_e32 v33, 0xffff0000, v67
	ds_read_b128 v[64:67], v92 offset:1024
	v_lshlrev_b32_e32 v28, 16, v16
	v_and_b32_e32 v29, 0xffff0000, v16
	v_pk_mul_f32 v[80:81], v[40:41], v[80:81] op_sel_hi:[0,1]
	s_waitcnt lgkmcnt(1)
	v_pk_fma_f32 v[28:29], v[68:69], v[80:81], v[28:29]
	v_pk_mul_f32 v[68:69], v[40:41], v[84:85] op_sel_hi:[0,1]
	v_lshlrev_b32_e32 v16, 16, v17
	v_and_b32_e32 v17, 0xffff0000, v17
	v_pk_mul_f32 v[24:25], v[40:41], v[24:25] op_sel_hi:[0,1]
	s_waitcnt lgkmcnt(0)
	v_pk_fma_f32 v[80:81], v[66:67], v[68:69], v[72:73]
	ds_read_b128 v[66:69], v92 offset:2048
	v_pk_fma_f32 v[24:25], v[70:71], v[24:25], v[16:17]
	ds_read_b128 v[70:73], v92 offset:3072
	v_pk_mul_f32 v[16:17], v[40:41], v[82:83] op_sel_hi:[0,1]
	v_lshlrev_b32_e32 v74, 16, v20
	v_and_b32_e32 v75, 0xffff0000, v20
	v_pk_fma_f32 v[82:83], v[64:65], v[16:17], v[48:49]
	v_pk_mul_f32 v[16:17], v[40:41], v[86:87] op_sel_hi:[0,1]
	s_waitcnt lgkmcnt(1)
	v_pk_fma_f32 v[84:85], v[66:67], v[16:17], v[74:75]
	v_pk_mul_f32 v[16:17], v[40:41], v[90:91] op_sel_hi:[0,1]
	s_waitcnt lgkmcnt(0)
; #define GAS __attribute__((address_space(1)))
; #define LAS __attribute__((address_space(3)))
; __device__ __forceinline__ float rsq(float x) { return __builtin_amdgcn_rsqf(x); }
; __device__ __forceinline__ void post_mix_front(Frame& F, int l, int m, const f32x4 (&y)[4], f32x4 (&x)[4], const LAS float* PV) {
;     const int lane = F.lane, b = m >> 12; const LAS f32x4* A = (const LAS f32x4*)(PV + b * 3072); const LAS f32x4* Bv = A + 256; const LAS f32x4* Cv = A + 512;
;     const float rstd = rsq(row_ss(y, lane) * (1.0f / DM) + EPS);
; #pragma unroll
;     for (int j = 0; j < 4; ++j) { const int c4 = lane + 64 * j; x[j] = x[j] + A[c4] * (y[j] * rstd); }
;     roww_store_bf16((GAS bf16*)(F.ws + WS_XR) + (size_t)m * DM, lane, x);
;     const float rstd2 = rsq(row_ss(x, lane) * (1.0f / DM) + EPS);
;     v4u hw;
; #pragma unroll
;     for (int j = 0; j < 4; ++j) { const int c4 = lane + 64 * j; x[j] = x[j] * rstd2 * Bv[c4] + Cv[c4]; hw[j] = pk4_f8(x[j][0], x[j][1], x[j][2], x[j][3]); }
;     ((GAS v4u*)((GAS unsigned char*)(F.ws + WS_HN) + (size_t)m * DM))[lane] = hw;
; }
	v_pk_fma_f32 v[86:87], v[70:71], v[16:17], v[76:77]
	v_mul_f32_e32 v16, v29, v29
	v_mul_f32_e32 v17, v25, v25
	v_pk_mul_f32 v[34:35], v[40:41], v[34:35] op_sel_hi:[0,1]
	v_fmac_f32_e32 v16, v28, v28
	v_fmac_f32_e32 v17, v24, v24
	v_pk_fma_f32 v[78:79], v[72:73], v[34:35], v[78:79]
	v_add_f32_e32 v16, v16, v17
	v_mul_f32_e32 v17, v83, v83
	v_mul_f32_e32 v34, v81, v81
	v_lshlrev_b32_e32 v20, 16, v21
	v_and_b32_e32 v21, 0xffff0000, v21
	v_pk_mul_f32 v[48:49], v[40:41], v[88:89] op_sel_hi:[0,1]
	v_fmac_f32_e32 v17, v82, v82
	v_fmac_f32_e32 v34, v80, v80
	v_pk_fma_f32 v[20:21], v[68:69], v[48:49], v[20:21]
	v_add_f32_e32 v17, v17, v34
	v_add_f32_e32 v16, v16, v17
	v_mul_f32_e32 v17, v85, v85
	v_mul_f32_e32 v34, v21, v21
	v_fmac_f32_e32 v17, v84, v84
	v_fmac_f32_e32 v34, v20, v20
	v_add_f32_e32 v17, v17, v34
	v_add_f32_e32 v16, v17, v16
	v_mul_f32_e32 v17, v87, v87
	v_mul_f32_e32 v34, v79, v79
	v_fmac_f32_e32 v17, v86, v86
	v_fmac_f32_e32 v34, v78, v78
	v_add_f32_e32 v17, v17, v34
	v_add_f32_e32 v16, v17, v16
	v_cvt_pk_bf16_f32 v64, v28, v29
	v_cvt_pk_bf16_f32 v65, v24, v25
	v_add_f32_dpp v16, v16, v16 quad_perm:[1,0,3,2] row_mask:0xf bank_mask:0xf bound_ctrl:1
	v_cvt_pk_bf16_f32 v66, v82, v83
	v_cvt_pk_bf16_f32 v67, v80, v81
	v_add_f32_dpp v16, v16, v16 quad_perm:[2,3,0,1] row_mask:0xf bank_mask:0xf bound_ctrl:1
	v_cvt_pk_bf16_f32 v68, v84, v85
	v_cvt_pk_bf16_f32 v69, v20, v21
	v_add_f32_dpp v16, v16, v16 row_half_mirror row_mask:0xf bank_mask:0xf bound_ctrl:1
	v_cvt_pk_bf16_f32 v70, v86, v87
	v_cvt_pk_bf16_f32 v71, v78, v79
	v_add_f32_dpp v16, v16, v16 row_mirror row_mask:0xf bank_mask:0xf bound_ctrl:1
	v_mov_b32_e32 v17, v16
	s_nop 1
	v_permlane16_swap_b32_e32 v16, v17
	v_add_f32_e32 v16, v16, v17
	v_mov_b32_e32 v17, v16
	s_nop 1
	v_permlane32_swap_b32_e32 v16, v17
	v_add_f32_e32 v16, v16, v17
	global_store_dwordx4 v[14:15], v[64:67], off
	v_fmamk_f32 v16, v16, 0x3a800000, v225
	global_store_dwordx4 v[14:15], v[68:71], off offset:16
	v_rsq_f32_e32 v88, v16
	ds_read_b128 v[14:17], v92 offset:4096
	ds_read_b128 v[64:67], v92 offset:8192
	ds_read_b128 v[68:71], v92 offset:5120
	ds_read_b128 v[72:75], v92 offset:9216
	v_lshlrev_b32_e32 v60, 16, v52
	v_pk_mul_f32 v[28:29], v[28:29], v[88:89] op_sel_hi:[1,0]
	v_pk_mul_f32 v[24:25], v[24:25], v[88:89] op_sel_hi:[1,0]
	s_waitcnt lgkmcnt(2)
	v_pk_fma_f32 v[48:49], v[14:15], v[28:29], v[64:65]
	v_mov_b32_e32 v64, v183
	v_med3_f32 v14, v48, s33, v226
	v_med3_f32 v15, v49, s33, v226
	v_cvt_pk_fp8_f32 v64, v14, v15
	v_pk_fma_f32 v[40:41], v[16:17], v[24:25], v[66:67]
	v_mov_b32_e32 v65, v183
	v_med3_f32 v14, v40, s33, v226
	v_med3_f32 v15, v41, s33, v226
	v_cvt_pk_fp8_f32 v64, v14, v15 op_sel:[0,0,1]
	v_pk_mul_f32 v[14:15], v[82:83], v[88:89] op_sel_hi:[1,0]
	v_pk_mul_f32 v[16:17], v[80:81], v[88:89] op_sel_hi:[1,0]
	s_waitcnt lgkmcnt(0)
	v_pk_fma_f32 v[34:35], v[68:69], v[14:15], v[72:73]
	v_pk_fma_f32 v[28:29], v[70:71], v[16:17], v[74:75]
	v_med3_f32 v14, v34, s33, v226
	v_med3_f32 v15, v35, s33, v226
	v_cvt_pk_fp8_f32 v65, v14, v15
	v_med3_f32 v14, v28, s33, v226
	v_med3_f32 v15, v29, s33, v226
	v_pk_mul_f32 v[24:25], v[84:85], v[88:89] op_sel_hi:[1,0]
	v_cvt_pk_fp8_f32 v65, v14, v15 op_sel:[0,0,1]
	ds_read_b128 v[14:17], v92 offset:6144
	ds_read_b128 v[66:69], v92 offset:10240
	ds_read_b128 v[70:73], v92 offset:7168
	ds_read_b128 v[74:77], v92 offset:11264
	v_pk_mul_f32 v[20:21], v[20:21], v[88:89] op_sel_hi:[1,0]
	v_and_b32_e32 v61, 0xffff0000, v52
	v_lshlrev_b32_e32 v62, 16, v53
	s_waitcnt lgkmcnt(2)
	v_pk_fma_f32 v[24:25], v[24:25], v[14:15], v[66:67]
	v_mov_b32_e32 v66, v183
	v_med3_f32 v14, v24, s33, v226
	v_med3_f32 v15, v25, s33, v226
	v_cvt_pk_fp8_f32 v66, v14, v15
	v_pk_fma_f32 v[20:21], v[20:21], v[16:17], v[68:69]
	v_mov_b32_e32 v67, v183
	v_med3_f32 v14, v20, s33, v226
	v_med3_f32 v15, v21, s33, v226
	v_cvt_pk_fp8_f32 v66, v14, v15 op_sel:[0,0,1]
	v_pk_mul_f32 v[14:15], v[86:87], v[88:89] op_sel_hi:[1,0]
	v_pk_mul_f32 v[68:69], v[78:79], v[88:89] op_sel_hi:[1,0]
	s_waitcnt lgkmcnt(0)
	v_pk_fma_f32 v[16:17], v[14:15], v[70:71], v[74:75]
	v_mul_f32_e32 v70, v47, v47
	v_med3_f32 v14, v16, s33, v226
	v_med3_f32 v15, v17, s33, v226
	v_cvt_pk_fp8_f32 v67, v14, v15
	v_pk_fma_f32 v[14:15], v[68:69], v[72:73], v[76:77]
	v_fmac_f32_e32 v70, v46, v46
	v_med3_f32 v68, v14, s33, v226
	v_med3_f32 v69, v15, s33, v226
	v_cvt_pk_fp8_f32 v67, v68, v69 op_sel:[0,0,1]
	v_mul_f32_e32 v68, v59, v59
	v_mul_f32_e32 v69, v57, v57
	v_fmac_f32_e32 v68, v58, v58
	v_fmac_f32_e32 v69, v56, v56
	v_add_f32_e32 v68, v68, v69
	v_mul_f32_e32 v69, v51, v51
	v_fmac_f32_e32 v69, v50, v50
	v_add_f32_e32 v69, v69, v70
	v_add_f32_e32 v68, v68, v69
	v_mul_f32_e32 v69, v39, v39
	v_mul_f32_e32 v70, v37, v37
	v_fmac_f32_e32 v69, v38, v38
	v_fmac_f32_e32 v70, v36, v36
	v_add_f32_e32 v69, v69, v70
	v_add_f32_e32 v68, v68, v69
	v_mul_f32_e32 v69, v23, v23
	v_mul_f32_e32 v70, v19, v19
	v_fmac_f32_e32 v69, v22, v22
	v_fmac_f32_e32 v70, v18, v18
	v_add_f32_e32 v69, v69, v70
	v_add_f32_e32 v68, v69, v68
	v_lshl_add_u64 v[72:73], s[80:81], 0, v[10:11]
	v_add_u32_e32 v75, s2, v96
	v_add_f32_dpp v68, v68, v68 quad_perm:[1,0,3,2] row_mask:0xf bank_mask:0xf bound_ctrl:1
	global_store_dwordx4 v[72:73], v[64:67], off
	v_and_b32_e32 v63, 0xffff0000, v53
	v_add_f32_dpp v68, v68, v68 quad_perm:[2,3,0,1] row_mask:0xf bank_mask:0xf bound_ctrl:1
	v_lshlrev_b32_e32 v52, 16, v54
	v_and_b32_e32 v53, 0xffff0000, v54
	v_add_f32_dpp v68, v68, v68 row_half_mirror row_mask:0xf bank_mask:0xf bound_ctrl:1
	v_lshlrev_b32_e32 v54, 16, v55
	v_and_b32_e32 v55, 0xffff0000, v55
	v_add_f32_dpp v68, v68, v68 row_mirror row_mask:0xf bank_mask:0xf bound_ctrl:1
	v_mov_b32_e32 v69, v68
	s_nop 1
	v_permlane16_swap_b32_e32 v68, v69
	v_add_f32_e32 v68, v68, v69
	v_mov_b32_e32 v69, v68
	s_nop 1
	v_permlane32_swap_b32_e32 v68, v69
	v_add_f32_e32 v68, v68, v69
	v_fmamk_f32 v68, v68, 0x3a800000, v225
	v_rsq_f32_e32 v74, v68
	ds_read_b128 v[68:71], v75
	s_lshl_b64 s[2:3], s[26:27], 10
	v_pk_mul_f32 v[64:65], v[74:75], v[58:59] op_sel_hi:[0,1]
	v_pk_mul_f32 v[66:67], v[74:75], v[56:57] op_sel_hi:[0,1]
	ds_read_b128 v[56:59], v75 offset:1024
	v_pk_mul_f32 v[50:51], v[74:75], v[50:51] op_sel_hi:[0,1]
	v_pk_mul_f32 v[46:47], v[74:75], v[46:47] op_sel_hi:[0,1]
	s_waitcnt lgkmcnt(1)
; #define GAS __attribute__((address_space(1)))
; #define LAS __attribute__((address_space(3)))
; __device__ __forceinline__ float rsq(float x) { return __builtin_amdgcn_rsqf(x); }
; __device__ __forceinline__ void post_mix_front(Frame& F, int l, int m, const f32x4 (&y)[4], f32x4 (&x)[4], const LAS float* PV) {
;     const int lane = F.lane, b = m >> 12; const LAS f32x4* A = (const LAS f32x4*)(PV + b * 3072); const LAS f32x4* Bv = A + 256; const LAS f32x4* Cv = A + 512;
;     const float rstd = rsq(row_ss(y, lane) * (1.0f / DM) + EPS);
; #pragma unroll
;     for (int j = 0; j < 4; ++j) { const int c4 = lane + 64 * j; x[j] = x[j] + A[c4] * (y[j] * rstd); }
;     roww_store_bf16((GAS bf16*)(F.ws + WS_XR) + (size_t)m * DM, lane, x);
;     const float rstd2 = rsq(row_ss(x, lane) * (1.0f / DM) + EPS);
;     v4u hw;
; #pragma unroll
;     for (int j = 0; j < 4; ++j) { const int c4 = lane + 64 * j; x[j] = x[j] * rstd2 * Bv[c4] + Cv[c4]; hw[j] = pk4_f8(x[j][0], x[j][1], x[j][2], x[j][3]); }
;     ((GAS v4u*)((GAS unsigned char*)(F.ws + WS_HN) + (size_t)m * DM))[lane] = hw;
; }
	v_pk_fma_f32 v[64:65], v[68:69], v[64:65], v[60:61]
	v_pk_fma_f32 v[62:63], v[70:71], v[66:67], v[62:63]
	s_waitcnt lgkmcnt(0)
	v_pk_fma_f32 v[46:47], v[58:59], v[46:47], v[54:55]
	ds_read_b128 v[58:61], v75 offset:2048
	v_pk_fma_f32 v[72:73], v[56:57], v[50:51], v[52:53]
	v_pk_mul_f32 v[50:51], v[74:75], v[38:39] op_sel_hi:[0,1]
	v_pk_mul_f32 v[52:53], v[74:75], v[36:37] op_sel_hi:[0,1]
	ds_read_b128 v[36:39], v75 offset:3072
	v_pk_mul_f32 v[22:23], v[74:75], v[22:23] op_sel_hi:[0,1]
	v_pk_mul_f32 v[18:19], v[74:75], v[18:19] op_sel_hi:[0,1]
	s_waitcnt lgkmcnt(1)
	v_pk_fma_f32 v[76:77], v[60:61], v[52:53], v[44:45]
	v_pk_fma_f32 v[78:79], v[58:59], v[50:51], v[42:43]
	s_waitcnt lgkmcnt(0)
	v_pk_fma_f32 v[22:23], v[36:37], v[22:23], v[26:27]
	v_mul_f32_e32 v26, v65, v65
	v_mul_f32_e32 v27, v63, v63
	v_fmac_f32_e32 v26, v64, v64
	v_fmac_f32_e32 v27, v62, v62
	v_pk_fma_f32 v[18:19], v[38:39], v[18:19], v[32:33]
	v_add_f32_e32 v26, v26, v27
	v_mul_f32_e32 v27, v73, v73
	v_mul_f32_e32 v32, v47, v47
	v_fmac_f32_e32 v27, v72, v72
	v_fmac_f32_e32 v32, v46, v46
	v_add_f32_e32 v27, v27, v32
	v_add_f32_e32 v26, v26, v27
	v_mul_f32_e32 v27, v79, v79
	v_mul_f32_e32 v32, v77, v77
	v_fmac_f32_e32 v27, v78, v78
	v_fmac_f32_e32 v32, v76, v76
	v_add_f32_e32 v27, v27, v32
	v_add_f32_e32 v26, v27, v26
	v_mul_f32_e32 v27, v23, v23
	v_mul_f32_e32 v32, v19, v19
	v_fmac_f32_e32 v27, v22, v22
	v_fmac_f32_e32 v32, v18, v18
	v_add_f32_e32 v27, v27, v32
	v_add_f32_e32 v26, v27, v26
	ds_read_b128 v[36:39], v75 offset:4096
	ds_read_b128 v[54:57], v75 offset:8192
	v_add_f32_dpp v26, v26, v26 quad_perm:[1,0,3,2] row_mask:0xf bank_mask:0xf bound_ctrl:1
	v_mov_b32_e32 v70, v183
	v_cvt_pk_bf16_f32 v42, v64, v65
	v_add_f32_dpp v26, v26, v26 quad_perm:[2,3,0,1] row_mask:0xf bank_mask:0xf bound_ctrl:1
	v_cvt_pk_bf16_f32 v43, v62, v63
	v_cvt_pk_bf16_f32 v45, v46, v47
	v_add_f32_dpp v26, v26, v26 row_half_mirror row_mask:0xf bank_mask:0xf bound_ctrl:1
	v_mov_b32_e32 v71, v183
	v_cvt_pk_bf16_f32 v51, v76, v77
	v_add_f32_dpp v26, v26, v26 row_mirror row_mask:0xf bank_mask:0xf bound_ctrl:1
	v_mov_b32_e32 v27, v26
	s_nop 1
	v_permlane16_swap_b32_e32 v26, v27
	v_add_f32_e32 v26, v26, v27
	v_mov_b32_e32 v27, v26
	s_nop 1
	v_permlane32_swap_b32_e32 v26, v27
	v_add_f32_e32 v26, v26, v27
	v_fmamk_f32 v26, v26, 0x3a800000, v225
	v_rsq_f32_e32 v80, v26
	v_cvt_pk_bf16_f32 v44, v72, v73
	v_cvt_pk_bf16_f32 v52, v22, v23
	v_cvt_pk_bf16_f32 v53, v18, v19
	v_pk_mul_f32 v[26:27], v[64:65], v[80:81] op_sel_hi:[1,0]
	v_pk_mul_f32 v[32:33], v[62:63], v[80:81] op_sel_hi:[1,0]
	s_waitcnt lgkmcnt(0)
	v_pk_fma_f32 v[60:61], v[36:37], v[26:27], v[54:55]
	ds_read_b128 v[62:65], v75 offset:5120
	ds_read_b128 v[66:69], v75 offset:9216
	v_med3_f32 v26, v60, s33, v226
	v_med3_f32 v27, v61, s33, v226
	v_cvt_pk_fp8_f32 v70, v26, v27
	v_pk_fma_f32 v[54:55], v[38:39], v[32:33], v[56:57]
	v_pk_mul_f32 v[32:33], v[46:47], v[80:81] op_sel_hi:[1,0]
	v_med3_f32 v26, v54, s33, v226
	v_med3_f32 v27, v55, s33, v226
	v_cvt_pk_fp8_f32 v70, v26, v27 op_sel:[0,0,1]
	v_pk_mul_f32 v[26:27], v[72:73], v[80:81] op_sel_hi:[1,0]
	s_waitcnt lgkmcnt(0)
	v_pk_fma_f32 v[38:39], v[64:65], v[32:33], v[68:69]
	v_pk_fma_f32 v[46:47], v[62:63], v[26:27], v[66:67]
	ds_read_b128 v[56:59], v75 offset:6144
	ds_read_b128 v[62:65], v75 offset:10240
	v_med3_f32 v26, v46, s33, v226
	v_med3_f32 v27, v47, s33, v226
	v_cvt_pk_fp8_f32 v71, v26, v27
	v_med3_f32 v26, v38, s33, v226
	v_med3_f32 v27, v39, s33, v226
	v_pk_mul_f32 v[36:37], v[76:77], v[80:81] op_sel_hi:[1,0]
	v_cvt_pk_fp8_f32 v71, v26, v27 op_sel:[0,0,1]
	v_pk_mul_f32 v[26:27], v[78:79], v[80:81] op_sel_hi:[1,0]
	ds_read_b128 v[66:69], v75 offset:7168
	ds_read_b128 v[74:77], v75 offset:11264
	s_waitcnt lgkmcnt(2)
	v_pk_fma_f32 v[32:33], v[26:27], v[56:57], v[62:63]
	v_mov_b32_e32 v72, v183
	v_med3_f32 v26, v32, s33, v226
	v_med3_f32 v27, v33, s33, v226
	v_cvt_pk_fp8_f32 v72, v26, v27
	v_pk_fma_f32 v[26:27], v[36:37], v[58:59], v[64:65]
	v_pk_mul_f32 v[22:23], v[22:23], v[80:81] op_sel_hi:[1,0]
	v_med3_f32 v36, v26, s33, v226
	v_med3_f32 v37, v27, s33, v226
	s_waitcnt lgkmcnt(0)
	v_pk_fma_f32 v[22:23], v[22:23], v[66:67], v[74:75]
	v_cvt_pk_fp8_f32 v72, v36, v37 op_sel:[0,0,1]
	v_med3_f32 v36, v22, s33, v226
	v_med3_f32 v37, v23, s33, v226
	v_mov_b32_e32 v73, v183
	v_cvt_pk_fp8_f32 v73, v36, v37
	v_pk_mul_f32 v[18:19], v[18:19], v[80:81] op_sel_hi:[1,0]
	v_cvt_pk_bf16_f32 v50, v78, v79
	v_pk_fma_f32 v[18:19], v[18:19], v[68:69], v[76:77]
	global_store_dwordx4 v[30:31], v[42:45], off
	global_store_dwordx4 v[30:31], v[50:53], off offset:16
	v_med3_f32 v36, v18, s33, v226
	v_med3_f32 v37, v19, s33, v226
	v_cvt_pk_fp8_f32 v73, v36, v37 op_sel:[0,0,1]
	v_lshl_add_u64 v[30:31], v[6:7], 0, s[2:3]
	s_lshl_b64 s[2:3], s[24:25], 11
	global_store_dwordx4 v[30:31], v[70:73], off
	v_lshl_add_u64 v[30:31], v[2:3], 0, s[2:3]
	global_load_dwordx4 v[42:45], v[30:31], off
	global_load_dwordx4 v[50:53], v[30:31], off offset:16
	v_lshl_add_u64 v[30:31], v[2:3], 0, s[34:35]
	global_load_dwordx4 v[56:59], v[30:31], off
	global_load_dwordx4 v[64:67], v[30:31], off offset:16
	v_lshl_add_u64 v[30:31], v[4:5], 0, s[2:3]
	global_load_dwordx4 v[78:81], v[30:31], off
	global_load_dwordx4 v[88:91], v[30:31], off offset:16
	v_lshl_add_u64 v[70:71], v[4:5], 0, s[34:35]
	global_load_dwordx4 v[98:101], v[70:71], off
	global_load_dwordx4 v[102:105], v[70:71], off offset:16
	s_ashr_i32 s34, s24, 12
	s_mul_i32 s2, s34, 0x3000
	s_waitcnt vmcnt(7)
	v_and_b32_e32 v37, 0xffff0000, v42
	v_and_b32_e32 v69, 0xffff0000, v43
	v_lshlrev_b32_e32 v36, 16, v42
	v_lshlrev_b32_e32 v68, 16, v43
	s_waitcnt vmcnt(5)
; #define GAS __attribute__((address_space(1)))
; #define LAS __attribute__((address_space(3)))
; __device__ __forceinline__ float rsq(float x) { return __builtin_amdgcn_rsqf(x); }
; __device__ __forceinline__ void post_mix_front(Frame& F, int l, int m, const f32x4 (&y)[4], f32x4 (&x)[4], const LAS float* PV) {
;     const int lane = F.lane, b = m >> 12; const LAS f32x4* A = (const LAS f32x4*)(PV + b * 3072); const LAS f32x4* Bv = A + 256; const LAS f32x4* Cv = A + 512;
;     const float rstd = rsq(row_ss(y, lane) * (1.0f / DM) + EPS);
; #pragma unroll
;     for (int j = 0; j < 4; ++j) { const int c4 = lane + 64 * j; x[j] = x[j] + A[c4] * (y[j] * rstd); }
;     roww_store_bf16((GAS bf16*)(F.ws + WS_XR) + (size_t)m * DM, lane, x);
;     const float rstd2 = rsq(row_ss(x, lane) * (1.0f / DM) + EPS);
;     v4u hw;
; #pragma unroll
;     for (int j = 0; j < 4; ++j) { const int c4 = lane + 64 * j; x[j] = x[j] * rstd2 * Bv[c4] + Cv[c4]; hw[j] = pk4_f8(x[j][0], x[j][1], x[j][2], x[j][3]); }
;     ((GAS v4u*)((GAS unsigned char*)(F.ws + WS_HN) + (size_t)m * DM))[lane] = hw;
; }
	v_lshlrev_b32_e32 v86, 16, v56
	v_and_b32_e32 v87, 0xffff0000, v56
	v_lshlrev_b32_e32 v84, 16, v57
	v_and_b32_e32 v85, 0xffff0000, v57
	s_waitcnt vmcnt(4)
	v_lshlrev_b32_e32 v62, 16, v64
	v_and_b32_e32 v63, 0xffff0000, v64
	v_lshlrev_b32_e32 v56, 16, v65
	v_and_b32_e32 v57, 0xffff0000, v65
	s_waitcnt vmcnt(3)
	v_lshlrev_b32_e32 v64, 16, v79
	v_and_b32_e32 v65, 0xffff0000, v79
	v_mul_f32_e32 v79, v37, v37
	v_mul_f32_e32 v97, v69, v69
	v_lshlrev_b32_e32 v74, 16, v44
	v_and_b32_e32 v75, 0xffff0000, v44
	v_lshlrev_b32_e32 v44, 16, v45
	v_and_b32_e32 v45, 0xffff0000, v45
	v_fmac_f32_e32 v79, v36, v36
	v_fmac_f32_e32 v97, v68, v68
	s_waitcnt vmcnt(1)
	v_lshlrev_b32_e32 v92, 16, v98
	v_and_b32_e32 v93, 0xffff0000, v98
	v_add_f32_e32 v79, v79, v97
	v_mul_f32_e32 v97, v75, v75
	v_mul_f32_e32 v98, v45, v45
	v_fmac_f32_e32 v97, v74, v74
	v_fmac_f32_e32 v98, v44, v44
	v_and_b32_e32 v107, 0xffff0000, v50
	v_and_b32_e32 v109, 0xffff0000, v51
	v_add_f32_e32 v97, v97, v98
	v_lshlrev_b32_e32 v106, 16, v50
	v_lshlrev_b32_e32 v108, 16, v51
	v_add_f32_e32 v79, v79, v97
	v_mul_f32_e32 v97, v107, v107
	v_mul_f32_e32 v98, v109, v109
	v_fmac_f32_e32 v97, v106, v106
	v_fmac_f32_e32 v98, v108, v108
	v_lshlrev_b32_e32 v110, 16, v52
	v_and_b32_e32 v111, 0xffff0000, v52
	v_lshlrev_b32_e32 v52, 16, v53
	v_and_b32_e32 v53, 0xffff0000, v53
	v_add_f32_e32 v97, v97, v98
	v_add_f32_e32 v79, v79, v97
	v_mul_f32_e32 v97, v111, v111
	v_mul_f32_e32 v98, v53, v53
	v_fmac_f32_e32 v97, v110, v110
	v_fmac_f32_e32 v98, v52, v52
	v_add_f32_e32 v97, v97, v98
	v_add_f32_e32 v79, v97, v79
	v_lshlrev_b32_e32 v116, 16, v88
	v_and_b32_e32 v117, 0xffff0000, v88
	v_add_f32_dpp v79, v79, v79 quad_perm:[1,0,3,2] row_mask:0xf bank_mask:0xf bound_ctrl:1
	v_lshlrev_b32_e32 v118, 16, v89
	v_and_b32_e32 v119, 0xffff0000, v89
	v_add_f32_dpp v79, v79, v79 quad_perm:[2,3,0,1] row_mask:0xf bank_mask:0xf bound_ctrl:1
	v_lshlrev_b32_e32 v120, 16, v90
	v_and_b32_e32 v121, 0xffff0000, v90
	v_add_f32_dpp v79, v79, v79 row_half_mirror row_mask:0xf bank_mask:0xf bound_ctrl:1
	v_lshlrev_b32_e32 v122, 16, v91
	v_and_b32_e32 v123, 0xffff0000, v91
	v_add_f32_dpp v79, v79, v79 row_mirror row_mask:0xf bank_mask:0xf bound_ctrl:1
	v_mov_b32_e32 v97, v79
	s_nop 1
	v_permlane16_swap_b32_e32 v79, v97
	v_add_f32_e32 v79, v79, v97
	v_mov_b32_e32 v97, v79
	s_nop 1
	v_permlane32_swap_b32_e32 v79, v97
	v_add_f32_e32 v79, v79, v97
	v_fmamk_f32 v79, v79, 0x3a800000, v225
	v_add_u32_e32 v97, s2, v96
	v_lshlrev_b32_e32 v94, 16, v99
	v_and_b32_e32 v95, 0xffff0000, v99
	v_lshlrev_b32_e32 v88, 16, v100
	v_and_b32_e32 v89, 0xffff0000, v100
	v_lshlrev_b32_e32 v90, 16, v101
	v_and_b32_e32 v91, 0xffff0000, v101
	v_rsq_f32_e32 v124, v79
	ds_read_b128 v[98:101], v97
	v_lshlrev_b32_e32 v76, 16, v58
	v_and_b32_e32 v77, 0xffff0000, v58
	v_lshlrev_b32_e32 v72, 16, v59
	v_and_b32_e32 v73, 0xffff0000, v59
	v_lshlrev_b32_e32 v50, 16, v66
	v_and_b32_e32 v51, 0xffff0000, v66
	v_lshlrev_b32_e32 v42, 16, v67
	v_and_b32_e32 v43, 0xffff0000, v67
	v_lshlrev_b32_e32 v58, 16, v78
	v_and_b32_e32 v59, 0xffff0000, v78
	v_lshlrev_b32_e32 v112, 16, v80
	v_and_b32_e32 v113, 0xffff0000, v80
	v_lshlrev_b32_e32 v114, 16, v81
	v_and_b32_e32 v115, 0xffff0000, v81
	s_waitcnt vmcnt(0)
	v_lshlrev_b32_e32 v80, 16, v102
	v_and_b32_e32 v81, 0xffff0000, v102
	v_lshlrev_b32_e32 v82, 16, v103
	v_and_b32_e32 v83, 0xffff0000, v103
	v_lshlrev_b32_e32 v66, 16, v104
	v_and_b32_e32 v67, 0xffff0000, v104
	v_lshlrev_b32_e32 v78, 16, v105
	v_and_b32_e32 v79, 0xffff0000, v105
	ds_read_b128 v[102:105], v97 offset:1024
	v_pk_mul_f32 v[36:37], v[124:125], v[36:37] op_sel_hi:[0,1]
	v_pk_mul_f32 v[68:69], v[124:125], v[68:69] op_sel_hi:[0,1]
	s_waitcnt lgkmcnt(1)
	v_pk_fma_f32 v[36:37], v[98:99], v[36:37], v[58:59]
	v_pk_mul_f32 v[58:59], v[124:125], v[74:75] op_sel_hi:[0,1]
	v_pk_mul_f32 v[44:45], v[124:125], v[44:45] op_sel_hi:[0,1]
	v_pk_fma_f32 v[64:65], v[100:101], v[68:69], v[64:65]
	s_waitcnt lgkmcnt(0)
	v_pk_fma_f32 v[44:45], v[104:105], v[44:45], v[114:115]
	ds_read_b128 v[98:101], v97 offset:2048
	v_pk_fma_f32 v[58:59], v[102:103], v[58:59], v[112:113]
	ds_read_b128 v[102:105], v97 offset:3072
	v_pk_mul_f32 v[74:75], v[124:125], v[108:109] op_sel_hi:[0,1]
	v_pk_mul_f32 v[52:53], v[124:125], v[52:53] op_sel_hi:[0,1]
	v_pk_mul_f32 v[68:69], v[124:125], v[106:107] op_sel_hi:[0,1]
	s_waitcnt lgkmcnt(1)
	v_pk_fma_f32 v[114:115], v[100:101], v[74:75], v[118:119]
	s_waitcnt lgkmcnt(0)
	v_pk_fma_f32 v[118:119], v[104:105], v[52:53], v[122:123]
	v_mul_f32_e32 v52, v37, v37
	v_mul_f32_e32 v53, v65, v65
	v_pk_fma_f32 v[116:117], v[98:99], v[68:69], v[116:117]
	v_pk_mul_f32 v[68:69], v[124:125], v[110:111] op_sel_hi:[0,1]
	v_fmac_f32_e32 v52, v36, v36
	v_fmac_f32_e32 v53, v64, v64
	v_pk_fma_f32 v[120:121], v[102:103], v[68:69], v[120:121]
	v_add_f32_e32 v52, v52, v53
	v_mul_f32_e32 v53, v59, v59
	v_mul_f32_e32 v68, v45, v45
	v_fmac_f32_e32 v53, v58, v58
	v_fmac_f32_e32 v68, v44, v44
	v_add_f32_e32 v53, v53, v68
	v_add_f32_e32 v52, v52, v53
	v_mul_f32_e32 v53, v117, v117
	v_mul_f32_e32 v68, v115, v115
	v_fmac_f32_e32 v53, v116, v116
	v_fmac_f32_e32 v68, v114, v114
	v_add_f32_e32 v53, v53, v68
	v_add_f32_e32 v52, v53, v52
	v_mul_f32_e32 v53, v121, v121
	v_mul_f32_e32 v68, v119, v119
	v_fmac_f32_e32 v53, v120, v120
	v_fmac_f32_e32 v68, v118, v118
	v_add_f32_e32 v53, v53, v68
	v_add_f32_e32 v52, v53, v52
	v_cvt_pk_bf16_f32 v98, v36, v37
	v_cvt_pk_bf16_f32 v99, v64, v65
	v_add_f32_dpp v52, v52, v52 quad_perm:[1,0,3,2] row_mask:0xf bank_mask:0xf bound_ctrl:1
	v_cvt_pk_bf16_f32 v100, v58, v59
	v_cvt_pk_bf16_f32 v101, v44, v45
	v_add_f32_dpp v52, v52, v52 quad_perm:[2,3,0,1] row_mask:0xf bank_mask:0xf bound_ctrl:1
	v_cvt_pk_bf16_f32 v102, v116, v117
	v_cvt_pk_bf16_f32 v103, v114, v115
	v_add_f32_dpp v52, v52, v52 row_half_mirror row_mask:0xf bank_mask:0xf bound_ctrl:1
	v_cvt_pk_bf16_f32 v104, v120, v121
	v_cvt_pk_bf16_f32 v105, v118, v119
	v_add_f32_dpp v52, v52, v52 row_mirror row_mask:0xf bank_mask:0xf bound_ctrl:1
	v_mov_b32_e32 v53, v52
	s_nop 1
	v_permlane16_swap_b32_e32 v52, v53
	v_add_f32_e32 v52, v52, v53
	v_mov_b32_e32 v53, v52
	s_nop 1
	v_permlane32_swap_b32_e32 v52, v53
	v_add_f32_e32 v52, v52, v53
	global_store_dwordx4 v[30:31], v[98:101], off
	v_fmamk_f32 v52, v52, 0x3a800000, v225
	global_store_dwordx4 v[30:31], v[102:105], off offset:16
	v_rsq_f32_e32 v122, v52
	ds_read_b128 v[98:101], v97 offset:4096
	ds_read_b128 v[102:105], v97 offset:8192
	ds_read_b128 v[106:109], v97 offset:5120
	ds_read_b128 v[110:113], v97 offset:9216
	s_lshl_b64 s[2:3], s[24:25], 10
	v_pk_mul_f32 v[30:31], v[36:37], v[122:123] op_sel_hi:[1,0]
	v_pk_mul_f32 v[36:37], v[64:65], v[122:123] op_sel_hi:[1,0]
	s_waitcnt lgkmcnt(2)
; #define GAS __attribute__((address_space(1)))
; #define LAS __attribute__((address_space(3)))
; __device__ __forceinline__ float rsq(float x) { return __builtin_amdgcn_rsqf(x); }
; __device__ __forceinline__ void post_mix_front(Frame& F, int l, int m, const f32x4 (&y)[4], f32x4 (&x)[4], const LAS float* PV) {
;     const int lane = F.lane, b = m >> 12; const LAS f32x4* A = (const LAS f32x4*)(PV + b * 3072); const LAS f32x4* Bv = A + 256; const LAS f32x4* Cv = A + 512;
;     const float rstd = rsq(row_ss(y, lane) * (1.0f / DM) + EPS);
; #pragma unroll
;     for (int j = 0; j < 4; ++j) { const int c4 = lane + 64 * j; x[j] = x[j] + A[c4] * (y[j] * rstd); }
;     roww_store_bf16((GAS bf16*)(F.ws + WS_XR) + (size_t)m * DM, lane, x);
;     const float rstd2 = rsq(row_ss(x, lane) * (1.0f / DM) + EPS);
;     v4u hw;
; #pragma unroll
;     for (int j = 0; j < 4; ++j) { const int c4 = lane + 64 * j; x[j] = x[j] * rstd2 * Bv[c4] + Cv[c4]; hw[j] = pk4_f8(x[j][0], x[j][1], x[j][2], x[j][3]); }
;     ((GAS v4u*)((GAS unsigned char*)(F.ws + WS_HN) + (size_t)m * DM))[lane] = hw;
; }
	v_pk_fma_f32 v[74:75], v[98:99], v[30:31], v[102:103]
	v_mov_b32_e32 v98, v183
	v_med3_f32 v30, v74, s33, v226
	v_med3_f32 v31, v75, s33, v226
	v_cvt_pk_fp8_f32 v98, v30, v31
	v_pk_fma_f32 v[68:69], v[100:101], v[36:37], v[104:105]
	v_mov_b32_e32 v99, v183
	v_med3_f32 v30, v68, s33, v226
	v_med3_f32 v31, v69, s33, v226
	v_cvt_pk_fp8_f32 v98, v30, v31 op_sel:[0,0,1]
	v_pk_mul_f32 v[30:31], v[58:59], v[122:123] op_sel_hi:[1,0]
	v_pk_mul_f32 v[36:37], v[44:45], v[122:123] op_sel_hi:[1,0]
	s_waitcnt lgkmcnt(0)
	v_pk_fma_f32 v[64:65], v[106:107], v[30:31], v[110:111]
	ds_read_b128 v[100:103], v97 offset:6144
	ds_read_b128 v[104:107], v97 offset:10240
	v_med3_f32 v30, v64, s33, v226
	v_med3_f32 v31, v65, s33, v226
	v_cvt_pk_fp8_f32 v99, v30, v31
	v_pk_fma_f32 v[58:59], v[108:109], v[36:37], v[112:113]
	v_pk_mul_f32 v[36:37], v[114:115], v[122:123] op_sel_hi:[1,0]
	v_med3_f32 v30, v58, s33, v226
	v_med3_f32 v31, v59, s33, v226
	v_cvt_pk_fp8_f32 v99, v30, v31 op_sel:[0,0,1]
	v_pk_mul_f32 v[30:31], v[116:117], v[122:123] op_sel_hi:[1,0]
	ds_read_b128 v[108:111], v97 offset:7168
	ds_read_b128 v[112:115], v97 offset:11264
	s_waitcnt lgkmcnt(2)
	v_pk_fma_f32 v[52:53], v[30:31], v[100:101], v[104:105]
	v_mov_b32_e32 v100, v183
	v_med3_f32 v30, v52, s33, v226
	v_med3_f32 v31, v53, s33, v226
	v_cvt_pk_fp8_f32 v100, v30, v31
	v_pk_fma_f32 v[44:45], v[36:37], v[102:103], v[106:107]
	v_mov_b32_e32 v101, v183
	v_med3_f32 v30, v44, s33, v226
	v_med3_f32 v31, v45, s33, v226
	v_cvt_pk_fp8_f32 v100, v30, v31 op_sel:[0,0,1]
	v_pk_mul_f32 v[30:31], v[120:121], v[122:123] op_sel_hi:[1,0]
	v_pk_mul_f32 v[102:103], v[118:119], v[122:123] op_sel_hi:[1,0]
	s_waitcnt lgkmcnt(0)
	v_pk_fma_f32 v[36:37], v[30:31], v[108:109], v[112:113]
	v_lshl_add_u64 v[106:107], v[6:7], 0, s[2:3]
	v_med3_f32 v30, v36, s33, v226
	v_med3_f32 v31, v37, s33, v226
	v_cvt_pk_fp8_f32 v101, v30, v31
	v_pk_fma_f32 v[30:31], v[102:103], v[110:111], v[114:115]
	v_mul_f32_e32 v103, v73, v73
	v_med3_f32 v97, v30, s33, v226
	v_med3_f32 v102, v31, s33, v226
	v_cvt_pk_fp8_f32 v101, v97, v102 op_sel:[0,0,1]
	v_mul_f32_e32 v97, v87, v87
	v_mul_f32_e32 v102, v85, v85
	v_fmac_f32_e32 v97, v86, v86
	v_fmac_f32_e32 v102, v84, v84
	v_add_f32_e32 v97, v97, v102
	v_mul_f32_e32 v102, v77, v77
	v_fmac_f32_e32 v102, v76, v76
	v_fmac_f32_e32 v103, v72, v72
	v_add_f32_e32 v102, v102, v103
	v_add_f32_e32 v97, v97, v102
	v_mul_f32_e32 v102, v63, v63
	v_mul_f32_e32 v103, v57, v57
	v_fmac_f32_e32 v102, v62, v62
	v_fmac_f32_e32 v103, v56, v56
	v_add_f32_e32 v102, v102, v103
	v_add_f32_e32 v97, v97, v102
	v_mul_f32_e32 v102, v51, v51
	v_mul_f32_e32 v103, v43, v43
	v_fmac_f32_e32 v102, v50, v50
	v_fmac_f32_e32 v103, v42, v42
	v_add_f32_e32 v102, v102, v103
	v_add_f32_e32 v97, v102, v97
	s_mul_i32 s2, s36, 0x3000
	global_store_dwordx4 v[106:107], v[98:101], off
	v_add_f32_dpp v97, v97, v97 quad_perm:[1,0,3,2] row_mask:0xf bank_mask:0xf bound_ctrl:1
	s_nop 1
	v_add_f32_dpp v97, v97, v97 quad_perm:[2,3,0,1] row_mask:0xf bank_mask:0xf bound_ctrl:1
	s_nop 1
	v_add_f32_dpp v97, v97, v97 row_half_mirror row_mask:0xf bank_mask:0xf bound_ctrl:1
	s_nop 1
	v_add_f32_dpp v97, v97, v97 row_mirror row_mask:0xf bank_mask:0xf bound_ctrl:1
	v_mov_b32_e32 v102, v97
	s_nop 1
	v_permlane16_swap_b32_e32 v97, v102
	v_add_f32_e32 v97, v97, v102
	v_mov_b32_e32 v102, v97
	s_nop 1
	v_permlane32_swap_b32_e32 v97, v102
	v_add_f32_e32 v97, v97, v102
	v_fmamk_f32 v97, v97, 0x3a800000, v225
	v_rsq_f32_e32 v108, v97
	v_add_u32_e32 v97, s2, v96
	ds_read_b128 v[102:105], v97
	s_lshl_b64 s[2:3], s[22:23], 10
	v_pk_mul_f32 v[98:99], v[108:109], v[86:87] op_sel_hi:[0,1]
	v_pk_mul_f32 v[100:101], v[108:109], v[84:85] op_sel_hi:[0,1]
	ds_read_b128 v[84:87], v97 offset:1024
	v_pk_mul_f32 v[76:77], v[108:109], v[76:77] op_sel_hi:[0,1]
	v_pk_mul_f32 v[72:73], v[108:109], v[72:73] op_sel_hi:[0,1]
	s_waitcnt lgkmcnt(1)
	v_pk_fma_f32 v[94:95], v[104:105], v[100:101], v[94:95]
	v_pk_fma_f32 v[98:99], v[102:103], v[98:99], v[92:93]
	s_waitcnt lgkmcnt(0)
	v_pk_fma_f32 v[72:73], v[86:87], v[72:73], v[90:91]
	ds_read_b128 v[90:93], v97 offset:2048
	v_pk_fma_f32 v[100:101], v[84:85], v[76:77], v[88:89]
	ds_read_b128 v[84:87], v97 offset:3072
	v_pk_mul_f32 v[50:51], v[108:109], v[50:51] op_sel_hi:[0,1]
	v_pk_mul_f32 v[62:63], v[108:109], v[62:63] op_sel_hi:[0,1]
	v_pk_mul_f32 v[56:57], v[108:109], v[56:57] op_sel_hi:[0,1]
	s_waitcnt lgkmcnt(1)
	v_pk_fma_f32 v[56:57], v[92:93], v[56:57], v[82:83]
	s_waitcnt lgkmcnt(0)
	v_pk_fma_f32 v[50:51], v[84:85], v[50:51], v[66:67]
	v_mul_f32_e32 v66, v99, v99
	v_mul_f32_e32 v67, v95, v95
	v_fmac_f32_e32 v66, v98, v98
	v_fmac_f32_e32 v67, v94, v94
	v_add_f32_e32 v66, v66, v67
	v_mul_f32_e32 v67, v101, v101
	v_mul_f32_e32 v84, v73, v73
	v_fmac_f32_e32 v67, v100, v100
	v_fmac_f32_e32 v84, v72, v72
	v_pk_fma_f32 v[62:63], v[90:91], v[62:63], v[80:81]
	v_add_f32_e32 v67, v67, v84
	v_add_f32_e32 v66, v66, v67
	v_mul_f32_e32 v67, v63, v63
	v_mul_f32_e32 v84, v57, v57
	v_pk_mul_f32 v[42:43], v[108:109], v[42:43] op_sel_hi:[0,1]
	v_fmac_f32_e32 v67, v62, v62
	v_fmac_f32_e32 v84, v56, v56
	v_pk_fma_f32 v[42:43], v[86:87], v[42:43], v[78:79]
	v_add_f32_e32 v67, v67, v84
	v_add_f32_e32 v66, v67, v66
	v_mul_f32_e32 v67, v51, v51
	v_mul_f32_e32 v84, v43, v43
	v_fmac_f32_e32 v67, v50, v50
	v_fmac_f32_e32 v84, v42, v42
	v_add_f32_e32 v67, v67, v84
	v_add_f32_e32 v66, v67, v66
	v_cvt_pk_bf16_f32 v76, v98, v99
	v_cvt_pk_bf16_f32 v77, v94, v95
	v_add_f32_dpp v66, v66, v66 quad_perm:[1,0,3,2] row_mask:0xf bank_mask:0xf bound_ctrl:1
	v_cvt_pk_bf16_f32 v78, v100, v101
	v_cvt_pk_bf16_f32 v79, v72, v73
	v_add_f32_dpp v66, v66, v66 quad_perm:[2,3,0,1] row_mask:0xf bank_mask:0xf bound_ctrl:1
	global_store_dwordx4 v[70:71], v[76:79], off
	ds_read_b128 v[76:79], v97 offset:4096
	ds_read_b128 v[84:87], v97 offset:8192
	v_add_f32_dpp v66, v66, v66 row_half_mirror row_mask:0xf bank_mask:0xf bound_ctrl:1
	v_cvt_pk_bf16_f32 v80, v62, v63
	v_cvt_pk_bf16_f32 v81, v56, v57
	v_add_f32_dpp v66, v66, v66 row_mirror row_mask:0xf bank_mask:0xf bound_ctrl:1
	v_mov_b32_e32 v67, v66
	s_nop 1
	v_permlane16_swap_b32_e32 v66, v67
	v_add_f32_e32 v66, v66, v67
	v_mov_b32_e32 v67, v66
	s_nop 1
	v_permlane32_swap_b32_e32 v66, v67
	v_add_f32_e32 v66, v66, v67
	v_fmamk_f32 v66, v66, 0x3a800000, v225
	v_rsq_f32_e32 v106, v66
	v_cvt_pk_bf16_f32 v82, v50, v51
	v_cvt_pk_bf16_f32 v83, v42, v43
	v_pk_mul_f32 v[66:67], v[98:99], v[106:107] op_sel_hi:[1,0]
	s_waitcnt lgkmcnt(0)
; #define GAS __attribute__((address_space(1)))
; #define LAS __attribute__((address_space(3)))
; __device__ __forceinline__ float rsq(float x) { return __builtin_amdgcn_rsqf(x); }
; __device__ __forceinline__ void post_mix_front(Frame& F, int l, int m, const f32x4 (&y)[4], f32x4 (&x)[4], const LAS float* PV) {
;     ...
;     const float rstd2 = rsq(row_ss(x, lane) * (1.0f / DM) + EPS);
;     v4u hw;
; #pragma unroll
;     for (int j = 0; j < 4; ++j) { const int c4 = lane + 64 * j; x[j] = x[j] * rstd2 * Bv[c4] + Cv[c4]; hw[j] = pk4_f8(x[j][0], x[j][1], x[j][2], x[j][3]); }
;     ((GAS v4u*)((GAS unsigned char*)(F.ws + WS_HN) + (size_t)m * DM))[lane] = hw;
; __device__ __forceinline__ void phase_post_mix(Frame& F, int l) {
;     ...
;         for (int j = 0; j < 4; ++j) { const LAS float* wg = rws + (lane + 64 * j) * 68;
; #pragma unroll
;             for (int i = 0; i < 4; ++i) { const f32x4 w0 = *(const LAS f32x4*)(wg + 16 * i), w1 = *(const LAS f32x4*)(wg + 16 * i + 4), w2 = *(const LAS f32x4*)(wg + 16 * i + 8), w3 = *(const LAS f32x4*)(wg + 16 * i + 12);
;                 const r_f32x2 wv[8] = {{w0[0], w0[1]}, {w0[2], w0[3]}, {w1[0], w1[1]}, {w1[2], w1[3]}, {w2[0], w2[1]}, {w2[2], w2[3]}, {w3[0], w3[1]}, {w3[2], w3[3]}};
; #pragma unroll
;                 for (int q = 0; q < 4; ++q) { const float h = xx[q][j][i]; const r_f32x2 hh = {h, h};
; #pragma unroll
;                     for (int e = 0; e < 8; ++e) lg2[q][e] = __builtin_elementwise_fma(hh, wv[e], lg2[q][e]); }
	v_pk_fma_f32 v[108:109], v[76:77], v[66:67], v[84:85]
	v_mov_b32_e32 v84, v183
	v_med3_f32 v66, v108, s33, v226
	v_med3_f32 v67, v109, s33, v226
	v_pk_mul_f32 v[98:99], v[94:95], v[106:107] op_sel_hi:[1,0]
	ds_read_b128 v[88:91], v97 offset:5120
	ds_read_b128 v[92:95], v97 offset:9216
	v_cvt_pk_fp8_f32 v84, v66, v67
	v_pk_fma_f32 v[76:77], v[78:79], v[98:99], v[86:87]
	v_pk_mul_f32 v[78:79], v[72:73], v[106:107] op_sel_hi:[1,0]
	v_med3_f32 v66, v76, s33, v226
	v_med3_f32 v67, v77, s33, v226
	v_cvt_pk_fp8_f32 v84, v66, v67 op_sel:[0,0,1]
	v_pk_mul_f32 v[66:67], v[100:101], v[106:107] op_sel_hi:[1,0]
	v_mov_b32_e32 v85, v183
	s_waitcnt lgkmcnt(0)
	v_pk_fma_f32 v[72:73], v[88:89], v[66:67], v[92:93]
	v_pk_mul_f32 v[62:63], v[62:63], v[106:107] op_sel_hi:[1,0]
	v_med3_f32 v66, v72, s33, v226
	v_med3_f32 v67, v73, s33, v226
	v_cvt_pk_fp8_f32 v85, v66, v67
	v_pk_fma_f32 v[66:67], v[90:91], v[78:79], v[94:95]
	ds_read_b128 v[86:89], v97 offset:6144
	ds_read_b128 v[90:93], v97 offset:10240
	v_med3_f32 v78, v66, s33, v226
	v_med3_f32 v79, v67, s33, v226
	ds_read_b128 v[98:101], v97 offset:7168
	ds_read_b128 v[102:105], v97 offset:11264
	v_cvt_pk_fp8_f32 v85, v78, v79 op_sel:[0,0,1]
	s_waitcnt lgkmcnt(2)
	v_pk_fma_f32 v[62:63], v[62:63], v[86:87], v[90:91]
	v_mov_b32_e32 v86, v183
	v_med3_f32 v78, v62, s33, v226
	v_med3_f32 v79, v63, s33, v226
	v_cvt_pk_fp8_f32 v86, v78, v79
	v_pk_mul_f32 v[56:57], v[56:57], v[106:107] op_sel_hi:[1,0]
	v_pk_mul_f32 v[50:51], v[50:51], v[106:107] op_sel_hi:[1,0]
	v_pk_fma_f32 v[56:57], v[56:57], v[88:89], v[92:93]
	s_waitcnt lgkmcnt(0)
	v_pk_fma_f32 v[50:51], v[50:51], v[98:99], v[102:103]
	v_med3_f32 v78, v56, s33, v226
	v_med3_f32 v79, v57, s33, v226
	v_cvt_pk_fp8_f32 v86, v78, v79 op_sel:[0,0,1]
	v_med3_f32 v78, v50, s33, v226
	v_med3_f32 v79, v51, s33, v226
	v_mov_b32_e32 v87, v183
	v_cvt_pk_fp8_f32 v87, v78, v79
	v_pk_mul_f32 v[42:43], v[42:43], v[106:107] op_sel_hi:[1,0]
	global_store_dwordx4 v[70:71], v[80:83], off offset:16
	v_pk_fma_f32 v[42:43], v[42:43], v[100:101], v[104:105]
	v_lshl_add_u64 v[70:71], v[6:7], 0, s[2:3]
	v_med3_f32 v78, v42, s33, v226
	v_med3_f32 v79, v43, s33, v226
	v_cvt_pk_fp8_f32 v87, v78, v79 op_sel:[0,0,1]
	ds_read_b128 v[78:81], v1
	s_mov_b32 s2, 0xc2ce8ed0
	global_store_dwordx4 v[70:71], v[84:87], off
	ds_read_b128 v[82:85], v1 offset:16
	ds_read_b128 v[86:89], v1 offset:32
	ds_read_b128 v[90:93], v1 offset:48
	s_waitcnt lgkmcnt(3)
	v_pk_fma_f32 v[70:71], v[48:49], v[78:79], 0 op_sel_hi:[0,1,0]
	v_pk_fma_f32 v[94:95], v[48:49], v[80:81], 0 op_sel_hi:[0,1,0]
	s_waitcnt lgkmcnt(2)
	v_pk_fma_f32 v[98:99], v[48:49], v[82:83], 0 op_sel_hi:[0,1,0]
	v_pk_fma_f32 v[100:101], v[48:49], v[84:85], 0 op_sel_hi:[0,1,0]
	s_waitcnt lgkmcnt(1)
	v_pk_fma_f32 v[102:103], v[48:49], v[86:87], 0 op_sel_hi:[0,1,0]
	v_pk_fma_f32 v[104:105], v[48:49], v[88:89], 0 op_sel_hi:[0,1,0]
	s_waitcnt lgkmcnt(0)
	v_pk_fma_f32 v[106:107], v[48:49], v[90:91], 0 op_sel_hi:[0,1,0]
	v_pk_fma_f32 v[110:111], v[48:49], v[92:93], 0 op_sel_hi:[0,1,0]
	v_pk_fma_f32 v[112:113], v[60:61], v[78:79], 0 op_sel_hi:[0,1,0]
	v_pk_fma_f32 v[114:115], v[60:61], v[80:81], 0 op_sel_hi:[0,1,0]
	v_pk_fma_f32 v[116:117], v[60:61], v[82:83], 0 op_sel_hi:[0,1,0]
	v_pk_fma_f32 v[118:119], v[60:61], v[84:85], 0 op_sel_hi:[0,1,0]
	v_pk_fma_f32 v[120:121], v[60:61], v[86:87], 0 op_sel_hi:[0,1,0]
	v_pk_fma_f32 v[122:123], v[60:61], v[88:89], 0 op_sel_hi:[0,1,0]
	v_pk_fma_f32 v[124:125], v[60:61], v[90:91], 0 op_sel_hi:[0,1,0]
	v_pk_fma_f32 v[126:127], v[60:61], v[92:93], 0 op_sel_hi:[0,1,0]
	v_pk_fma_f32 v[128:129], v[74:75], v[78:79], 0 op_sel_hi:[0,1,0]
	v_pk_fma_f32 v[130:131], v[74:75], v[80:81], 0 op_sel_hi:[0,1,0]
	v_pk_fma_f32 v[132:133], v[74:75], v[82:83], 0 op_sel_hi:[0,1,0]
	v_pk_fma_f32 v[134:135], v[74:75], v[84:85], 0 op_sel_hi:[0,1,0]
	v_pk_fma_f32 v[136:137], v[74:75], v[86:87], 0 op_sel_hi:[0,1,0]
	v_pk_fma_f32 v[138:139], v[74:75], v[88:89], 0 op_sel_hi:[0,1,0]
	v_pk_fma_f32 v[140:141], v[74:75], v[90:91], 0 op_sel_hi:[0,1,0]
	v_pk_fma_f32 v[142:143], v[74:75], v[92:93], 0 op_sel_hi:[0,1,0]
	v_pk_fma_f32 v[144:145], v[108:109], v[78:79], 0 op_sel_hi:[0,1,0]
	v_pk_fma_f32 v[146:147], v[108:109], v[80:81], 0 op_sel_hi:[0,1,0]
	v_pk_fma_f32 v[148:149], v[108:109], v[82:83], 0 op_sel_hi:[0,1,0]
	v_pk_fma_f32 v[150:151], v[108:109], v[84:85], 0 op_sel_hi:[0,1,0]
	v_pk_fma_f32 v[152:153], v[108:109], v[86:87], 0 op_sel_hi:[0,1,0]
	v_pk_fma_f32 v[154:155], v[108:109], v[88:89], 0 op_sel_hi:[0,1,0]
	v_pk_fma_f32 v[156:157], v[108:109], v[90:91], 0 op_sel_hi:[0,1,0]
	v_pk_fma_f32 v[158:159], v[108:109], v[92:93], 0 op_sel_hi:[0,1,0]
	ds_read_b128 v[78:81], v1 offset:64
	ds_read_b128 v[82:85], v1 offset:80
	ds_read_b128 v[86:89], v1 offset:96
	ds_read_b128 v[90:93], v1 offset:112
	s_waitcnt lgkmcnt(3)
	v_pk_fma_f32 v[70:71], v[48:49], v[78:79], v[70:71] op_sel:[1,0,0]
	v_pk_fma_f32 v[94:95], v[48:49], v[80:81], v[94:95] op_sel:[1,0,0]
	s_waitcnt lgkmcnt(2)
	v_pk_fma_f32 v[98:99], v[48:49], v[82:83], v[98:99] op_sel:[1,0,0]
	v_pk_fma_f32 v[100:101], v[48:49], v[84:85], v[100:101] op_sel:[1,0,0]
	s_waitcnt lgkmcnt(1)
	v_pk_fma_f32 v[102:103], v[48:49], v[86:87], v[102:103] op_sel:[1,0,0]
	v_pk_fma_f32 v[104:105], v[48:49], v[88:89], v[104:105] op_sel:[1,0,0]
	s_waitcnt lgkmcnt(0)
; #define LAS __attribute__((address_space(3)))
; __device__ __forceinline__ void phase_post_mix(Frame& F, int l) {
;     ...
;         for (int j = 0; j < 4; ++j) { const LAS float* wg = rws + (lane + 64 * j) * 68;
; #pragma unroll
;             for (int i = 0; i < 4; ++i) { const f32x4 w0 = *(const LAS f32x4*)(wg + 16 * i), w1 = *(const LAS f32x4*)(wg + 16 * i + 4), w2 = *(const LAS f32x4*)(wg + 16 * i + 8), w3 = *(const LAS f32x4*)(wg + 16 * i + 12);
;                 const r_f32x2 wv[8] = {{w0[0], w0[1]}, {w0[2], w0[3]}, {w1[0], w1[1]}, {w1[2], w1[3]}, {w2[0], w2[1]}, {w2[2], w2[3]}, {w3[0], w3[1]}, {w3[2], w3[3]}};
; #pragma unroll
;                 for (int q = 0; q < 4; ++q) { const float h = xx[q][j][i]; const r_f32x2 hh = {h, h};
; #pragma unroll
;                     for (int e = 0; e < 8; ++e) lg2[q][e] = __builtin_elementwise_fma(hh, wv[e], lg2[q][e]); }
; #pragma unroll
;                 for (int q = 0; q < 4; ++q)
;                     asm volatile("" : "+v"(lg2[q][0]), "+v"(lg2[q][1]), "+v"(lg2[q][2]), "+v"(lg2[q][3]), "+v"(lg2[q][4]), "+v"(lg2[q][5]), "+v"(lg2[q][6]), "+v"(lg2[q][7]));
;                 } }
	v_pk_fma_f32 v[106:107], v[48:49], v[90:91], v[106:107] op_sel:[1,0,0]
	v_pk_fma_f32 v[48:49], v[48:49], v[92:93], v[110:111] op_sel:[1,0,0]
	v_pk_fma_f32 v[110:111], v[60:61], v[78:79], v[112:113] op_sel:[1,0,0]
	v_pk_fma_f32 v[112:113], v[60:61], v[80:81], v[114:115] op_sel:[1,0,0]
	v_pk_fma_f32 v[114:115], v[60:61], v[82:83], v[116:117] op_sel:[1,0,0]
	v_pk_fma_f32 v[116:117], v[60:61], v[84:85], v[118:119] op_sel:[1,0,0]
	v_pk_fma_f32 v[118:119], v[60:61], v[86:87], v[120:121] op_sel:[1,0,0]
	v_pk_fma_f32 v[120:121], v[60:61], v[88:89], v[122:123] op_sel:[1,0,0]
	v_pk_fma_f32 v[122:123], v[60:61], v[90:91], v[124:125] op_sel:[1,0,0]
	v_pk_fma_f32 v[60:61], v[60:61], v[92:93], v[126:127] op_sel:[1,0,0]
	v_pk_fma_f32 v[124:125], v[74:75], v[78:79], v[128:129] op_sel:[1,0,0]
	v_pk_fma_f32 v[126:127], v[74:75], v[80:81], v[130:131] op_sel:[1,0,0]
	v_pk_fma_f32 v[128:129], v[74:75], v[82:83], v[132:133] op_sel:[1,0,0]
	v_pk_fma_f32 v[130:131], v[74:75], v[84:85], v[134:135] op_sel:[1,0,0]
	v_pk_fma_f32 v[132:133], v[74:75], v[86:87], v[136:137] op_sel:[1,0,0]
	v_pk_fma_f32 v[134:135], v[74:75], v[88:89], v[138:139] op_sel:[1,0,0]
	v_pk_fma_f32 v[136:137], v[74:75], v[90:91], v[140:141] op_sel:[1,0,0]
	v_pk_fma_f32 v[74:75], v[74:75], v[92:93], v[142:143] op_sel:[1,0,0]
	v_pk_fma_f32 v[138:139], v[108:109], v[78:79], v[144:145] op_sel:[1,0,0]
	v_pk_fma_f32 v[140:141], v[108:109], v[80:81], v[146:147] op_sel:[1,0,0]
	v_pk_fma_f32 v[142:143], v[108:109], v[82:83], v[148:149] op_sel:[1,0,0]
	v_pk_fma_f32 v[144:145], v[108:109], v[84:85], v[150:151] op_sel:[1,0,0]
	v_pk_fma_f32 v[146:147], v[108:109], v[86:87], v[152:153] op_sel:[1,0,0]
	v_pk_fma_f32 v[148:149], v[108:109], v[88:89], v[154:155] op_sel:[1,0,0]
	v_pk_fma_f32 v[150:151], v[108:109], v[90:91], v[156:157] op_sel:[1,0,0]
	v_pk_fma_f32 v[108:109], v[108:109], v[92:93], v[158:159] op_sel:[1,0,0]
	s_nop 0
	ds_read_b128 v[78:81], v1 offset:128
	ds_read_b128 v[82:85], v1 offset:144
	ds_read_b128 v[86:89], v1 offset:160
	ds_read_b128 v[90:93], v1 offset:176
	s_waitcnt lgkmcnt(3)
	v_pk_fma_f32 v[70:71], v[40:41], v[78:79], v[70:71] op_sel_hi:[0,1,1]
	v_pk_fma_f32 v[94:95], v[40:41], v[80:81], v[94:95] op_sel_hi:[0,1,1]
	s_waitcnt lgkmcnt(2)
	v_pk_fma_f32 v[98:99], v[40:41], v[82:83], v[98:99] op_sel_hi:[0,1,1]
	v_pk_fma_f32 v[100:101], v[40:41], v[84:85], v[100:101] op_sel_hi:[0,1,1]
	s_waitcnt lgkmcnt(1)
	v_pk_fma_f32 v[102:103], v[40:41], v[86:87], v[102:103] op_sel_hi:[0,1,1]
	v_pk_fma_f32 v[104:105], v[40:41], v[88:89], v[104:105] op_sel_hi:[0,1,1]
	s_waitcnt lgkmcnt(0)
	v_pk_fma_f32 v[106:107], v[40:41], v[90:91], v[106:107] op_sel_hi:[0,1,1]
	v_pk_fma_f32 v[48:49], v[40:41], v[92:93], v[48:49] op_sel_hi:[0,1,1]
	v_pk_fma_f32 v[110:111], v[54:55], v[78:79], v[110:111] op_sel_hi:[0,1,1]
	v_pk_fma_f32 v[112:113], v[54:55], v[80:81], v[112:113] op_sel_hi:[0,1,1]
	v_pk_fma_f32 v[114:115], v[54:55], v[82:83], v[114:115] op_sel_hi:[0,1,1]
	v_pk_fma_f32 v[116:117], v[54:55], v[84:85], v[116:117] op_sel_hi:[0,1,1]
	v_pk_fma_f32 v[118:119], v[54:55], v[86:87], v[118:119] op_sel_hi:[0,1,1]
	v_pk_fma_f32 v[120:121], v[54:55], v[88:89], v[120:121] op_sel_hi:[0,1,1]
	v_pk_fma_f32 v[122:123], v[54:55], v[90:91], v[122:123] op_sel_hi:[0,1,1]
	v_pk_fma_f32 v[60:61], v[54:55], v[92:93], v[60:61] op_sel_hi:[0,1,1]
	v_pk_fma_f32 v[124:125], v[68:69], v[78:79], v[124:125] op_sel_hi:[0,1,1]
	v_pk_fma_f32 v[126:127], v[68:69], v[80:81], v[126:127] op_sel_hi:[0,1,1]
	v_pk_fma_f32 v[128:129], v[68:69], v[82:83], v[128:129] op_sel_hi:[0,1,1]
	v_pk_fma_f32 v[130:131], v[68:69], v[84:85], v[130:131] op_sel_hi:[0,1,1]
	v_pk_fma_f32 v[132:133], v[68:69], v[86:87], v[132:133] op_sel_hi:[0,1,1]
	v_pk_fma_f32 v[134:135], v[68:69], v[88:89], v[134:135] op_sel_hi:[0,1,1]
	v_pk_fma_f32 v[136:137], v[68:69], v[90:91], v[136:137] op_sel_hi:[0,1,1]
	v_pk_fma_f32 v[74:75], v[68:69], v[92:93], v[74:75] op_sel_hi:[0,1,1]
	v_pk_fma_f32 v[138:139], v[76:77], v[78:79], v[138:139] op_sel_hi:[0,1,1]
	v_pk_fma_f32 v[140:141], v[76:77], v[80:81], v[140:141] op_sel_hi:[0,1,1]
	v_pk_fma_f32 v[142:143], v[76:77], v[82:83], v[142:143] op_sel_hi:[0,1,1]
	v_pk_fma_f32 v[144:145], v[76:77], v[84:85], v[144:145] op_sel_hi:[0,1,1]
	v_pk_fma_f32 v[146:147], v[76:77], v[86:87], v[146:147] op_sel_hi:[0,1,1]
	v_pk_fma_f32 v[148:149], v[76:77], v[88:89], v[148:149] op_sel_hi:[0,1,1]
	v_pk_fma_f32 v[150:151], v[76:77], v[90:91], v[150:151] op_sel_hi:[0,1,1]
	v_pk_fma_f32 v[108:109], v[76:77], v[92:93], v[108:109] op_sel_hi:[0,1,1]
	ds_read_b128 v[78:81], v1 offset:192
	ds_read_b128 v[82:85], v1 offset:208
	ds_read_b128 v[86:89], v1 offset:224
	ds_read_b128 v[90:93], v1 offset:240
	s_waitcnt lgkmcnt(3)
	v_pk_fma_f32 v[152:153], v[40:41], v[78:79], v[70:71] op_sel:[1,0,0]
	v_pk_fma_f32 v[94:95], v[40:41], v[80:81], v[94:95] op_sel:[1,0,0]
	s_waitcnt lgkmcnt(2)
	v_pk_fma_f32 v[98:99], v[40:41], v[82:83], v[98:99] op_sel:[1,0,0]
	v_pk_fma_f32 v[100:101], v[40:41], v[84:85], v[100:101] op_sel:[1,0,0]
	s_waitcnt lgkmcnt(1)
	v_pk_fma_f32 v[102:103], v[40:41], v[86:87], v[102:103] op_sel:[1,0,0]
	v_pk_fma_f32 v[104:105], v[40:41], v[88:89], v[104:105] op_sel:[1,0,0]
	s_waitcnt lgkmcnt(0)
; #define LAS __attribute__((address_space(3)))
; __device__ __forceinline__ void phase_post_mix(Frame& F, int l) {
;     ...
;         for (int j = 0; j < 4; ++j) { const LAS float* wg = rws + (lane + 64 * j) * 68;
; #pragma unroll
;             for (int i = 0; i < 4; ++i) { const f32x4 w0 = *(const LAS f32x4*)(wg + 16 * i), w1 = *(const LAS f32x4*)(wg + 16 * i + 4), w2 = *(const LAS f32x4*)(wg + 16 * i + 8), w3 = *(const LAS f32x4*)(wg + 16 * i + 12);
;                 const r_f32x2 wv[8] = {{w0[0], w0[1]}, {w0[2], w0[3]}, {w1[0], w1[1]}, {w1[2], w1[3]}, {w2[0], w2[1]}, {w2[2], w2[3]}, {w3[0], w3[1]}, {w3[2], w3[3]}};
; #pragma unroll
;                 for (int q = 0; q < 4; ++q) { const float h = xx[q][j][i]; const r_f32x2 hh = {h, h};
; #pragma unroll
;                     for (int e = 0; e < 8; ++e) lg2[q][e] = __builtin_elementwise_fma(hh, wv[e], lg2[q][e]); }
; #pragma unroll
;                 for (int q = 0; q < 4; ++q)
;                     asm volatile("" : "+v"(lg2[q][0]), "+v"(lg2[q][1]), "+v"(lg2[q][2]), "+v"(lg2[q][3]), "+v"(lg2[q][4]), "+v"(lg2[q][5]), "+v"(lg2[q][6]), "+v"(lg2[q][7]));
;                 } }
	v_pk_fma_f32 v[106:107], v[40:41], v[90:91], v[106:107] op_sel:[1,0,0]
	v_pk_fma_f32 v[40:41], v[40:41], v[92:93], v[48:49] op_sel:[1,0,0]
	v_pk_fma_f32 v[48:49], v[54:55], v[78:79], v[110:111] op_sel:[1,0,0]
	v_pk_fma_f32 v[110:111], v[54:55], v[80:81], v[112:113] op_sel:[1,0,0]
	v_pk_fma_f32 v[112:113], v[54:55], v[82:83], v[114:115] op_sel:[1,0,0]
	v_pk_fma_f32 v[114:115], v[54:55], v[84:85], v[116:117] op_sel:[1,0,0]
	v_pk_fma_f32 v[116:117], v[54:55], v[86:87], v[118:119] op_sel:[1,0,0]
	v_pk_fma_f32 v[118:119], v[54:55], v[88:89], v[120:121] op_sel:[1,0,0]
	v_pk_fma_f32 v[120:121], v[54:55], v[90:91], v[122:123] op_sel:[1,0,0]
	v_pk_fma_f32 v[54:55], v[54:55], v[92:93], v[60:61] op_sel:[1,0,0]
	v_pk_fma_f32 v[60:61], v[68:69], v[78:79], v[124:125] op_sel:[1,0,0]
	v_pk_fma_f32 v[122:123], v[68:69], v[80:81], v[126:127] op_sel:[1,0,0]
	v_pk_fma_f32 v[124:125], v[68:69], v[82:83], v[128:129] op_sel:[1,0,0]
	v_pk_fma_f32 v[126:127], v[68:69], v[84:85], v[130:131] op_sel:[1,0,0]
	v_pk_fma_f32 v[128:129], v[68:69], v[86:87], v[132:133] op_sel:[1,0,0]
	v_pk_fma_f32 v[130:131], v[68:69], v[88:89], v[134:135] op_sel:[1,0,0]
	v_pk_fma_f32 v[132:133], v[68:69], v[90:91], v[136:137] op_sel:[1,0,0]
	v_pk_fma_f32 v[134:135], v[68:69], v[92:93], v[74:75] op_sel:[1,0,0]
	v_pk_fma_f32 v[136:137], v[76:77], v[78:79], v[138:139] op_sel:[1,0,0]
	v_pk_fma_f32 v[138:139], v[76:77], v[80:81], v[140:141] op_sel:[1,0,0]
	v_pk_fma_f32 v[140:141], v[76:77], v[82:83], v[142:143] op_sel:[1,0,0]
	v_pk_fma_f32 v[142:143], v[76:77], v[84:85], v[144:145] op_sel:[1,0,0]
	v_pk_fma_f32 v[86:87], v[76:77], v[86:87], v[146:147] op_sel:[1,0,0]
	v_pk_fma_f32 v[88:89], v[76:77], v[88:89], v[148:149] op_sel:[1,0,0]
	v_pk_fma_f32 v[90:91], v[76:77], v[90:91], v[150:151] op_sel:[1,0,0]
	v_pk_fma_f32 v[92:93], v[76:77], v[92:93], v[108:109] op_sel:[1,0,0]
	s_nop 0
	ds_read_b128 v[68:71], v1 offset:17408
	ds_read_b128 v[74:77], v1 offset:17424
	ds_read_b128 v[78:81], v1 offset:17440
	ds_read_b128 v[82:85], v1 offset:17456
	s_waitcnt lgkmcnt(3)
	v_pk_fma_f32 v[108:109], v[34:35], v[68:69], v[152:153] op_sel_hi:[0,1,1]
	v_pk_fma_f32 v[94:95], v[34:35], v[70:71], v[94:95] op_sel_hi:[0,1,1]
	s_waitcnt lgkmcnt(2)
	v_pk_fma_f32 v[98:99], v[34:35], v[74:75], v[98:99] op_sel_hi:[0,1,1]
	v_pk_fma_f32 v[100:101], v[34:35], v[76:77], v[100:101] op_sel_hi:[0,1,1]
	s_waitcnt lgkmcnt(1)
	v_pk_fma_f32 v[102:103], v[34:35], v[78:79], v[102:103] op_sel_hi:[0,1,1]
	v_pk_fma_f32 v[104:105], v[34:35], v[80:81], v[104:105] op_sel_hi:[0,1,1]
	s_waitcnt lgkmcnt(0)
	v_pk_fma_f32 v[106:107], v[34:35], v[82:83], v[106:107] op_sel_hi:[0,1,1]
	v_pk_fma_f32 v[40:41], v[34:35], v[84:85], v[40:41] op_sel_hi:[0,1,1]
	v_pk_fma_f32 v[48:49], v[46:47], v[68:69], v[48:49] op_sel_hi:[0,1,1]
	v_pk_fma_f32 v[110:111], v[46:47], v[70:71], v[110:111] op_sel_hi:[0,1,1]
	v_pk_fma_f32 v[112:113], v[46:47], v[74:75], v[112:113] op_sel_hi:[0,1,1]
	v_pk_fma_f32 v[114:115], v[46:47], v[76:77], v[114:115] op_sel_hi:[0,1,1]
	v_pk_fma_f32 v[116:117], v[46:47], v[78:79], v[116:117] op_sel_hi:[0,1,1]
	v_pk_fma_f32 v[118:119], v[46:47], v[80:81], v[118:119] op_sel_hi:[0,1,1]
	v_pk_fma_f32 v[120:121], v[46:47], v[82:83], v[120:121] op_sel_hi:[0,1,1]
	v_pk_fma_f32 v[54:55], v[46:47], v[84:85], v[54:55] op_sel_hi:[0,1,1]
	v_pk_fma_f32 v[60:61], v[64:65], v[68:69], v[60:61] op_sel_hi:[0,1,1]
	v_pk_fma_f32 v[122:123], v[64:65], v[70:71], v[122:123] op_sel_hi:[0,1,1]
	v_pk_fma_f32 v[124:125], v[64:65], v[74:75], v[124:125] op_sel_hi:[0,1,1]
	v_pk_fma_f32 v[126:127], v[64:65], v[76:77], v[126:127] op_sel_hi:[0,1,1]
	v_pk_fma_f32 v[128:129], v[64:65], v[78:79], v[128:129] op_sel_hi:[0,1,1]
	v_pk_fma_f32 v[130:131], v[64:65], v[80:81], v[130:131] op_sel_hi:[0,1,1]
	v_pk_fma_f32 v[132:133], v[64:65], v[82:83], v[132:133] op_sel_hi:[0,1,1]
	v_pk_fma_f32 v[134:135], v[64:65], v[84:85], v[134:135] op_sel_hi:[0,1,1]
	v_pk_fma_f32 v[136:137], v[72:73], v[68:69], v[136:137] op_sel_hi:[0,1,1]
	v_pk_fma_f32 v[138:139], v[72:73], v[70:71], v[138:139] op_sel_hi:[0,1,1]
	v_pk_fma_f32 v[140:141], v[72:73], v[74:75], v[140:141] op_sel_hi:[0,1,1]
	v_pk_fma_f32 v[142:143], v[72:73], v[76:77], v[142:143] op_sel_hi:[0,1,1]
	v_pk_fma_f32 v[86:87], v[72:73], v[78:79], v[86:87] op_sel_hi:[0,1,1]
	v_pk_fma_f32 v[88:89], v[72:73], v[80:81], v[88:89] op_sel_hi:[0,1,1]
	v_pk_fma_f32 v[90:91], v[72:73], v[82:83], v[90:91] op_sel_hi:[0,1,1]
	v_pk_fma_f32 v[92:93], v[72:73], v[84:85], v[92:93] op_sel_hi:[0,1,1]
	ds_read_b128 v[68:71], v1 offset:17472
	ds_read_b128 v[74:77], v1 offset:17488
	ds_read_b128 v[78:81], v1 offset:17504
	ds_read_b128 v[82:85], v1 offset:17520
	s_waitcnt lgkmcnt(3)
	v_pk_fma_f32 v[108:109], v[34:35], v[68:69], v[108:109] op_sel:[1,0,0]
	v_pk_fma_f32 v[94:95], v[34:35], v[70:71], v[94:95] op_sel:[1,0,0]
	s_waitcnt lgkmcnt(2)
	v_pk_fma_f32 v[98:99], v[34:35], v[74:75], v[98:99] op_sel:[1,0,0]
	v_pk_fma_f32 v[100:101], v[34:35], v[76:77], v[100:101] op_sel:[1,0,0]
	s_waitcnt lgkmcnt(1)
	v_pk_fma_f32 v[102:103], v[34:35], v[78:79], v[102:103] op_sel:[1,0,0]
	v_pk_fma_f32 v[104:105], v[34:35], v[80:81], v[104:105] op_sel:[1,0,0]
	s_waitcnt lgkmcnt(0)
; #define LAS __attribute__((address_space(3)))
; __device__ __forceinline__ void phase_post_mix(Frame& F, int l) {
;     ...
;         for (int j = 0; j < 4; ++j) { const LAS float* wg = rws + (lane + 64 * j) * 68;
; #pragma unroll
;             for (int i = 0; i < 4; ++i) { const f32x4 w0 = *(const LAS f32x4*)(wg + 16 * i), w1 = *(const LAS f32x4*)(wg + 16 * i + 4), w2 = *(const LAS f32x4*)(wg + 16 * i + 8), w3 = *(const LAS f32x4*)(wg + 16 * i + 12);
;                 const r_f32x2 wv[8] = {{w0[0], w0[1]}, {w0[2], w0[3]}, {w1[0], w1[1]}, {w1[2], w1[3]}, {w2[0], w2[1]}, {w2[2], w2[3]}, {w3[0], w3[1]}, {w3[2], w3[3]}};
; #pragma unroll
;                 for (int q = 0; q < 4; ++q) { const float h = xx[q][j][i]; const r_f32x2 hh = {h, h};
; #pragma unroll
;                     for (int e = 0; e < 8; ++e) lg2[q][e] = __builtin_elementwise_fma(hh, wv[e], lg2[q][e]); }
; #pragma unroll
;                 for (int q = 0; q < 4; ++q)
;                     asm volatile("" : "+v"(lg2[q][0]), "+v"(lg2[q][1]), "+v"(lg2[q][2]), "+v"(lg2[q][3]), "+v"(lg2[q][4]), "+v"(lg2[q][5]), "+v"(lg2[q][6]), "+v"(lg2[q][7]));
;                 } }
	v_pk_fma_f32 v[106:107], v[34:35], v[82:83], v[106:107] op_sel:[1,0,0]
	v_pk_fma_f32 v[34:35], v[34:35], v[84:85], v[40:41] op_sel:[1,0,0]
	v_pk_fma_f32 v[40:41], v[46:47], v[68:69], v[48:49] op_sel:[1,0,0]
	v_pk_fma_f32 v[110:111], v[46:47], v[70:71], v[110:111] op_sel:[1,0,0]
	v_pk_fma_f32 v[112:113], v[46:47], v[74:75], v[112:113] op_sel:[1,0,0]
	v_pk_fma_f32 v[114:115], v[46:47], v[76:77], v[114:115] op_sel:[1,0,0]
	v_pk_fma_f32 v[116:117], v[46:47], v[78:79], v[116:117] op_sel:[1,0,0]
	v_pk_fma_f32 v[118:119], v[46:47], v[80:81], v[118:119] op_sel:[1,0,0]
	v_pk_fma_f32 v[120:121], v[46:47], v[82:83], v[120:121] op_sel:[1,0,0]
	v_pk_fma_f32 v[54:55], v[46:47], v[84:85], v[54:55] op_sel:[1,0,0]
	v_pk_fma_f32 v[60:61], v[64:65], v[68:69], v[60:61] op_sel:[1,0,0]
	v_pk_fma_f32 v[122:123], v[64:65], v[70:71], v[122:123] op_sel:[1,0,0]
	v_pk_fma_f32 v[124:125], v[64:65], v[74:75], v[124:125] op_sel:[1,0,0]
	v_pk_fma_f32 v[126:127], v[64:65], v[76:77], v[126:127] op_sel:[1,0,0]
	v_pk_fma_f32 v[128:129], v[64:65], v[78:79], v[128:129] op_sel:[1,0,0]
	v_pk_fma_f32 v[130:131], v[64:65], v[80:81], v[130:131] op_sel:[1,0,0]
	v_pk_fma_f32 v[132:133], v[64:65], v[82:83], v[132:133] op_sel:[1,0,0]
	v_pk_fma_f32 v[64:65], v[64:65], v[84:85], v[134:135] op_sel:[1,0,0]
	v_pk_fma_f32 v[134:135], v[72:73], v[68:69], v[136:137] op_sel:[1,0,0]
	v_pk_fma_f32 v[136:137], v[72:73], v[70:71], v[138:139] op_sel:[1,0,0]
	v_pk_fma_f32 v[138:139], v[72:73], v[74:75], v[140:141] op_sel:[1,0,0]
	v_pk_fma_f32 v[140:141], v[72:73], v[76:77], v[142:143] op_sel:[1,0,0]
	v_pk_fma_f32 v[86:87], v[72:73], v[78:79], v[86:87] op_sel:[1,0,0]
	v_pk_fma_f32 v[80:81], v[72:73], v[80:81], v[88:89] op_sel:[1,0,0]
	v_pk_fma_f32 v[82:83], v[72:73], v[82:83], v[90:91] op_sel:[1,0,0]
	v_pk_fma_f32 v[84:85], v[72:73], v[84:85], v[92:93] op_sel:[1,0,0]
	s_nop 0
	ds_read_b128 v[46:49], v1 offset:17536
	ds_read_b128 v[68:71], v1 offset:17552
	ds_read_b128 v[72:75], v1 offset:17568
	ds_read_b128 v[76:79], v1 offset:17584
	s_waitcnt lgkmcnt(3)
	v_pk_fma_f32 v[88:89], v[28:29], v[46:47], v[108:109] op_sel_hi:[0,1,1]
	v_pk_fma_f32 v[90:91], v[28:29], v[48:49], v[94:95] op_sel_hi:[0,1,1]
	s_waitcnt lgkmcnt(2)
	v_pk_fma_f32 v[92:93], v[28:29], v[68:69], v[98:99] op_sel_hi:[0,1,1]
	v_pk_fma_f32 v[94:95], v[28:29], v[70:71], v[100:101] op_sel_hi:[0,1,1]
	s_waitcnt lgkmcnt(1)
	v_pk_fma_f32 v[98:99], v[28:29], v[72:73], v[102:103] op_sel_hi:[0,1,1]
	v_pk_fma_f32 v[100:101], v[28:29], v[74:75], v[104:105] op_sel_hi:[0,1,1]
	s_waitcnt lgkmcnt(0)
	v_pk_fma_f32 v[102:103], v[28:29], v[76:77], v[106:107] op_sel_hi:[0,1,1]
	v_pk_fma_f32 v[34:35], v[28:29], v[78:79], v[34:35] op_sel_hi:[0,1,1]
	v_pk_fma_f32 v[40:41], v[38:39], v[46:47], v[40:41] op_sel_hi:[0,1,1]
	v_pk_fma_f32 v[104:105], v[38:39], v[48:49], v[110:111] op_sel_hi:[0,1,1]
	v_pk_fma_f32 v[106:107], v[38:39], v[68:69], v[112:113] op_sel_hi:[0,1,1]
	v_pk_fma_f32 v[108:109], v[38:39], v[70:71], v[114:115] op_sel_hi:[0,1,1]
	v_pk_fma_f32 v[110:111], v[38:39], v[72:73], v[116:117] op_sel_hi:[0,1,1]
	v_pk_fma_f32 v[112:113], v[38:39], v[74:75], v[118:119] op_sel_hi:[0,1,1]
	v_pk_fma_f32 v[114:115], v[38:39], v[76:77], v[120:121] op_sel_hi:[0,1,1]
	v_pk_fma_f32 v[54:55], v[38:39], v[78:79], v[54:55] op_sel_hi:[0,1,1]
	v_pk_fma_f32 v[60:61], v[58:59], v[46:47], v[60:61] op_sel_hi:[0,1,1]
	v_pk_fma_f32 v[116:117], v[58:59], v[48:49], v[122:123] op_sel_hi:[0,1,1]
	v_pk_fma_f32 v[118:119], v[58:59], v[68:69], v[124:125] op_sel_hi:[0,1,1]
	v_pk_fma_f32 v[120:121], v[58:59], v[70:71], v[126:127] op_sel_hi:[0,1,1]
	v_pk_fma_f32 v[122:123], v[58:59], v[72:73], v[128:129] op_sel_hi:[0,1,1]
	v_pk_fma_f32 v[124:125], v[58:59], v[74:75], v[130:131] op_sel_hi:[0,1,1]
	v_pk_fma_f32 v[126:127], v[58:59], v[76:77], v[132:133] op_sel_hi:[0,1,1]
	v_pk_fma_f32 v[64:65], v[58:59], v[78:79], v[64:65] op_sel_hi:[0,1,1]
	v_pk_fma_f32 v[128:129], v[66:67], v[46:47], v[134:135] op_sel_hi:[0,1,1]
	v_pk_fma_f32 v[130:131], v[66:67], v[48:49], v[136:137] op_sel_hi:[0,1,1]
	v_pk_fma_f32 v[132:133], v[66:67], v[68:69], v[138:139] op_sel_hi:[0,1,1]
	v_pk_fma_f32 v[134:135], v[66:67], v[70:71], v[140:141] op_sel_hi:[0,1,1]
	v_pk_fma_f32 v[86:87], v[66:67], v[72:73], v[86:87] op_sel_hi:[0,1,1]
	v_pk_fma_f32 v[80:81], v[66:67], v[74:75], v[80:81] op_sel_hi:[0,1,1]
	v_pk_fma_f32 v[82:83], v[66:67], v[76:77], v[82:83] op_sel_hi:[0,1,1]
	v_pk_fma_f32 v[84:85], v[66:67], v[78:79], v[84:85] op_sel_hi:[0,1,1]
	ds_read_b128 v[46:49], v1 offset:17600
	ds_read_b128 v[68:71], v1 offset:17616
	ds_read_b128 v[72:75], v1 offset:17632
	ds_read_b128 v[76:79], v1 offset:17648
	s_waitcnt lgkmcnt(3)
	v_pk_fma_f32 v[88:89], v[28:29], v[46:47], v[88:89] op_sel:[1,0,0]
	v_pk_fma_f32 v[90:91], v[28:29], v[48:49], v[90:91] op_sel:[1,0,0]
	s_waitcnt lgkmcnt(2)
	v_pk_fma_f32 v[92:93], v[28:29], v[68:69], v[92:93] op_sel:[1,0,0]
	v_pk_fma_f32 v[94:95], v[28:29], v[70:71], v[94:95] op_sel:[1,0,0]
	s_waitcnt lgkmcnt(1)
	v_pk_fma_f32 v[98:99], v[28:29], v[72:73], v[98:99] op_sel:[1,0,0]
	v_pk_fma_f32 v[100:101], v[28:29], v[74:75], v[100:101] op_sel:[1,0,0]
	s_waitcnt lgkmcnt(0)
; #define LAS __attribute__((address_space(3)))
; __device__ __forceinline__ void phase_post_mix(Frame& F, int l) {
;     ...
;         for (int j = 0; j < 4; ++j) { const LAS float* wg = rws + (lane + 64 * j) * 68;
; #pragma unroll
;             for (int i = 0; i < 4; ++i) { const f32x4 w0 = *(const LAS f32x4*)(wg + 16 * i), w1 = *(const LAS f32x4*)(wg + 16 * i + 4), w2 = *(const LAS f32x4*)(wg + 16 * i + 8), w3 = *(const LAS f32x4*)(wg + 16 * i + 12);
;                 const r_f32x2 wv[8] = {{w0[0], w0[1]}, {w0[2], w0[3]}, {w1[0], w1[1]}, {w1[2], w1[3]}, {w2[0], w2[1]}, {w2[2], w2[3]}, {w3[0], w3[1]}, {w3[2], w3[3]}};
; #pragma unroll
;                 for (int q = 0; q < 4; ++q) { const float h = xx[q][j][i]; const r_f32x2 hh = {h, h};
; #pragma unroll
;                     for (int e = 0; e < 8; ++e) lg2[q][e] = __builtin_elementwise_fma(hh, wv[e], lg2[q][e]); }
; #pragma unroll
;                 for (int q = 0; q < 4; ++q)
;                     asm volatile("" : "+v"(lg2[q][0]), "+v"(lg2[q][1]), "+v"(lg2[q][2]), "+v"(lg2[q][3]), "+v"(lg2[q][4]), "+v"(lg2[q][5]), "+v"(lg2[q][6]), "+v"(lg2[q][7]));
;                 } }
	v_pk_fma_f32 v[102:103], v[28:29], v[76:77], v[102:103] op_sel:[1,0,0]
	v_pk_fma_f32 v[28:29], v[28:29], v[78:79], v[34:35] op_sel:[1,0,0]
	v_pk_fma_f32 v[34:35], v[38:39], v[46:47], v[40:41] op_sel:[1,0,0]
	v_pk_fma_f32 v[104:105], v[38:39], v[48:49], v[104:105] op_sel:[1,0,0]
	v_pk_fma_f32 v[106:107], v[38:39], v[68:69], v[106:107] op_sel:[1,0,0]
	v_pk_fma_f32 v[108:109], v[38:39], v[70:71], v[108:109] op_sel:[1,0,0]
	v_pk_fma_f32 v[110:111], v[38:39], v[72:73], v[110:111] op_sel:[1,0,0]
	v_pk_fma_f32 v[112:113], v[38:39], v[74:75], v[112:113] op_sel:[1,0,0]
	v_pk_fma_f32 v[114:115], v[38:39], v[76:77], v[114:115] op_sel:[1,0,0]
	v_pk_fma_f32 v[54:55], v[38:39], v[78:79], v[54:55] op_sel:[1,0,0]
	v_pk_fma_f32 v[136:137], v[58:59], v[46:47], v[60:61] op_sel:[1,0,0]
	v_pk_fma_f32 v[116:117], v[58:59], v[48:49], v[116:117] op_sel:[1,0,0]
	v_pk_fma_f32 v[118:119], v[58:59], v[68:69], v[118:119] op_sel:[1,0,0]
	v_pk_fma_f32 v[120:121], v[58:59], v[70:71], v[120:121] op_sel:[1,0,0]
	v_pk_fma_f32 v[122:123], v[58:59], v[72:73], v[122:123] op_sel:[1,0,0]
	v_pk_fma_f32 v[124:125], v[58:59], v[74:75], v[124:125] op_sel:[1,0,0]
	v_pk_fma_f32 v[126:127], v[58:59], v[76:77], v[126:127] op_sel:[1,0,0]
	v_pk_fma_f32 v[138:139], v[58:59], v[78:79], v[64:65] op_sel:[1,0,0]
	v_pk_fma_f32 v[128:129], v[66:67], v[46:47], v[128:129] op_sel:[1,0,0]
	v_pk_fma_f32 v[130:131], v[66:67], v[48:49], v[130:131] op_sel:[1,0,0]
	v_pk_fma_f32 v[68:69], v[66:67], v[68:69], v[132:133] op_sel:[1,0,0]
	v_pk_fma_f32 v[70:71], v[66:67], v[70:71], v[134:135] op_sel:[1,0,0]
	v_pk_fma_f32 v[72:73], v[66:67], v[72:73], v[86:87] op_sel:[1,0,0]
	v_pk_fma_f32 v[74:75], v[66:67], v[74:75], v[80:81] op_sel:[1,0,0]
	v_pk_fma_f32 v[76:77], v[66:67], v[76:77], v[82:83] op_sel:[1,0,0]
	v_pk_fma_f32 v[78:79], v[66:67], v[78:79], v[84:85] op_sel:[1,0,0]
	s_nop 0
	ds_read_b128 v[38:41], v1 offset:34816
	ds_read_b128 v[46:49], v1 offset:34832
	ds_read_b128 v[58:61], v1 offset:34848
	ds_read_b128 v[64:67], v1 offset:34864
	s_waitcnt lgkmcnt(3)
	v_pk_fma_f32 v[80:81], v[24:25], v[38:39], v[88:89] op_sel_hi:[0,1,1]
	v_pk_fma_f32 v[82:83], v[24:25], v[40:41], v[90:91] op_sel_hi:[0,1,1]
	s_waitcnt lgkmcnt(2)
	v_pk_fma_f32 v[84:85], v[24:25], v[46:47], v[92:93] op_sel_hi:[0,1,1]
	v_pk_fma_f32 v[86:87], v[24:25], v[48:49], v[94:95] op_sel_hi:[0,1,1]
	s_waitcnt lgkmcnt(1)
	v_pk_fma_f32 v[88:89], v[24:25], v[58:59], v[98:99] op_sel_hi:[0,1,1]
	v_pk_fma_f32 v[90:91], v[24:25], v[60:61], v[100:101] op_sel_hi:[0,1,1]
	s_waitcnt lgkmcnt(0)
	v_pk_fma_f32 v[92:93], v[24:25], v[64:65], v[102:103] op_sel_hi:[0,1,1]
	v_pk_fma_f32 v[28:29], v[24:25], v[66:67], v[28:29] op_sel_hi:[0,1,1]
	v_pk_fma_f32 v[34:35], v[32:33], v[38:39], v[34:35] op_sel_hi:[0,1,1]
	v_pk_fma_f32 v[94:95], v[32:33], v[40:41], v[104:105] op_sel_hi:[0,1,1]
	v_pk_fma_f32 v[98:99], v[32:33], v[46:47], v[106:107] op_sel_hi:[0,1,1]
	v_pk_fma_f32 v[100:101], v[32:33], v[48:49], v[108:109] op_sel_hi:[0,1,1]
	v_pk_fma_f32 v[102:103], v[32:33], v[58:59], v[110:111] op_sel_hi:[0,1,1]
	v_pk_fma_f32 v[104:105], v[32:33], v[60:61], v[112:113] op_sel_hi:[0,1,1]
	v_pk_fma_f32 v[106:107], v[32:33], v[64:65], v[114:115] op_sel_hi:[0,1,1]
	v_pk_fma_f32 v[54:55], v[32:33], v[66:67], v[54:55] op_sel_hi:[0,1,1]
	v_pk_fma_f32 v[108:109], v[52:53], v[38:39], v[136:137] op_sel_hi:[0,1,1]
	v_pk_fma_f32 v[110:111], v[52:53], v[40:41], v[116:117] op_sel_hi:[0,1,1]
	v_pk_fma_f32 v[112:113], v[52:53], v[46:47], v[118:119] op_sel_hi:[0,1,1]
	v_pk_fma_f32 v[114:115], v[52:53], v[48:49], v[120:121] op_sel_hi:[0,1,1]
	v_pk_fma_f32 v[116:117], v[52:53], v[58:59], v[122:123] op_sel_hi:[0,1,1]
	v_pk_fma_f32 v[118:119], v[52:53], v[60:61], v[124:125] op_sel_hi:[0,1,1]
	v_pk_fma_f32 v[120:121], v[52:53], v[64:65], v[126:127] op_sel_hi:[0,1,1]
	v_pk_fma_f32 v[122:123], v[52:53], v[66:67], v[138:139] op_sel_hi:[0,1,1]
	v_pk_fma_f32 v[124:125], v[62:63], v[38:39], v[128:129] op_sel_hi:[0,1,1]
	v_pk_fma_f32 v[126:127], v[62:63], v[40:41], v[130:131] op_sel_hi:[0,1,1]
	v_pk_fma_f32 v[68:69], v[62:63], v[46:47], v[68:69] op_sel_hi:[0,1,1]
	v_pk_fma_f32 v[70:71], v[62:63], v[48:49], v[70:71] op_sel_hi:[0,1,1]
	v_pk_fma_f32 v[72:73], v[62:63], v[58:59], v[72:73] op_sel_hi:[0,1,1]
	v_pk_fma_f32 v[74:75], v[62:63], v[60:61], v[74:75] op_sel_hi:[0,1,1]
	v_pk_fma_f32 v[76:77], v[62:63], v[64:65], v[76:77] op_sel_hi:[0,1,1]
	v_pk_fma_f32 v[78:79], v[62:63], v[66:67], v[78:79] op_sel_hi:[0,1,1]
	ds_read_b128 v[38:41], v1 offset:34880
	ds_read_b128 v[46:49], v1 offset:34896
	ds_read_b128 v[58:61], v1 offset:34912
	ds_read_b128 v[64:67], v1 offset:34928
	s_waitcnt lgkmcnt(3)
	v_pk_fma_f32 v[80:81], v[24:25], v[38:39], v[80:81] op_sel:[1,0,0]
	v_pk_fma_f32 v[82:83], v[24:25], v[40:41], v[82:83] op_sel:[1,0,0]
	s_waitcnt lgkmcnt(2)
	v_pk_fma_f32 v[84:85], v[24:25], v[46:47], v[84:85] op_sel:[1,0,0]
	v_pk_fma_f32 v[86:87], v[24:25], v[48:49], v[86:87] op_sel:[1,0,0]
	s_waitcnt lgkmcnt(1)
	v_pk_fma_f32 v[88:89], v[24:25], v[58:59], v[88:89] op_sel:[1,0,0]
	v_pk_fma_f32 v[90:91], v[24:25], v[60:61], v[90:91] op_sel:[1,0,0]
	s_waitcnt lgkmcnt(0)
; #define LAS __attribute__((address_space(3)))
; __device__ __forceinline__ void phase_post_mix(Frame& F, int l) {
;     ...
;         for (int j = 0; j < 4; ++j) { const LAS float* wg = rws + (lane + 64 * j) * 68;
; #pragma unroll
;             for (int i = 0; i < 4; ++i) { const f32x4 w0 = *(const LAS f32x4*)(wg + 16 * i), w1 = *(const LAS f32x4*)(wg + 16 * i + 4), w2 = *(const LAS f32x4*)(wg + 16 * i + 8), w3 = *(const LAS f32x4*)(wg + 16 * i + 12);
;                 const r_f32x2 wv[8] = {{w0[0], w0[1]}, {w0[2], w0[3]}, {w1[0], w1[1]}, {w1[2], w1[3]}, {w2[0], w2[1]}, {w2[2], w2[3]}, {w3[0], w3[1]}, {w3[2], w3[3]}};
; #pragma unroll
;                 for (int q = 0; q < 4; ++q) { const float h = xx[q][j][i]; const r_f32x2 hh = {h, h};
; #pragma unroll
;                     for (int e = 0; e < 8; ++e) lg2[q][e] = __builtin_elementwise_fma(hh, wv[e], lg2[q][e]); }
; #pragma unroll
;                 for (int q = 0; q < 4; ++q)
;                     asm volatile("" : "+v"(lg2[q][0]), "+v"(lg2[q][1]), "+v"(lg2[q][2]), "+v"(lg2[q][3]), "+v"(lg2[q][4]), "+v"(lg2[q][5]), "+v"(lg2[q][6]), "+v"(lg2[q][7]));
;                 } }
	v_pk_fma_f32 v[92:93], v[24:25], v[64:65], v[92:93] op_sel:[1,0,0]
	v_pk_fma_f32 v[24:25], v[24:25], v[66:67], v[28:29] op_sel:[1,0,0]
	v_pk_fma_f32 v[28:29], v[32:33], v[38:39], v[34:35] op_sel:[1,0,0]
	v_pk_fma_f32 v[94:95], v[32:33], v[40:41], v[94:95] op_sel:[1,0,0]
	v_pk_fma_f32 v[98:99], v[32:33], v[46:47], v[98:99] op_sel:[1,0,0]
	v_pk_fma_f32 v[100:101], v[32:33], v[48:49], v[100:101] op_sel:[1,0,0]
	v_pk_fma_f32 v[102:103], v[32:33], v[58:59], v[102:103] op_sel:[1,0,0]
	v_pk_fma_f32 v[104:105], v[32:33], v[60:61], v[104:105] op_sel:[1,0,0]
	v_pk_fma_f32 v[106:107], v[32:33], v[64:65], v[106:107] op_sel:[1,0,0]
	v_pk_fma_f32 v[128:129], v[32:33], v[66:67], v[54:55] op_sel:[1,0,0]
	v_pk_fma_f32 v[108:109], v[52:53], v[38:39], v[108:109] op_sel:[1,0,0]
	v_pk_fma_f32 v[110:111], v[52:53], v[40:41], v[110:111] op_sel:[1,0,0]
	v_pk_fma_f32 v[112:113], v[52:53], v[46:47], v[112:113] op_sel:[1,0,0]
	v_pk_fma_f32 v[114:115], v[52:53], v[48:49], v[114:115] op_sel:[1,0,0]
	v_pk_fma_f32 v[116:117], v[52:53], v[58:59], v[116:117] op_sel:[1,0,0]
	v_pk_fma_f32 v[118:119], v[52:53], v[60:61], v[118:119] op_sel:[1,0,0]
	v_pk_fma_f32 v[120:121], v[52:53], v[64:65], v[120:121] op_sel:[1,0,0]
	v_pk_fma_f32 v[122:123], v[52:53], v[66:67], v[122:123] op_sel:[1,0,0]
	v_pk_fma_f32 v[124:125], v[62:63], v[38:39], v[124:125] op_sel:[1,0,0]
	v_pk_fma_f32 v[126:127], v[62:63], v[40:41], v[126:127] op_sel:[1,0,0]
	v_pk_fma_f32 v[68:69], v[62:63], v[46:47], v[68:69] op_sel:[1,0,0]
	v_pk_fma_f32 v[70:71], v[62:63], v[48:49], v[70:71] op_sel:[1,0,0]
	v_pk_fma_f32 v[58:59], v[62:63], v[58:59], v[72:73] op_sel:[1,0,0]
	v_pk_fma_f32 v[60:61], v[62:63], v[60:61], v[74:75] op_sel:[1,0,0]
	v_pk_fma_f32 v[64:65], v[62:63], v[64:65], v[76:77] op_sel:[1,0,0]
	v_pk_fma_f32 v[62:63], v[62:63], v[66:67], v[78:79] op_sel:[1,0,0]
	s_nop 0
	ds_read_b128 v[32:35], v1 offset:34944
	ds_read_b128 v[38:41], v1 offset:34960
	ds_read_b128 v[46:49], v1 offset:34976
	ds_read_b128 v[52:55], v1 offset:34992
	s_waitcnt lgkmcnt(3)
	v_pk_fma_f32 v[66:67], v[20:21], v[32:33], v[80:81] op_sel_hi:[0,1,1]
	v_pk_fma_f32 v[72:73], v[20:21], v[34:35], v[82:83] op_sel_hi:[0,1,1]
	s_waitcnt lgkmcnt(2)
	v_pk_fma_f32 v[74:75], v[20:21], v[38:39], v[84:85] op_sel_hi:[0,1,1]
	v_pk_fma_f32 v[76:77], v[20:21], v[40:41], v[86:87] op_sel_hi:[0,1,1]
	s_waitcnt lgkmcnt(1)
	v_pk_fma_f32 v[78:79], v[20:21], v[46:47], v[88:89] op_sel_hi:[0,1,1]
	v_pk_fma_f32 v[80:81], v[20:21], v[48:49], v[90:91] op_sel_hi:[0,1,1]
	s_waitcnt lgkmcnt(0)
	v_pk_fma_f32 v[82:83], v[20:21], v[52:53], v[92:93] op_sel_hi:[0,1,1]
	v_pk_fma_f32 v[24:25], v[20:21], v[54:55], v[24:25] op_sel_hi:[0,1,1]
	v_pk_fma_f32 v[28:29], v[26:27], v[32:33], v[28:29] op_sel_hi:[0,1,1]
	v_pk_fma_f32 v[84:85], v[26:27], v[34:35], v[94:95] op_sel_hi:[0,1,1]
	v_pk_fma_f32 v[86:87], v[26:27], v[38:39], v[98:99] op_sel_hi:[0,1,1]
	v_pk_fma_f32 v[88:89], v[26:27], v[40:41], v[100:101] op_sel_hi:[0,1,1]
	v_pk_fma_f32 v[90:91], v[26:27], v[46:47], v[102:103] op_sel_hi:[0,1,1]
	v_pk_fma_f32 v[92:93], v[26:27], v[48:49], v[104:105] op_sel_hi:[0,1,1]
	v_pk_fma_f32 v[94:95], v[26:27], v[52:53], v[106:107] op_sel_hi:[0,1,1]
	v_pk_fma_f32 v[98:99], v[26:27], v[54:55], v[128:129] op_sel_hi:[0,1,1]
	v_pk_fma_f32 v[100:101], v[44:45], v[32:33], v[108:109] op_sel_hi:[0,1,1]
	v_pk_fma_f32 v[102:103], v[44:45], v[34:35], v[110:111] op_sel_hi:[0,1,1]
	v_pk_fma_f32 v[104:105], v[44:45], v[38:39], v[112:113] op_sel_hi:[0,1,1]
	v_pk_fma_f32 v[106:107], v[44:45], v[40:41], v[114:115] op_sel_hi:[0,1,1]
	v_pk_fma_f32 v[108:109], v[44:45], v[46:47], v[116:117] op_sel_hi:[0,1,1]
	v_pk_fma_f32 v[110:111], v[44:45], v[48:49], v[118:119] op_sel_hi:[0,1,1]
	v_pk_fma_f32 v[112:113], v[44:45], v[52:53], v[120:121] op_sel_hi:[0,1,1]
	v_pk_fma_f32 v[114:115], v[44:45], v[54:55], v[122:123] op_sel_hi:[0,1,1]
	v_pk_fma_f32 v[116:117], v[56:57], v[32:33], v[124:125] op_sel_hi:[0,1,1]
	v_pk_fma_f32 v[118:119], v[56:57], v[34:35], v[126:127] op_sel_hi:[0,1,1]
	v_pk_fma_f32 v[68:69], v[56:57], v[38:39], v[68:69] op_sel_hi:[0,1,1]
	v_pk_fma_f32 v[70:71], v[56:57], v[40:41], v[70:71] op_sel_hi:[0,1,1]
	v_pk_fma_f32 v[58:59], v[56:57], v[46:47], v[58:59] op_sel_hi:[0,1,1]
	v_pk_fma_f32 v[60:61], v[56:57], v[48:49], v[60:61] op_sel_hi:[0,1,1]
	v_pk_fma_f32 v[64:65], v[56:57], v[52:53], v[64:65] op_sel_hi:[0,1,1]
	v_pk_fma_f32 v[62:63], v[56:57], v[54:55], v[62:63] op_sel_hi:[0,1,1]
	ds_read_b128 v[32:35], v1 offset:35008
	ds_read_b128 v[38:41], v1 offset:35024
	ds_read_b128 v[46:49], v1 offset:35040
	ds_read_b128 v[52:55], v1 offset:35056
	s_waitcnt lgkmcnt(3)
	v_pk_fma_f32 v[66:67], v[20:21], v[32:33], v[66:67] op_sel:[1,0,0]
	v_pk_fma_f32 v[72:73], v[20:21], v[34:35], v[72:73] op_sel:[1,0,0]
	s_waitcnt lgkmcnt(2)
	v_pk_fma_f32 v[74:75], v[20:21], v[38:39], v[74:75] op_sel:[1,0,0]
	v_pk_fma_f32 v[76:77], v[20:21], v[40:41], v[76:77] op_sel:[1,0,0]
	s_waitcnt lgkmcnt(1)
	v_pk_fma_f32 v[78:79], v[20:21], v[46:47], v[78:79] op_sel:[1,0,0]
	v_pk_fma_f32 v[80:81], v[20:21], v[48:49], v[80:81] op_sel:[1,0,0]
	s_waitcnt lgkmcnt(0)
; #define LAS __attribute__((address_space(3)))
; __device__ __forceinline__ void phase_post_mix(Frame& F, int l) {
;     ...
;         for (int j = 0; j < 4; ++j) { const LAS float* wg = rws + (lane + 64 * j) * 68;
; #pragma unroll
;             for (int i = 0; i < 4; ++i) { const f32x4 w0 = *(const LAS f32x4*)(wg + 16 * i), w1 = *(const LAS f32x4*)(wg + 16 * i + 4), w2 = *(const LAS f32x4*)(wg + 16 * i + 8), w3 = *(const LAS f32x4*)(wg + 16 * i + 12);
;                 const r_f32x2 wv[8] = {{w0[0], w0[1]}, {w0[2], w0[3]}, {w1[0], w1[1]}, {w1[2], w1[3]}, {w2[0], w2[1]}, {w2[2], w2[3]}, {w3[0], w3[1]}, {w3[2], w3[3]}};
; #pragma unroll
;                 for (int q = 0; q < 4; ++q) { const float h = xx[q][j][i]; const r_f32x2 hh = {h, h};
; #pragma unroll
;                     for (int e = 0; e < 8; ++e) lg2[q][e] = __builtin_elementwise_fma(hh, wv[e], lg2[q][e]); }
; #pragma unroll
;                 for (int q = 0; q < 4; ++q)
;                     asm volatile("" : "+v"(lg2[q][0]), "+v"(lg2[q][1]), "+v"(lg2[q][2]), "+v"(lg2[q][3]), "+v"(lg2[q][4]), "+v"(lg2[q][5]), "+v"(lg2[q][6]), "+v"(lg2[q][7]));
;                 } }
	v_pk_fma_f32 v[82:83], v[20:21], v[52:53], v[82:83] op_sel:[1,0,0]
	v_pk_fma_f32 v[20:21], v[20:21], v[54:55], v[24:25] op_sel:[1,0,0]
	v_pk_fma_f32 v[28:29], v[26:27], v[32:33], v[28:29] op_sel:[1,0,0]
	v_pk_fma_f32 v[84:85], v[26:27], v[34:35], v[84:85] op_sel:[1,0,0]
	v_pk_fma_f32 v[86:87], v[26:27], v[38:39], v[86:87] op_sel:[1,0,0]
	v_pk_fma_f32 v[88:89], v[26:27], v[40:41], v[88:89] op_sel:[1,0,0]
	v_pk_fma_f32 v[90:91], v[26:27], v[46:47], v[90:91] op_sel:[1,0,0]
	v_pk_fma_f32 v[92:93], v[26:27], v[48:49], v[92:93] op_sel:[1,0,0]
	v_pk_fma_f32 v[94:95], v[26:27], v[52:53], v[94:95] op_sel:[1,0,0]
	v_pk_fma_f32 v[98:99], v[26:27], v[54:55], v[98:99] op_sel:[1,0,0]
	v_pk_fma_f32 v[100:101], v[44:45], v[32:33], v[100:101] op_sel:[1,0,0]
	v_pk_fma_f32 v[102:103], v[44:45], v[34:35], v[102:103] op_sel:[1,0,0]
	v_pk_fma_f32 v[104:105], v[44:45], v[38:39], v[104:105] op_sel:[1,0,0]
	v_pk_fma_f32 v[106:107], v[44:45], v[40:41], v[106:107] op_sel:[1,0,0]
	v_pk_fma_f32 v[108:109], v[44:45], v[46:47], v[108:109] op_sel:[1,0,0]
	v_pk_fma_f32 v[110:111], v[44:45], v[48:49], v[110:111] op_sel:[1,0,0]
	v_pk_fma_f32 v[112:113], v[44:45], v[52:53], v[112:113] op_sel:[1,0,0]
	v_pk_fma_f32 v[114:115], v[44:45], v[54:55], v[114:115] op_sel:[1,0,0]
	v_pk_fma_f32 v[116:117], v[56:57], v[32:33], v[116:117] op_sel:[1,0,0]
	v_pk_fma_f32 v[118:119], v[56:57], v[34:35], v[118:119] op_sel:[1,0,0]
	v_pk_fma_f32 v[68:69], v[56:57], v[38:39], v[68:69] op_sel:[1,0,0]
	v_pk_fma_f32 v[70:71], v[56:57], v[40:41], v[70:71] op_sel:[1,0,0]
	v_pk_fma_f32 v[58:59], v[56:57], v[46:47], v[58:59] op_sel:[1,0,0]
	v_pk_fma_f32 v[48:49], v[56:57], v[48:49], v[60:61] op_sel:[1,0,0]
	v_pk_fma_f32 v[52:53], v[56:57], v[52:53], v[64:65] op_sel:[1,0,0]
	v_pk_fma_f32 v[54:55], v[56:57], v[54:55], v[62:63] op_sel:[1,0,0]
	s_nop 0
	ds_read_b128 v[24:27], v1 offset:52224
	ds_read_b128 v[32:35], v1 offset:52240
	ds_read_b128 v[38:41], v1 offset:52256
	ds_read_b128 v[44:47], v1 offset:52272
	s_waitcnt lgkmcnt(3)
	v_pk_fma_f32 v[56:57], v[16:17], v[24:25], v[66:67] op_sel_hi:[0,1,1]
	v_pk_fma_f32 v[60:61], v[16:17], v[26:27], v[72:73] op_sel_hi:[0,1,1]
	s_waitcnt lgkmcnt(2)
	v_pk_fma_f32 v[62:63], v[16:17], v[32:33], v[74:75] op_sel_hi:[0,1,1]
	v_pk_fma_f32 v[64:65], v[16:17], v[34:35], v[76:77] op_sel_hi:[0,1,1]
	s_waitcnt lgkmcnt(1)
	v_pk_fma_f32 v[66:67], v[16:17], v[38:39], v[78:79] op_sel_hi:[0,1,1]
	v_pk_fma_f32 v[72:73], v[16:17], v[40:41], v[80:81] op_sel_hi:[0,1,1]
	s_waitcnt lgkmcnt(0)
	v_pk_fma_f32 v[74:75], v[16:17], v[44:45], v[82:83] op_sel_hi:[0,1,1]
	v_pk_fma_f32 v[20:21], v[16:17], v[46:47], v[20:21] op_sel_hi:[0,1,1]
	v_pk_fma_f32 v[28:29], v[22:23], v[24:25], v[28:29] op_sel_hi:[0,1,1]
	v_pk_fma_f32 v[76:77], v[22:23], v[26:27], v[84:85] op_sel_hi:[0,1,1]
	v_pk_fma_f32 v[78:79], v[22:23], v[32:33], v[86:87] op_sel_hi:[0,1,1]
	v_pk_fma_f32 v[80:81], v[22:23], v[34:35], v[88:89] op_sel_hi:[0,1,1]
	v_pk_fma_f32 v[82:83], v[22:23], v[38:39], v[90:91] op_sel_hi:[0,1,1]
	v_pk_fma_f32 v[84:85], v[22:23], v[40:41], v[92:93] op_sel_hi:[0,1,1]
	v_pk_fma_f32 v[86:87], v[22:23], v[44:45], v[94:95] op_sel_hi:[0,1,1]
	v_pk_fma_f32 v[88:89], v[22:23], v[46:47], v[98:99] op_sel_hi:[0,1,1]
	v_pk_fma_f32 v[90:91], v[36:37], v[24:25], v[100:101] op_sel_hi:[0,1,1]
	v_pk_fma_f32 v[92:93], v[36:37], v[26:27], v[102:103] op_sel_hi:[0,1,1]
	v_pk_fma_f32 v[94:95], v[36:37], v[32:33], v[104:105] op_sel_hi:[0,1,1]
	v_pk_fma_f32 v[98:99], v[36:37], v[34:35], v[106:107] op_sel_hi:[0,1,1]
	v_pk_fma_f32 v[100:101], v[36:37], v[38:39], v[108:109] op_sel_hi:[0,1,1]
	v_pk_fma_f32 v[102:103], v[36:37], v[40:41], v[110:111] op_sel_hi:[0,1,1]
	v_pk_fma_f32 v[104:105], v[36:37], v[44:45], v[112:113] op_sel_hi:[0,1,1]
	v_pk_fma_f32 v[106:107], v[36:37], v[46:47], v[114:115] op_sel_hi:[0,1,1]
	v_pk_fma_f32 v[108:109], v[50:51], v[24:25], v[116:117] op_sel_hi:[0,1,1]
	v_pk_fma_f32 v[110:111], v[50:51], v[26:27], v[118:119] op_sel_hi:[0,1,1]
	v_pk_fma_f32 v[68:69], v[50:51], v[32:33], v[68:69] op_sel_hi:[0,1,1]
	v_pk_fma_f32 v[70:71], v[50:51], v[34:35], v[70:71] op_sel_hi:[0,1,1]
	v_pk_fma_f32 v[58:59], v[50:51], v[38:39], v[58:59] op_sel_hi:[0,1,1]
	v_pk_fma_f32 v[48:49], v[50:51], v[40:41], v[48:49] op_sel_hi:[0,1,1]
	v_pk_fma_f32 v[52:53], v[50:51], v[44:45], v[52:53] op_sel_hi:[0,1,1]
	v_pk_fma_f32 v[54:55], v[50:51], v[46:47], v[54:55] op_sel_hi:[0,1,1]
	ds_read_b128 v[24:27], v1 offset:52288
	ds_read_b128 v[32:35], v1 offset:52304
	ds_read_b128 v[38:41], v1 offset:52320
	ds_read_b128 v[44:47], v1 offset:52336
	s_waitcnt lgkmcnt(3)
	v_pk_fma_f32 v[56:57], v[16:17], v[24:25], v[56:57] op_sel:[1,0,0]
	v_pk_fma_f32 v[60:61], v[16:17], v[26:27], v[60:61] op_sel:[1,0,0]
	s_waitcnt lgkmcnt(2)
	v_pk_fma_f32 v[62:63], v[16:17], v[32:33], v[62:63] op_sel:[1,0,0]
	v_pk_fma_f32 v[64:65], v[16:17], v[34:35], v[64:65] op_sel:[1,0,0]
	s_waitcnt lgkmcnt(1)
	v_pk_fma_f32 v[66:67], v[16:17], v[38:39], v[66:67] op_sel:[1,0,0]
	v_pk_fma_f32 v[72:73], v[16:17], v[40:41], v[72:73] op_sel:[1,0,0]
	s_waitcnt lgkmcnt(0)
; #define LAS __attribute__((address_space(3)))
; __device__ __forceinline__ void phase_post_mix(Frame& F, int l) {
;     ...
;         for (int j = 0; j < 4; ++j) { const LAS float* wg = rws + (lane + 64 * j) * 68;
; #pragma unroll
;             for (int i = 0; i < 4; ++i) { const f32x4 w0 = *(const LAS f32x4*)(wg + 16 * i), w1 = *(const LAS f32x4*)(wg + 16 * i + 4), w2 = *(const LAS f32x4*)(wg + 16 * i + 8), w3 = *(const LAS f32x4*)(wg + 16 * i + 12);
;                 const r_f32x2 wv[8] = {{w0[0], w0[1]}, {w0[2], w0[3]}, {w1[0], w1[1]}, {w1[2], w1[3]}, {w2[0], w2[1]}, {w2[2], w2[3]}, {w3[0], w3[1]}, {w3[2], w3[3]}};
; #pragma unroll
;                 for (int q = 0; q < 4; ++q) { const float h = xx[q][j][i]; const r_f32x2 hh = {h, h};
; #pragma unroll
;                     for (int e = 0; e < 8; ++e) lg2[q][e] = __builtin_elementwise_fma(hh, wv[e], lg2[q][e]); }
; #pragma unroll
;                 for (int q = 0; q < 4; ++q)
;                     asm volatile("" : "+v"(lg2[q][0]), "+v"(lg2[q][1]), "+v"(lg2[q][2]), "+v"(lg2[q][3]), "+v"(lg2[q][4]), "+v"(lg2[q][5]), "+v"(lg2[q][6]), "+v"(lg2[q][7]));
;                 } }
	v_pk_fma_f32 v[74:75], v[16:17], v[44:45], v[74:75] op_sel:[1,0,0]
	v_pk_fma_f32 v[16:17], v[16:17], v[46:47], v[20:21] op_sel:[1,0,0]
	v_pk_fma_f32 v[28:29], v[22:23], v[24:25], v[28:29] op_sel:[1,0,0]
	v_pk_fma_f32 v[76:77], v[22:23], v[26:27], v[76:77] op_sel:[1,0,0]
	v_pk_fma_f32 v[78:79], v[22:23], v[32:33], v[78:79] op_sel:[1,0,0]
	v_pk_fma_f32 v[80:81], v[22:23], v[34:35], v[80:81] op_sel:[1,0,0]
	v_pk_fma_f32 v[82:83], v[22:23], v[38:39], v[82:83] op_sel:[1,0,0]
	v_pk_fma_f32 v[84:85], v[22:23], v[40:41], v[84:85] op_sel:[1,0,0]
	v_pk_fma_f32 v[86:87], v[22:23], v[44:45], v[86:87] op_sel:[1,0,0]
	v_pk_fma_f32 v[88:89], v[22:23], v[46:47], v[88:89] op_sel:[1,0,0]
	v_pk_fma_f32 v[90:91], v[36:37], v[24:25], v[90:91] op_sel:[1,0,0]
	v_pk_fma_f32 v[92:93], v[36:37], v[26:27], v[92:93] op_sel:[1,0,0]
	v_pk_fma_f32 v[94:95], v[36:37], v[32:33], v[94:95] op_sel:[1,0,0]
	v_pk_fma_f32 v[98:99], v[36:37], v[34:35], v[98:99] op_sel:[1,0,0]
	v_pk_fma_f32 v[100:101], v[36:37], v[38:39], v[100:101] op_sel:[1,0,0]
	v_pk_fma_f32 v[102:103], v[36:37], v[40:41], v[102:103] op_sel:[1,0,0]
	v_pk_fma_f32 v[104:105], v[36:37], v[44:45], v[104:105] op_sel:[1,0,0]
	v_pk_fma_f32 v[106:107], v[36:37], v[46:47], v[106:107] op_sel:[1,0,0]
	v_pk_fma_f32 v[108:109], v[50:51], v[24:25], v[108:109] op_sel:[1,0,0]
	v_pk_fma_f32 v[110:111], v[50:51], v[26:27], v[110:111] op_sel:[1,0,0]
	v_pk_fma_f32 v[68:69], v[50:51], v[32:33], v[68:69] op_sel:[1,0,0]
	v_pk_fma_f32 v[70:71], v[50:51], v[34:35], v[70:71] op_sel:[1,0,0]
	v_pk_fma_f32 v[58:59], v[50:51], v[38:39], v[58:59] op_sel:[1,0,0]
	v_pk_fma_f32 v[40:41], v[50:51], v[40:41], v[48:49] op_sel:[1,0,0]
	v_pk_fma_f32 v[44:45], v[50:51], v[44:45], v[52:53] op_sel:[1,0,0]
	v_pk_fma_f32 v[46:47], v[50:51], v[46:47], v[54:55] op_sel:[1,0,0]
	s_nop 0
	ds_read_b128 v[20:23], v1 offset:52352
	ds_read_b128 v[24:27], v1 offset:52368
	ds_read_b128 v[32:35], v1 offset:52384
	ds_read_b128 v[36:39], v1 offset:52400
	s_waitcnt lgkmcnt(3)
	v_pk_fma_f32 v[48:49], v[14:15], v[20:21], v[56:57] op_sel_hi:[0,1,1]
	v_pk_fma_f32 v[50:51], v[14:15], v[22:23], v[60:61] op_sel_hi:[0,1,1]
	s_waitcnt lgkmcnt(2)
	v_pk_fma_f32 v[52:53], v[14:15], v[24:25], v[62:63] op_sel_hi:[0,1,1]
	v_pk_fma_f32 v[54:55], v[14:15], v[26:27], v[64:65] op_sel_hi:[0,1,1]
	s_waitcnt lgkmcnt(1)
	v_pk_fma_f32 v[56:57], v[14:15], v[32:33], v[66:67] op_sel_hi:[0,1,1]
	v_pk_fma_f32 v[60:61], v[14:15], v[34:35], v[72:73] op_sel_hi:[0,1,1]
	s_waitcnt lgkmcnt(0)
	v_pk_fma_f32 v[62:63], v[14:15], v[36:37], v[74:75] op_sel_hi:[0,1,1]
	v_pk_fma_f32 v[16:17], v[14:15], v[38:39], v[16:17] op_sel_hi:[0,1,1]
	v_pk_fma_f32 v[28:29], v[18:19], v[20:21], v[28:29] op_sel_hi:[0,1,1]
	v_pk_fma_f32 v[76:77], v[18:19], v[22:23], v[76:77] op_sel_hi:[0,1,1]
	v_pk_fma_f32 v[78:79], v[18:19], v[24:25], v[78:79] op_sel_hi:[0,1,1]
	v_pk_fma_f32 v[80:81], v[18:19], v[26:27], v[80:81] op_sel_hi:[0,1,1]
	v_pk_fma_f32 v[82:83], v[18:19], v[32:33], v[82:83] op_sel_hi:[0,1,1]
	v_pk_fma_f32 v[84:85], v[18:19], v[34:35], v[84:85] op_sel_hi:[0,1,1]
	v_pk_fma_f32 v[86:87], v[18:19], v[36:37], v[86:87] op_sel_hi:[0,1,1]
	v_pk_fma_f32 v[88:89], v[18:19], v[38:39], v[88:89] op_sel_hi:[0,1,1]
	v_pk_fma_f32 v[90:91], v[30:31], v[20:21], v[90:91] op_sel_hi:[0,1,1]
	v_pk_fma_f32 v[92:93], v[30:31], v[22:23], v[92:93] op_sel_hi:[0,1,1]
	v_pk_fma_f32 v[94:95], v[30:31], v[24:25], v[94:95] op_sel_hi:[0,1,1]
	v_pk_fma_f32 v[98:99], v[30:31], v[26:27], v[98:99] op_sel_hi:[0,1,1]
	v_pk_fma_f32 v[100:101], v[30:31], v[32:33], v[100:101] op_sel_hi:[0,1,1]
	v_pk_fma_f32 v[102:103], v[30:31], v[34:35], v[102:103] op_sel_hi:[0,1,1]
	v_pk_fma_f32 v[104:105], v[30:31], v[36:37], v[104:105] op_sel_hi:[0,1,1]
	v_pk_fma_f32 v[106:107], v[30:31], v[38:39], v[106:107] op_sel_hi:[0,1,1]
	v_pk_fma_f32 v[108:109], v[42:43], v[20:21], v[108:109] op_sel_hi:[0,1,1]
	v_pk_fma_f32 v[110:111], v[42:43], v[22:23], v[110:111] op_sel_hi:[0,1,1]
	v_pk_fma_f32 v[24:25], v[42:43], v[24:25], v[68:69] op_sel_hi:[0,1,1]
	v_pk_fma_f32 v[112:113], v[42:43], v[26:27], v[70:71] op_sel_hi:[0,1,1]
	v_pk_fma_f32 v[114:115], v[42:43], v[32:33], v[58:59] op_sel_hi:[0,1,1]
	v_pk_fma_f32 v[116:117], v[42:43], v[34:35], v[40:41] op_sel_hi:[0,1,1]
	v_pk_fma_f32 v[118:119], v[42:43], v[36:37], v[44:45] op_sel_hi:[0,1,1]
	v_pk_fma_f32 v[120:121], v[42:43], v[38:39], v[46:47] op_sel_hi:[0,1,1]
	ds_read_b128 v[20:23], v1 offset:52416
	ds_read_b128 v[64:67], v1 offset:52432
	ds_read_b128 v[68:71], v1 offset:52448
	ds_read_b128 v[72:75], v1 offset:52464
	s_waitcnt lgkmcnt(3)
	v_pk_fma_f32 v[122:123], v[14:15], v[20:21], v[48:49] op_sel:[1,0,0]
	v_pk_fma_f32 v[124:125], v[14:15], v[22:23], v[50:51] op_sel:[1,0,0]
	s_waitcnt lgkmcnt(2)
	v_pk_fma_f32 v[126:127], v[14:15], v[64:65], v[52:53] op_sel:[1,0,0]
	v_pk_fma_f32 v[128:129], v[14:15], v[66:67], v[54:55] op_sel:[1,0,0]
	s_waitcnt lgkmcnt(1)
; #define GAS __attribute__((address_space(1)))
; __device__ __forceinline__ void post_mix_route(Frame& F, int m, float (&lg)[16]) {
;     const int lane = F.lane, b = m >> 12, t = m & (SEQ - 1);
;     const bool b5 = (lane & 32) != 0, b4 = (lane & 16) != 0, b3 = (lane & 8) != 0, b2 = (lane & 4) != 0;
;     float a8[8], a4[4], a2[2];
; #pragma unroll
;     for (int e = 0; e < 8; ++e) a8[e] = swap32_sum(lg[e], lg[8 + e]);
; #pragma unroll
;     for (int e = 0; e < 4; ++e) a4[e] = swap16_sum(a8[e], a8[4 + e]);
; #pragma unroll
;     for (int e = 0; e < 2; ++e) { const float keep = b3 ? a4[2 + e] : a4[e], send = b3 ? a4[e] : a4[2 + e]; a2[e] = keep + dpp_f<DPP_ROR8>(send); }
;     float v = (b2 ? a2[1] : a2[0]) + dpp_f<DPP_HMIR>(b2 ? a2[0] : a2[1]);
;     v += dpp_f<DPP_X2>(v); v += dpp_f<DPP_X1>(v);
;     float mx = fmaxf(v, dpp_f<DPP_HMIR>(v)); mx = fmaxf(mx, dpp_f<DPP_ROR8>(mx)); mx = swap16_max(mx); mx = swap32_max(mx);
;     const float ex = expf(v - mx); float den = ex + dpp_f<DPP_HMIR>(ex); den += dpp_f<DPP_ROR8>(den); den = swap16_sum(den, den); den = swap32_sum(den, den);
;     const int e = (b5 ? 8 : 0) + (b4 ? 4 : 0) + (b3 ? 2 : 0) + (b2 ? 1 : 0);
;     if ((lane & 3) == 0) ((GAS float*)(F.ws + WS_AFF))[((size_t)b * NEXP + e) * SEQ + t] = ex / den;
; __device__ __forceinline__ void phase_post_mix(Frame& F, int l) {
;     ...
;         for (int j = 0; j < 4; ++j) { const LAS float* wg = rws + (lane + 64 * j) * 68;
; #pragma unroll
;             for (int i = 0; i < 4; ++i) { const f32x4 w0 = *(const LAS f32x4*)(wg + 16 * i), w1 = *(const LAS f32x4*)(wg + 16 * i + 4), w2 = *(const LAS f32x4*)(wg + 16 * i + 8), w3 = *(const LAS f32x4*)(wg + 16 * i + 12);
;                 const r_f32x2 wv[8] = {{w0[0], w0[1]}, {w0[2], w0[3]}, {w1[0], w1[1]}, {w1[2], w1[3]}, {w2[0], w2[1]}, {w2[2], w2[3]}, {w3[0], w3[1]}, {w3[2], w3[3]}};
; #pragma unroll
;                 for (int q = 0; q < 4; ++q) { const float h = xx[q][j][i]; const r_f32x2 hh = {h, h};
; #pragma unroll
;                     for (int e = 0; e < 8; ++e) lg2[q][e] = __builtin_elementwise_fma(hh, wv[e], lg2[q][e]); }
; #pragma unroll
;                 for (int q = 0; q < 4; ++q)
;                     asm volatile("" : "+v"(lg2[q][0]), "+v"(lg2[q][1]), "+v"(lg2[q][2]), "+v"(lg2[q][3]), "+v"(lg2[q][4]), "+v"(lg2[q][5]), "+v"(lg2[q][6]), "+v"(lg2[q][7]));
;                 } }
	v_pk_fma_f32 v[130:131], v[14:15], v[68:69], v[56:57] op_sel:[1,0,0]
	v_pk_fma_f32 v[132:133], v[14:15], v[70:71], v[60:61] op_sel:[1,0,0]
	s_waitcnt lgkmcnt(0)
	v_pk_fma_f32 v[134:135], v[14:15], v[72:73], v[62:63] op_sel:[1,0,0]
	v_pk_fma_f32 v[136:137], v[14:15], v[74:75], v[16:17] op_sel:[1,0,0]
	v_pk_fma_f32 v[60:61], v[18:19], v[20:21], v[28:29] op_sel:[1,0,0]
	v_pk_fma_f32 v[56:57], v[18:19], v[22:23], v[76:77] op_sel:[1,0,0]
	v_permlane32_swap_b32_e32 v122, v130
	v_permlane32_swap_b32_e32 v123, v131
	v_permlane32_swap_b32_e32 v124, v132
	v_permlane32_swap_b32_e32 v125, v133
	v_permlane32_swap_b32_e32 v126, v134
	v_permlane32_swap_b32_e32 v127, v135
	v_permlane32_swap_b32_e32 v128, v136
	v_permlane32_swap_b32_e32 v129, v137
	v_pk_fma_f32 v[52:53], v[18:19], v[64:65], v[78:79] op_sel:[1,0,0]
	v_pk_fma_f32 v[48:49], v[18:19], v[66:67], v[80:81] op_sel:[1,0,0]
	v_pk_fma_f32 v[62:63], v[18:19], v[68:69], v[82:83] op_sel:[1,0,0]
	v_pk_fma_f32 v[58:59], v[18:19], v[70:71], v[84:85] op_sel:[1,0,0]
	v_pk_fma_f32 v[54:55], v[18:19], v[72:73], v[86:87] op_sel:[1,0,0]
	v_pk_fma_f32 v[50:51], v[18:19], v[74:75], v[88:89] op_sel:[1,0,0]
	v_pk_fma_f32 v[44:45], v[30:31], v[20:21], v[90:91] op_sel:[1,0,0]
	v_pk_fma_f32 v[38:39], v[30:31], v[22:23], v[92:93] op_sel:[1,0,0]
	v_pk_fma_f32 v[34:35], v[30:31], v[64:65], v[94:95] op_sel:[1,0,0]
	v_pk_fma_f32 v[32:33], v[30:31], v[66:67], v[98:99] op_sel:[1,0,0]
	v_pk_fma_f32 v[46:47], v[30:31], v[68:69], v[100:101] op_sel:[1,0,0]
	v_pk_fma_f32 v[26:27], v[42:43], v[20:21], v[108:109] op_sel:[1,0,0]
	v_pk_fma_f32 v[22:23], v[42:43], v[22:23], v[110:111] op_sel:[1,0,0]
	v_pk_fma_f32 v[18:19], v[42:43], v[64:65], v[24:25] op_sel:[1,0,0]
	v_pk_fma_f32 v[14:15], v[42:43], v[66:67], v[112:113] op_sel:[1,0,0]
	v_pk_fma_f32 v[28:29], v[42:43], v[68:69], v[114:115] op_sel:[1,0,0]
	v_pk_fma_f32 v[24:25], v[42:43], v[70:71], v[116:117] op_sel:[1,0,0]
	v_pk_fma_f32 v[20:21], v[42:43], v[72:73], v[118:119] op_sel:[1,0,0]
	v_pk_fma_f32 v[16:17], v[42:43], v[74:75], v[120:121] op_sel:[1,0,0]
	v_add_f32_e32 v42, v122, v130
	v_add_f32_e32 v43, v123, v131
	v_add_f32_e32 v64, v124, v132
	v_add_f32_e32 v65, v125, v133
	v_add_f32_e32 v66, v126, v134
	v_add_f32_e32 v67, v127, v135
	v_add_f32_e32 v68, v128, v136
	v_add_f32_e32 v69, v129, v137
	v_permlane16_swap_b32_e32 v42, v66
	v_permlane16_swap_b32_e32 v43, v67
	v_permlane16_swap_b32_e32 v64, v68
	v_permlane16_swap_b32_e32 v65, v69
	v_add_f32_e32 v42, v42, v66
	v_add_f32_e32 v43, v43, v67
	v_add_f32_e32 v64, v64, v68
	v_add_f32_e32 v65, v65, v69
	v_cndmask_b32_e64 v66, v64, v42, s[4:5]
	v_cndmask_b32_e64 v42, v42, v64, s[4:5]
	v_cndmask_b32_e64 v64, v65, v43, s[4:5]
	v_cndmask_b32_e64 v43, v43, v65, s[4:5]
	v_add_f32_dpp v42, v42, v66 row_ror:8 row_mask:0xf bank_mask:0xf bound_ctrl:1
	v_pk_fma_f32 v[40:41], v[30:31], v[70:71], v[102:103] op_sel:[1,0,0]
	v_add_f32_dpp v43, v43, v64 row_ror:8 row_mask:0xf bank_mask:0xf bound_ctrl:1
	v_cndmask_b32_e64 v64, v43, v42, s[6:7]
	v_cndmask_b32_e64 v42, v42, v43, s[6:7]
	v_pk_fma_f32 v[36:37], v[30:31], v[72:73], v[104:105] op_sel:[1,0,0]
	v_pk_fma_f32 v[30:31], v[30:31], v[74:75], v[106:107] op_sel:[1,0,0]
	v_add_f32_dpp v42, v42, v64 row_half_mirror row_mask:0xf bank_mask:0xf bound_ctrl:1
	s_nop 1
	v_add_f32_dpp v42, v42, v42 quad_perm:[2,3,0,1] row_mask:0xf bank_mask:0xf bound_ctrl:1
	s_nop 1
	v_add_f32_dpp v42, v42, v42 quad_perm:[1,0,3,2] row_mask:0xf bank_mask:0xf bound_ctrl:1
	s_nop 1
	v_mov_b32_dpp v43, v42 row_half_mirror row_mask:0xf bank_mask:0xf bound_ctrl:1
	v_max_f32_e32 v43, v43, v43
	v_max_f32_e32 v43, v42, v43
	s_nop 1
	v_mov_b32_dpp v64, v43 row_ror:8 row_mask:0xf bank_mask:0xf bound_ctrl:1
	v_max_f32_e32 v64, v64, v64
	v_max_f32_e32 v43, v43, v64
	v_mov_b32_e32 v64, v43
	s_nop 1
	v_permlane16_swap_b32_e32 v43, v64
	v_max_f32_e32 v64, v64, v64
	v_max_f32_e32 v43, v43, v43
	v_max_f32_e32 v43, v43, v64
	v_mov_b32_e32 v64, v43
	s_nop 1
	v_permlane32_swap_b32_e32 v43, v64
	v_max_f32_e32 v64, v64, v64
	v_max_f32_e32 v43, v43, v43
	v_max_f32_e32 v43, v43, v64
	v_sub_f32_e32 v42, v42, v43
	v_mul_f32_e32 v43, 0x3fb8aa3b, v42
	v_fma_f32 v64, v42, s78, -v43
	v_rndne_f32_e32 v65, v43
	v_fmac_f32_e32 v64, 0x32a5705f, v42
	v_sub_f32_e32 v43, v43, v65
	v_add_f32_e32 v43, v43, v64
	v_exp_f32_e32 v43, v43
	v_cvt_i32_f32_e32 v64, v65
	v_cmp_ngt_f32_e32 vcc, s2, v42
	s_mov_b32 s2, 0x42b17218
	v_ldexp_f32 v43, v43, v64
	v_cndmask_b32_e32 v43, 0, v43, vcc
	v_cmp_nlt_f32_e32 vcc, s2, v42
	s_nop 1
	v_cndmask_b32_e32 v42, v242, v43, vcc
	s_nop 1
	v_add_f32_dpp v43, v42, v42 row_half_mirror row_mask:0xf bank_mask:0xf bound_ctrl:1
	s_nop 1
	v_add_f32_dpp v43, v43, v43 row_ror:8 row_mask:0xf bank_mask:0xf bound_ctrl:1
	v_mov_b32_e32 v64, v43
	s_nop 1
	v_permlane16_swap_b32_e32 v43, v64
	v_add_f32_e32 v43, v43, v64
	v_mov_b32_e32 v64, v43
	s_nop 1
	v_permlane32_swap_b32_e32 v43, v64
	s_and_saveexec_b64 s[2:3], s[8:9]
	s_cbranch_execnz .LBB0_1224
	s_or_b64 exec, exec, s[2:3]
	s_cmp_eq_u32 s14, s26
	s_cbranch_scc0 .LBB0_1225

; #define GAS __attribute__((address_space(1)))
; __device__ __forceinline__ float rsq(float x) { return __builtin_amdgcn_rsqf(x); }
; __device__ __forceinline__ void post_mix_front(Frame& F, int l, int m, const f32x4 (&y)[4], f32x4 (&x)[4], const LAS float* PV) {
;     ...
;     roww_store_bf16((GAS bf16*)(F.ws + WS_XR) + (size_t)m * DM, lane, x);
;     const float rstd2 = rsq(row_ss(x, lane) * (1.0f / DM) + EPS);
;     v4u hw;
; #pragma unroll
;     for (int j = 0; j < 4; ++j) { const int c4 = lane + 64 * j; x[j] = x[j] * rstd2 * Bv[c4] + Cv[c4]; hw[j] = pk4_f8(x[j][0], x[j][1], x[j][2], x[j][3]); }
;     ((GAS v4u*)((GAS unsigned char*)(F.ws + WS_HN) + (size_t)m * DM))[lane] = hw;
; __device__ __forceinline__ void phase_post_mix(Frame& F, int l) {
;     ...
;     const int gw = F.vcu * NWAVES + F.wave, NGW = F.G * NWAVES, lane = F.lane;
;     const GAS float* xin = INP(F, I_X); const GAS bf16* xr = (const GAS bf16*)(F.ws + WS_XR); const GAS bf16* Y = (const GAS bf16*)(F.ws + WS_Y);
;     for (int m0 = gw; m0 < M; m0 += 4 * NGW) {
;         int mm[4]; f32x4 xx[4][4];
; #pragma unroll
;         for (int q = 0; q < 4; ++q) mm[q] = (m0 + q * NGW < M) ? m0 + q * NGW : m0;
.LBB0_1245:
	s_or_b64 exec, exec, s[2:3]
	s_ashr_i32 s89, s9, 6
	s_lshl_b32 s2, s8, 3
	s_add_i32 s14, s89, s2
	s_add_i32 s2, 0, 0x20000
	v_mov_b32_e32 v1, s2
	s_waitcnt lgkmcnt(0)
	s_barrier
	ds_read_b64 v[4:5], v1
	v_and_b32_e32 v186, 63, v2
	s_cmpk_gt_i32 s14, 0x3fff
	s_waitcnt lgkmcnt(0)
	v_readfirstlane_b32 s2, v4
	v_readfirstlane_b32 s3, v5
	s_cbranch_scc1 .LBB0_1262
	v_lshlrev_b32_e32 v182, 5, v186
	v_lshl_add_u64 v[4:5], s[80:81], 0, v[182:183]
	s_mov_b64 s[4:5], 0x4400000
	v_lshl_add_u64 v[34:35], v[4:5], 0, s[4:5]
	s_mov_b64 s[4:5], 0x27400000
	v_lshl_add_u64 v[38:39], v[4:5], 0, s[4:5]
	v_lshlrev_b32_e32 v4, 4, v186
	s_add_i32 s15, 0, 0x11000
	v_add_u32_e32 v98, s15, v4
	s_ashr_i32 s15, s14, 31
	s_lshl_b32 s42, s24, 3
	s_lshl_b32 s16, s24, 5
	s_lshl_b64 s[18:19], s[14:15], 10
	v_mov_b32_e32 v5, v183
	s_add_u32 s17, s18, 0xac00000
	s_waitcnt vmcnt(0)
	v_lshl_add_u64 v[8:9], s[80:81], 0, v[4:5]
	v_and_b32_e32 v3, 8, v2
	v_and_b32_e32 v5, 4, v2
	v_and_b32_e32 v2, 3, v2
	s_addc_u32 s18, s19, 0
	v_or_b32_e32 v44, s17, v4
	s_ashr_i32 s17, s16, 31
	s_lshl_b64 s[20:21], s[14:15], 11
	v_lshlrev_b32_e32 v6, 6, v186
	v_mov_b32_e32 v7, v183
	v_mad_u32_u24 v1, v186, s23, 0
	s_mov_b64 s[4:5], 0xac00000
	v_cmp_eq_u32_e64 s[8:9], 0, v2
	v_lshlrev_b32_e32 v2, 12, v186
	v_mov_b32_e32 v45, s18
	s_lshl_b64 s[18:19], s[16:17], 10
	v_or_b32_e32 v46, s20, v182
	v_mov_b32_e32 v47, s21
	s_lshl_b64 s[20:21], s[16:17], 11
	s_lshl_b64 s[22:23], s[14:15], 12
	v_lshl_add_u64 v[36:37], s[2:3], 0, v[6:7]
	v_lshl_add_u64 v[40:41], v[8:9], 0, s[4:5]
	v_cmp_eq_u32_e64 s[4:5], 0, v3
	v_and_b32_e32 v2, 0x3c000, v2
	v_mov_b32_e32 v3, v183
	s_add_u32 s2, s2, s22
	v_lshl_add_u64 v[2:3], s[80:81], 0, v[2:3]
	s_addc_u32 s3, s3, s23
	v_lshl_add_u64 v[42:43], v[2:3], 0, s[96:97]
	v_lshl_add_u64 v[2:3], s[2:3], 0, v[6:7]
	v_cmp_eq_u32_e64 s[6:7], 0, v5
	v_lshl_add_u64 v[48:49], v[2:3], 0, 32
	s_lshl_b64 s[22:23], s[16:17], 12
	s_lshl_b32 s15, s24, 4
	s_mul_i32 s17, s24, 24
	s_branch .LBB0_1249

; #define GAS __attribute__((address_space(1)))
; #define LAS __attribute__((address_space(3)))
; __device__ __forceinline__ float rsq(float x) { return __builtin_amdgcn_rsqf(x); }
; __device__ __forceinline__ void post_mix_front(Frame& F, int l, int m, const f32x4 (&y)[4], f32x4 (&x)[4], const LAS float* PV) {
;     const int lane = F.lane, b = m >> 12; const LAS f32x4* A = (const LAS f32x4*)(PV + b * 3072); const LAS f32x4* Bv = A + 256; const LAS f32x4* Cv = A + 512;
;     const float rstd = rsq(row_ss(y, lane) * (1.0f / DM) + EPS);
; #pragma unroll
;     for (int j = 0; j < 4; ++j) { const int c4 = lane + 64 * j; x[j] = x[j] + A[c4] * (y[j] * rstd); }
;     roww_store_bf16((GAS bf16*)(F.ws + WS_XR) + (size_t)m * DM, lane, x);
; __device__ __forceinline__ void phase_post_mix(Frame& F, int l) {
;     ...
;     for (int m0 = gw; m0 < M; m0 += 4 * NGW) {
;         int mm[4]; f32x4 xx[4][4];
; #pragma unroll
;         for (int q = 0; q < 4; ++q) mm[q] = (m0 + q * NGW < M) ? m0 + q * NGW : m0;
; #pragma unroll
;         for (int q = 0; q < 4; q += 2) { f32x4 ya[4], yb[4];
;             roww_load_bf16(Y + (size_t)mm[q] * DM, lane, ya); roww_load_bf16(Y + (size_t)mm[q + 1] * DM, lane, yb);
;             if (l == 0) { roww_load(xin + (size_t)mm[q] * DM, lane, xx[q]); roww_load(xin + (size_t)mm[q + 1] * DM, lane, xx[q + 1]); }
;             else { roww_load_bf16(xr + (size_t)mm[q] * DM, lane, xx[q]); roww_load_bf16(xr + (size_t)mm[q + 1] * DM, lane, xx[q + 1]); }
;             post_mix_front(F, l, mm[q], ya, xx[q], PV); post_mix_front(F, l, mm[q + 1], yb, xx[q + 1], PV); }
.LBB0_1249:
	v_lshl_add_u64 v[54:55], s[80:81], 0, v[46:47]
	v_add_co_u32_e32 v2, vcc, 0x4400000, v54
	s_mov_b64 s[2:3], 0x4400000
	s_nop 0
	v_addc_co_u32_e32 v3, vcc, 0, v55, vcc
	global_load_dwordx4 v[10:13], v[2:3], off
	v_lshl_add_u64 v[2:3], v[54:55], 0, s[2:3]
	global_load_dwordx4 v[14:17], v[2:3], off offset:16
	s_add_i32 s2, s42, s14
	s_cmpk_lt_i32 s2, 0x4000
	s_cselect_b32 s28, s2, s14
	s_add_i32 s2, s15, s14
	s_cmpk_lt_i32 s2, 0x4000
	s_cselect_b32 s26, s2, s14
	s_add_i32 s2, s17, s14
	s_cmpk_lt_i32 s2, 0x4000
	s_cselect_b32 s24, s2, s14
	s_ashr_i32 s29, s28, 31
	s_lshl_b64 s[2:3], s[28:29], 11
	v_lshl_add_u64 v[2:3], v[34:35], 0, s[2:3]
	global_load_dwordx4 v[50:53], v[2:3], off
	global_load_dwordx4 v[76:79], v[2:3], off offset:16
	global_load_dwordx4 v[18:21], v[48:49], off offset:16
	global_load_dwordx4 v[22:25], v[48:49], off
	global_load_dwordx4 v[26:29], v[48:49], off offset:-16
	global_load_dwordx4 v[30:33], v[48:49], off offset:-32
	s_ashr_i32 s30, s14, 12
	s_lshl_b64 s[34:35], s[28:29], 12
	s_mul_i32 s25, s30, 0x3000
	v_lshl_add_u64 v[80:81], v[36:37], 0, s[34:35]
	v_add_u32_e32 v91, s25, v98
	global_load_dwordx4 v[2:5], v[80:81], off offset:48
	global_load_dwordx4 v[6:9], v[80:81], off offset:32
	s_mov_b32 s25, 0x27400000
	s_ashr_i32 s34, s28, 12
	s_lshl_b64 s[36:37], s[28:29], 10
	s_ashr_i32 s27, s26, 31
	s_lshl_b64 s[38:39], s[26:27], 11
	s_lshl_b64 s[40:41], s[26:27], 10
	s_waitcnt vmcnt(0)
	v_and_b32_e32 v83, 0xffff0000, v10
	v_and_b32_e32 v85, 0xffff0000, v11
	v_and_b32_e32 v87, 0xffff0000, v12
	v_and_b32_e32 v89, 0xffff0000, v13
	v_lshlrev_b32_e32 v82, 16, v10
	v_lshlrev_b32_e32 v84, 16, v11
	v_lshlrev_b32_e32 v86, 16, v12
	v_lshlrev_b32_e32 v88, 16, v13
	v_and_b32_e32 v75, 0xffff0000, v14
	v_and_b32_e32 v73, 0xffff0000, v15
	v_mul_f32_e32 v10, v83, v83
	v_mul_f32_e32 v11, v85, v85
	v_mul_f32_e32 v12, v87, v87
	v_mul_f32_e32 v13, v89, v89
	v_lshlrev_b32_e32 v74, 16, v14
	v_lshlrev_b32_e32 v72, 16, v15
	v_and_b32_e32 v67, 0xffff0000, v16
	v_and_b32_e32 v61, 0xffff0000, v17
	v_mul_f32_e32 v14, v75, v75
	v_mul_f32_e32 v15, v73, v73
	v_fmac_f32_e32 v10, v82, v82
	v_fmac_f32_e32 v11, v84, v84
	v_fmac_f32_e32 v12, v86, v86
	v_fmac_f32_e32 v13, v88, v88
	v_lshlrev_b32_e32 v66, 16, v16
	v_lshlrev_b32_e32 v60, 16, v17
	v_mul_f32_e32 v16, v67, v67
	v_mul_f32_e32 v17, v61, v61
	v_fmac_f32_e32 v14, v74, v74
	v_fmac_f32_e32 v15, v72, v72
	v_add_f32_e32 v10, v10, v11
	v_add_f32_e32 v11, v12, v13
	v_fmac_f32_e32 v16, v66, v66
	v_fmac_f32_e32 v17, v60, v60
	v_add_f32_e32 v12, v14, v15
	v_add_f32_e32 v10, v10, v11
	v_add_f32_e32 v13, v16, v17
	v_add_f32_e32 v10, v10, v12
	v_add_f32_e32 v10, v13, v10
	v_lshlrev_b32_e32 v70, 16, v50
	v_and_b32_e32 v71, 0xffff0000, v50
	v_add_f32_dpp v10, v10, v10 quad_perm:[1,0,3,2] row_mask:0xf bank_mask:0xf bound_ctrl:1
	v_lshlrev_b32_e32 v68, 16, v51
	v_and_b32_e32 v69, 0xffff0000, v51
	v_add_f32_dpp v10, v10, v10 quad_perm:[2,3,0,1] row_mask:0xf bank_mask:0xf bound_ctrl:1
	v_lshlrev_b32_e32 v64, 16, v52
	v_and_b32_e32 v65, 0xffff0000, v52
	v_add_f32_dpp v10, v10, v10 row_half_mirror row_mask:0xf bank_mask:0xf bound_ctrl:1
	v_lshlrev_b32_e32 v62, 16, v53
	v_and_b32_e32 v63, 0xffff0000, v53
	v_add_f32_dpp v10, v10, v10 row_mirror row_mask:0xf bank_mask:0xf bound_ctrl:1
	v_mov_b32_e32 v11, v10
	s_nop 1
	v_permlane16_swap_b32_e32 v10, v11
	v_add_f32_e32 v10, v10, v11
	v_mov_b32_e32 v11, v10
	s_nop 1
	v_permlane32_swap_b32_e32 v10, v11
	v_add_f32_e32 v10, v10, v11
	v_fmamk_f32 v10, v10, 0x3a800000, v225
	v_rsq_f32_e32 v90, v10
	v_lshlrev_b32_e32 v58, 16, v76
	v_and_b32_e32 v59, 0xffff0000, v76
	v_lshlrev_b32_e32 v56, 16, v77
	v_and_b32_e32 v57, 0xffff0000, v77
	v_lshlrev_b32_e32 v52, 16, v78
	v_and_b32_e32 v53, 0xffff0000, v78
	v_lshlrev_b32_e32 v50, 16, v79
	v_and_b32_e32 v51, 0xffff0000, v79
	ds_read_b128 v[76:79], v91
	global_load_dwordx4 v[10:13], v[80:81], off offset:16
	global_load_dwordx4 v[14:17], v[80:81], off
	v_pk_mul_f32 v[92:93], v[90:91], v[82:83] op_sel_hi:[0,1]
	ds_read_b128 v[80:83], v91 offset:1024
	v_pk_mul_f32 v[84:85], v[90:91], v[84:85] op_sel_hi:[0,1]
	s_waitcnt lgkmcnt(1)
	v_pk_fma_f32 v[76:77], v[76:77], v[92:93], v[30:31]
	v_pk_mul_f32 v[30:31], v[90:91], v[88:89] op_sel_hi:[0,1]
	v_pk_fma_f32 v[32:33], v[78:79], v[84:85], v[32:33]
	v_pk_mul_f32 v[78:79], v[90:91], v[86:87] op_sel_hi:[0,1]
	s_waitcnt lgkmcnt(0)
	v_pk_fma_f32 v[82:83], v[82:83], v[30:31], v[28:29]
	ds_read_b128 v[28:31], v91 offset:2048
	v_pk_fma_f32 v[78:79], v[80:81], v[78:79], v[26:27]
	v_pk_mul_f32 v[26:27], v[90:91], v[74:75] op_sel_hi:[0,1]
	v_pk_mul_f32 v[80:81], v[90:91], v[72:73] op_sel_hi:[0,1]
	ds_read_b128 v[72:75], v91 offset:3072
	s_waitcnt lgkmcnt(1)
	v_pk_fma_f32 v[80:81], v[30:31], v[80:81], v[24:25]
	v_pk_fma_f32 v[84:85], v[28:29], v[26:27], v[22:23]
	v_pk_mul_f32 v[22:23], v[90:91], v[66:67] op_sel_hi:[0,1]
	v_pk_mul_f32 v[24:25], v[90:91], v[60:61] op_sel_hi:[0,1]
	v_add_co_u32_e32 v26, vcc, s25, v54
	s_waitcnt lgkmcnt(0)
; #define GAS __attribute__((address_space(1)))
; #define LAS __attribute__((address_space(3)))
; __device__ __forceinline__ float rsq(float x) { return __builtin_amdgcn_rsqf(x); }
; __device__ __forceinline__ void post_mix_front(Frame& F, int l, int m, const f32x4 (&y)[4], f32x4 (&x)[4], const LAS float* PV) {
;     const int lane = F.lane, b = m >> 12; const LAS f32x4* A = (const LAS f32x4*)(PV + b * 3072); const LAS f32x4* Bv = A + 256; const LAS f32x4* Cv = A + 512;
;     const float rstd = rsq(row_ss(y, lane) * (1.0f / DM) + EPS);
; #pragma unroll
;     for (int j = 0; j < 4; ++j) { const int c4 = lane + 64 * j; x[j] = x[j] + A[c4] * (y[j] * rstd); }
;     roww_store_bf16((GAS bf16*)(F.ws + WS_XR) + (size_t)m * DM, lane, x);
;     const float rstd2 = rsq(row_ss(x, lane) * (1.0f / DM) + EPS);
;     v4u hw;
; #pragma unroll
;     for (int j = 0; j < 4; ++j) { const int c4 = lane + 64 * j; x[j] = x[j] * rstd2 * Bv[c4] + Cv[c4]; hw[j] = pk4_f8(x[j][0], x[j][1], x[j][2], x[j][3]); }
;     ((GAS v4u*)((GAS unsigned char*)(F.ws + WS_HN) + (size_t)m * DM))[lane] = hw;
; }
	v_pk_fma_f32 v[86:87], v[74:75], v[24:25], v[20:21]
	v_pk_fma_f32 v[88:89], v[72:73], v[22:23], v[18:19]
	v_cvt_pk_bf16_f32 v18, v76, v77
	v_cvt_pk_bf16_f32 v19, v32, v33
	v_cvt_pk_bf16_f32 v20, v78, v79
	v_cvt_pk_bf16_f32 v21, v82, v83
	v_addc_co_u32_e32 v27, vcc, 0, v55, vcc
	global_store_dwordx4 v[26:27], v[18:21], off
	v_cvt_pk_bf16_f32 v22, v84, v85
	v_cvt_pk_bf16_f32 v23, v80, v81
	v_mul_f32_e32 v18, v77, v77
	v_mul_f32_e32 v19, v33, v33
	v_fmac_f32_e32 v18, v76, v76
	v_fmac_f32_e32 v19, v32, v32
	v_add_f32_e32 v18, v18, v19
	v_mul_f32_e32 v19, v79, v79
	v_mul_f32_e32 v20, v83, v83
	v_fmac_f32_e32 v19, v78, v78
	v_fmac_f32_e32 v20, v82, v82
	v_add_f32_e32 v19, v19, v20
	v_add_f32_e32 v18, v18, v19
	v_mul_f32_e32 v19, v85, v85
	v_mul_f32_e32 v20, v81, v81
	v_fmac_f32_e32 v19, v84, v84
	v_fmac_f32_e32 v20, v80, v80
	v_add_f32_e32 v19, v19, v20
	v_add_f32_e32 v18, v19, v18
	v_mul_f32_e32 v19, v89, v89
	v_mul_f32_e32 v20, v87, v87
	v_fmac_f32_e32 v19, v88, v88
	v_fmac_f32_e32 v20, v86, v86
	v_add_f32_e32 v19, v19, v20
	v_add_f32_e32 v18, v19, v18
	v_cvt_pk_bf16_f32 v24, v88, v89
	v_cvt_pk_bf16_f32 v25, v86, v87
	v_add_f32_dpp v18, v18, v18 quad_perm:[1,0,3,2] row_mask:0xf bank_mask:0xf bound_ctrl:1
	global_store_dwordx4 v[26:27], v[22:25], off offset:16
	v_mov_b32_e32 v72, v183
	v_add_f32_dpp v18, v18, v18 quad_perm:[2,3,0,1] row_mask:0xf bank_mask:0xf bound_ctrl:1
	v_mov_b32_e32 v73, v183
	v_mov_b32_e32 v74, v183
	v_add_f32_dpp v18, v18, v18 row_half_mirror row_mask:0xf bank_mask:0xf bound_ctrl:1
	v_mov_b32_e32 v75, v183
	s_mul_i32 s25, s34, 0x3000
	v_add_f32_dpp v18, v18, v18 row_mirror row_mask:0xf bank_mask:0xf bound_ctrl:1
	v_mov_b32_e32 v19, v18
	s_nop 1
	v_permlane16_swap_b32_e32 v18, v19
	v_add_f32_e32 v18, v18, v19
	v_mov_b32_e32 v19, v18
	s_nop 1
	v_permlane32_swap_b32_e32 v18, v19
	v_add_f32_e32 v18, v18, v19
	v_fmamk_f32 v18, v18, 0x3a800000, v225
	v_rsq_f32_e32 v90, v18
	ds_read_b128 v[18:21], v91 offset:4096
	ds_read_b128 v[22:25], v91 offset:8192
	v_lshl_add_u64 v[92:93], v[38:39], 0, s[2:3]
	v_pk_mul_f32 v[54:55], v[76:77], v[90:91] op_sel_hi:[1,0]
	v_pk_mul_f32 v[60:61], v[32:33], v[90:91] op_sel_hi:[1,0]
	s_waitcnt lgkmcnt(0)
	v_pk_fma_f32 v[66:67], v[18:19], v[54:55], v[22:23]
	ds_read_b128 v[26:29], v91 offset:5120
	ds_read_b128 v[30:33], v91 offset:9216
	v_med3_f32 v18, v66, s33, v226
	v_med3_f32 v19, v67, s33, v226
	v_cvt_pk_fp8_f32 v72, v18, v19
	v_pk_fma_f32 v[60:61], v[20:21], v[60:61], v[24:25]
	v_pk_mul_f32 v[20:21], v[82:83], v[90:91] op_sel_hi:[1,0]
	v_med3_f32 v18, v60, s33, v226
	v_med3_f32 v19, v61, s33, v226
	v_cvt_pk_fp8_f32 v72, v18, v19 op_sel:[0,0,1]
	v_pk_mul_f32 v[18:19], v[78:79], v[90:91] op_sel_hi:[1,0]
	s_waitcnt lgkmcnt(0)
	v_pk_fma_f32 v[32:33], v[28:29], v[20:21], v[32:33]
	v_pk_fma_f32 v[54:55], v[26:27], v[18:19], v[30:31]
	v_pk_mul_f32 v[26:27], v[84:85], v[90:91] op_sel_hi:[1,0]
	v_med3_f32 v18, v54, s33, v226
	v_med3_f32 v19, v55, s33, v226
	v_cvt_pk_fp8_f32 v73, v18, v19
	v_med3_f32 v18, v32, s33, v226
	v_med3_f32 v19, v33, s33, v226
	v_pk_mul_f32 v[30:31], v[80:81], v[90:91] op_sel_hi:[1,0]
	v_cvt_pk_fp8_f32 v73, v18, v19 op_sel:[0,0,1]
	ds_read_b128 v[18:21], v91 offset:6144
	ds_read_b128 v[22:25], v91 offset:10240
	ds_read_b128 v[76:79], v91 offset:7168
	ds_read_b128 v[80:83], v91 offset:11264
	v_add_u32_e32 v84, s25, v98
	s_ashr_i32 s25, s24, 31
	s_lshl_b64 s[2:3], s[24:25], 11
	s_waitcnt lgkmcnt(2)
	v_pk_fma_f32 v[28:29], v[26:27], v[18:19], v[22:23]
	v_mul_f32_e32 v26, v71, v71
	v_mul_f32_e32 v27, v69, v69
	v_fmac_f32_e32 v26, v70, v70
	v_fmac_f32_e32 v27, v68, v68
	v_pk_fma_f32 v[24:25], v[30:31], v[20:21], v[24:25]
	v_add_f32_e32 v26, v26, v27
	v_mul_f32_e32 v27, v65, v65
	v_mul_f32_e32 v30, v63, v63
	v_fmac_f32_e32 v27, v64, v64
	v_fmac_f32_e32 v30, v62, v62
	v_add_f32_e32 v27, v27, v30
	v_add_f32_e32 v26, v26, v27
	v_mul_f32_e32 v27, v59, v59
	v_mul_f32_e32 v30, v57, v57
	v_fmac_f32_e32 v27, v58, v58
	v_fmac_f32_e32 v30, v56, v56
	v_add_f32_e32 v27, v27, v30
	v_add_f32_e32 v26, v26, v27
	v_mul_f32_e32 v27, v53, v53
	v_mul_f32_e32 v30, v51, v51
	v_fmac_f32_e32 v27, v52, v52
	v_fmac_f32_e32 v30, v50, v50
	v_add_f32_e32 v27, v27, v30
	v_med3_f32 v18, v28, s33, v226
	v_med3_f32 v19, v29, s33, v226
	v_add_f32_e32 v26, v27, v26
	v_cvt_pk_fp8_f32 v74, v18, v19
	v_med3_f32 v18, v24, s33, v226
	v_add_f32_dpp v26, v26, v26 quad_perm:[1,0,3,2] row_mask:0xf bank_mask:0xf bound_ctrl:1
	v_med3_f32 v19, v25, s33, v226
	v_cvt_pk_fp8_f32 v74, v18, v19 op_sel:[0,0,1]
	v_add_f32_dpp v26, v26, v26 quad_perm:[2,3,0,1] row_mask:0xf bank_mask:0xf bound_ctrl:1
	v_pk_mul_f32 v[18:19], v[88:89], v[90:91] op_sel_hi:[1,0]
	v_pk_mul_f32 v[22:23], v[86:87], v[90:91] op_sel_hi:[1,0]
	v_add_f32_dpp v26, v26, v26 row_half_mirror row_mask:0xf bank_mask:0xf bound_ctrl:1
	s_waitcnt lgkmcnt(0)
	v_pk_fma_f32 v[20:21], v[18:19], v[76:77], v[80:81]
	v_add_f32_dpp v26, v26, v26 row_mirror row_mask:0xf bank_mask:0xf bound_ctrl:1
	v_mov_b32_e32 v27, v26
	s_nop 1
	v_permlane16_swap_b32_e32 v26, v27
	v_med3_f32 v18, v20, s33, v226
	v_med3_f32 v19, v21, s33, v226
	v_add_f32_e32 v26, v26, v27
	v_cvt_pk_fp8_f32 v75, v18, v19
	v_mov_b32_e32 v27, v26
	s_nop 1
	v_permlane32_swap_b32_e32 v26, v27
	v_pk_fma_f32 v[18:19], v[22:23], v[78:79], v[82:83]
	v_add_f32_e32 v26, v26, v27
	v_med3_f32 v22, v18, s33, v226
	v_med3_f32 v23, v19, s33, v226
	v_fmamk_f32 v26, v26, 0x3a800000, v225
	v_cvt_pk_fp8_f32 v75, v22, v23 op_sel:[0,0,1]
	v_rsq_f32_e32 v26, v26
	v_lshl_add_u64 v[22:23], s[80:81], 0, v[44:45]
	ds_read_b128 v[76:79], v84
	global_store_dwordx4 v[22:23], v[72:75], off
	v_pk_mul_f32 v[22:23], v[26:27], v[70:71] op_sel_hi:[0,1]
	v_pk_mul_f32 v[30:31], v[26:27], v[68:69] op_sel_hi:[0,1]
	ds_read_b128 v[68:71], v84 offset:1024
	s_waitcnt vmcnt(3) lgkmcnt(1)
; #define GAS __attribute__((address_space(1)))
; #define LAS __attribute__((address_space(3)))
; __device__ __forceinline__ float rsq(float x) { return __builtin_amdgcn_rsqf(x); }
; __device__ __forceinline__ void post_mix_front(Frame& F, int l, int m, const f32x4 (&y)[4], f32x4 (&x)[4], const LAS float* PV) {
;     const int lane = F.lane, b = m >> 12; const LAS f32x4* A = (const LAS f32x4*)(PV + b * 3072); const LAS f32x4* Bv = A + 256; const LAS f32x4* Cv = A + 512;
;     const float rstd = rsq(row_ss(y, lane) * (1.0f / DM) + EPS);
; #pragma unroll
;     for (int j = 0; j < 4; ++j) { const int c4 = lane + 64 * j; x[j] = x[j] + A[c4] * (y[j] * rstd); }
;     roww_store_bf16((GAS bf16*)(F.ws + WS_XR) + (size_t)m * DM, lane, x);
;     const float rstd2 = rsq(row_ss(x, lane) * (1.0f / DM) + EPS);
;     v4u hw;
; #pragma unroll
;     for (int j = 0; j < 4; ++j) { const int c4 = lane + 64 * j; x[j] = x[j] * rstd2 * Bv[c4] + Cv[c4]; hw[j] = pk4_f8(x[j][0], x[j][1], x[j][2], x[j][3]); }
;     ((GAS v4u*)((GAS unsigned char*)(F.ws + WS_HN) + (size_t)m * DM))[lane] = hw;
; }
; __device__ __forceinline__ void phase_post_mix(Frame& F, int l) {
;     ...
;         for (int q = 0; q < 4; q += 2) { f32x4 ya[4], yb[4];
;             roww_load_bf16(Y + (size_t)mm[q] * DM, lane, ya); roww_load_bf16(Y + (size_t)mm[q + 1] * DM, lane, yb);
;             if (l == 0) { roww_load(xin + (size_t)mm[q] * DM, lane, xx[q]); roww_load(xin + (size_t)mm[q + 1] * DM, lane, xx[q + 1]); }
;             else { roww_load_bf16(xr + (size_t)mm[q] * DM, lane, xx[q]); roww_load_bf16(xr + (size_t)mm[q + 1] * DM, lane, xx[q + 1]); }
	v_pk_fma_f32 v[22:23], v[76:77], v[22:23], v[14:15]
	v_pk_mul_f32 v[14:15], v[26:27], v[62:63] op_sel_hi:[0,1]
	v_pk_fma_f32 v[30:31], v[78:79], v[30:31], v[16:17]
	v_pk_mul_f32 v[16:17], v[26:27], v[64:65] op_sel_hi:[0,1]
	s_waitcnt lgkmcnt(0)
	v_pk_fma_f32 v[62:63], v[70:71], v[14:15], v[12:13]
	ds_read_b128 v[12:15], v84 offset:2048
	v_pk_fma_f32 v[64:65], v[68:69], v[16:17], v[10:11]
	v_pk_mul_f32 v[10:11], v[26:27], v[58:59] op_sel_hi:[0,1]
	v_pk_mul_f32 v[16:17], v[26:27], v[56:57] op_sel_hi:[0,1]
	ds_read_b128 v[56:59], v84 offset:3072
	s_waitcnt lgkmcnt(1)
	v_pk_fma_f32 v[72:73], v[12:13], v[10:11], v[6:7]
	v_mul_f32_e32 v10, v23, v23
	v_mul_f32_e32 v11, v31, v31
	v_fmac_f32_e32 v10, v22, v22
	v_fmac_f32_e32 v11, v30, v30
	v_add_f32_e32 v10, v10, v11
	v_mul_f32_e32 v11, v65, v65
	v_mul_f32_e32 v12, v63, v63
	v_fmac_f32_e32 v11, v64, v64
	v_fmac_f32_e32 v12, v62, v62
	v_pk_fma_f32 v[68:69], v[14:15], v[16:17], v[8:9]
	v_add_f32_e32 v11, v11, v12
	v_add_f32_e32 v10, v10, v11
	v_mul_f32_e32 v11, v73, v73
	v_mul_f32_e32 v12, v69, v69
	v_pk_mul_f32 v[6:7], v[26:27], v[52:53] op_sel_hi:[0,1]
	v_pk_mul_f32 v[8:9], v[26:27], v[50:51] op_sel_hi:[0,1]
	v_fmac_f32_e32 v11, v72, v72
	v_fmac_f32_e32 v12, v68, v68
	s_waitcnt lgkmcnt(0)
	v_pk_fma_f32 v[26:27], v[58:59], v[8:9], v[4:5]
	v_pk_fma_f32 v[88:89], v[56:57], v[6:7], v[2:3]
	v_add_f32_e32 v11, v11, v12
	v_add_f32_e32 v10, v11, v10
	v_mul_f32_e32 v11, v89, v89
	v_mul_f32_e32 v12, v27, v27
	v_fmac_f32_e32 v11, v88, v88
	v_fmac_f32_e32 v12, v26, v26
	v_add_f32_e32 v11, v11, v12
	v_add_f32_e32 v10, v11, v10
	v_cvt_pk_bf16_f32 v2, v22, v23
	v_cvt_pk_bf16_f32 v3, v30, v31
	v_add_f32_dpp v10, v10, v10 quad_perm:[1,0,3,2] row_mask:0xf bank_mask:0xf bound_ctrl:1
	v_cvt_pk_bf16_f32 v4, v64, v65
	v_cvt_pk_bf16_f32 v9, v26, v27
	v_add_f32_dpp v10, v10, v10 quad_perm:[2,3,0,1] row_mask:0xf bank_mask:0xf bound_ctrl:1
	v_cvt_pk_bf16_f32 v5, v62, v63
	v_cvt_pk_bf16_f32 v6, v72, v73
	v_add_f32_dpp v10, v10, v10 row_half_mirror row_mask:0xf bank_mask:0xf bound_ctrl:1
	v_cvt_pk_bf16_f32 v7, v68, v69
	v_cvt_pk_bf16_f32 v8, v88, v89
	v_add_f32_dpp v10, v10, v10 row_mirror row_mask:0xf bank_mask:0xf bound_ctrl:1
	v_mov_b32_e32 v11, v10
	s_nop 1
	v_permlane16_swap_b32_e32 v10, v11
	v_add_f32_e32 v10, v10, v11
	v_mov_b32_e32 v11, v10
	s_nop 1
	v_permlane32_swap_b32_e32 v10, v11
	v_add_f32_e32 v10, v10, v11
	v_fmamk_f32 v10, v10, 0x3a800000, v225
	v_rsq_f32_e32 v90, v10
	ds_read_b128 v[10:13], v84 offset:4096
	ds_read_b128 v[14:17], v84 offset:8192
	ds_read_b128 v[50:53], v84 offset:5120
	ds_read_b128 v[56:59], v84 offset:9216
	v_pk_mul_f32 v[22:23], v[22:23], v[90:91] op_sel_hi:[1,0]
	v_pk_mul_f32 v[30:31], v[30:31], v[90:91] op_sel_hi:[1,0]
	s_waitcnt lgkmcnt(2)
	v_pk_fma_f32 v[74:75], v[10:11], v[22:23], v[14:15]
	v_mov_b32_e32 v10, v183
	v_med3_f32 v11, v74, s33, v226
	v_med3_f32 v14, v75, s33, v226
	v_cvt_pk_fp8_f32 v10, v11, v14
	v_pk_fma_f32 v[70:71], v[12:13], v[30:31], v[16:17]
	v_pk_mul_f32 v[14:15], v[62:63], v[90:91] op_sel_hi:[1,0]
	v_med3_f32 v11, v70, s33, v226
	v_med3_f32 v12, v71, s33, v226
	v_cvt_pk_fp8_f32 v10, v11, v12 op_sel:[0,0,1]
	v_pk_mul_f32 v[12:13], v[64:65], v[90:91] op_sel_hi:[1,0]
	v_mov_b32_e32 v11, v183
	s_waitcnt lgkmcnt(0)
	v_pk_fma_f32 v[64:65], v[50:51], v[12:13], v[56:57]
	v_pk_fma_f32 v[58:59], v[52:53], v[14:15], v[58:59]
	v_med3_f32 v12, v64, s33, v226
	v_med3_f32 v13, v65, s33, v226
	v_cvt_pk_fp8_f32 v11, v12, v13
	v_med3_f32 v12, v58, s33, v226
	v_med3_f32 v13, v59, s33, v226
	v_pk_mul_f32 v[16:17], v[72:73], v[90:91] op_sel_hi:[1,0]
	v_cvt_pk_fp8_f32 v11, v12, v13 op_sel:[0,0,1]
	ds_read_b128 v[12:15], v84 offset:6144
	ds_read_b128 v[76:79], v84 offset:10240
	ds_read_b128 v[80:83], v84 offset:7168
	ds_read_b128 v[84:87], v84 offset:11264
	v_pk_mul_f32 v[22:23], v[68:69], v[90:91] op_sel_hi:[1,0]
	global_store_dwordx4 v[92:93], v[2:5], off
	global_store_dwordx4 v[92:93], v[6:9], off offset:16
	s_waitcnt lgkmcnt(2)
	v_pk_fma_f32 v[52:53], v[16:17], v[12:13], v[76:77]
	s_nop 0
	v_med3_f32 v13, v52, s33, v226
	v_med3_f32 v16, v53, s33, v226
	v_mov_b32_e32 v12, v183
	v_cvt_pk_fp8_f32 v12, v13, v16
	v_pk_fma_f32 v[30:31], v[22:23], v[14:15], v[78:79]
	v_pk_mul_f32 v[16:17], v[26:27], v[90:91] op_sel_hi:[1,0]
	v_med3_f32 v13, v30, s33, v226
	v_med3_f32 v14, v31, s33, v226
	v_cvt_pk_fp8_f32 v12, v13, v14 op_sel:[0,0,1]
	v_pk_mul_f32 v[14:15], v[88:89], v[90:91] op_sel_hi:[1,0]
	v_mov_b32_e32 v13, v183
	s_waitcnt lgkmcnt(0)
	v_pk_fma_f32 v[26:27], v[14:15], v[80:81], v[84:85]
	v_pk_fma_f32 v[22:23], v[16:17], v[82:83], v[86:87]
	v_med3_f32 v14, v26, s33, v226
	v_med3_f32 v15, v27, s33, v226
	v_cvt_pk_fp8_f32 v13, v14, v15
	v_med3_f32 v14, v22, s33, v226
	v_med3_f32 v15, v23, s33, v226
	v_lshl_add_u64 v[2:3], v[40:41], 0, s[36:37]
	v_cvt_pk_fp8_f32 v13, v14, v15 op_sel:[0,0,1]
	v_lshl_add_u64 v[6:7], v[34:35], 0, s[38:39]
	v_lshl_add_u64 v[14:15], v[34:35], 0, s[2:3]
	s_lshl_b64 s[36:37], s[26:27], 12
	global_store_dwordx4 v[2:3], v[10:13], off
	global_load_dwordx4 v[2:5], v[6:7], off
	s_nop 0
	global_load_dwordx4 v[6:9], v[6:7], off offset:16
	s_nop 0
	global_load_dwordx4 v[10:13], v[14:15], off
	s_nop 0
	global_load_dwordx4 v[14:17], v[14:15], off offset:16
	s_waitcnt vmcnt(3)
	v_lshlrev_b32_e32 v50, 16, v2
	v_and_b32_e32 v51, 0xffff0000, v2
	v_lshlrev_b32_e32 v56, 16, v3
	v_and_b32_e32 v57, 0xffff0000, v3
	v_lshl_add_u64 v[2:3], v[36:37], 0, s[36:37]
	global_load_dwordx4 v[76:79], v[2:3], off offset:16
	global_load_dwordx4 v[100:103], v[2:3], off
	global_load_dwordx4 v[104:107], v[2:3], off offset:48
	global_load_dwordx4 v[108:111], v[2:3], off offset:32
	s_waitcnt vmcnt(5)
; #define GAS __attribute__((address_space(1)))
; #define LAS __attribute__((address_space(3)))
; __device__ __forceinline__ float rsq(float x) { return __builtin_amdgcn_rsqf(x); }
; __device__ __forceinline__ void post_mix_front(Frame& F, int l, int m, const f32x4 (&y)[4], f32x4 (&x)[4], const LAS float* PV) {
;     const int lane = F.lane, b = m >> 12; const LAS f32x4* A = (const LAS f32x4*)(PV + b * 3072); const LAS f32x4* Bv = A + 256; const LAS f32x4* Cv = A + 512;
;     const float rstd = rsq(row_ss(y, lane) * (1.0f / DM) + EPS);
; #pragma unroll
;     for (int j = 0; j < 4; ++j) { const int c4 = lane + 64 * j; x[j] = x[j] + A[c4] * (y[j] * rstd); }
;     roww_store_bf16((GAS bf16*)(F.ws + WS_XR) + (size_t)m * DM, lane, x);
;     const float rstd2 = rsq(row_ss(x, lane) * (1.0f / DM) + EPS);
;     v4u hw;
; #pragma unroll
;     for (int j = 0; j < 4; ++j) { const int c4 = lane + 64 * j; x[j] = x[j] * rstd2 * Bv[c4] + Cv[c4]; hw[j] = pk4_f8(x[j][0], x[j][1], x[j][2], x[j][3]); }
;     ((GAS v4u*)((GAS unsigned char*)(F.ws + WS_HN) + (size_t)m * DM))[lane] = hw;
; }
; __device__ __forceinline__ void phase_post_mix(Frame& F, int l) {
;     ...
;         for (int q = 0; q < 4; q += 2) { f32x4 ya[4], yb[4];
;             roww_load_bf16(Y + (size_t)mm[q] * DM, lane, ya); roww_load_bf16(Y + (size_t)mm[q + 1] * DM, lane, yb);
;             if (l == 0) { roww_load(xin + (size_t)mm[q] * DM, lane, xx[q]); roww_load(xin + (size_t)mm[q + 1] * DM, lane, xx[q + 1]); }
;             else { roww_load_bf16(xr + (size_t)mm[q] * DM, lane, xx[q]); roww_load_bf16(xr + (size_t)mm[q + 1] * DM, lane, xx[q + 1]); }
	v_lshlrev_b32_e32 v96, 16, v10
	v_and_b32_e32 v97, 0xffff0000, v10
	v_lshlrev_b32_e32 v94, 16, v11
	v_and_b32_e32 v95, 0xffff0000, v11
	v_mul_f32_e32 v10, v51, v51
	v_mul_f32_e32 v11, v57, v57
	v_and_b32_e32 v63, 0xffff0000, v4
	v_and_b32_e32 v69, 0xffff0000, v5
	v_fmac_f32_e32 v10, v50, v50
	v_fmac_f32_e32 v11, v56, v56
	v_lshlrev_b32_e32 v62, 16, v4
	v_lshlrev_b32_e32 v68, 16, v5
	v_lshlrev_b32_e32 v92, 16, v12
	v_and_b32_e32 v93, 0xffff0000, v12
	v_add_f32_e32 v10, v10, v11
	v_mul_f32_e32 v11, v63, v63
	v_mul_f32_e32 v12, v69, v69
	v_fmac_f32_e32 v11, v62, v62
	v_fmac_f32_e32 v12, v68, v68
	v_and_b32_e32 v73, 0xffff0000, v6
	v_and_b32_e32 v121, 0xffff0000, v7
	v_add_f32_e32 v11, v11, v12
	v_lshlrev_b32_e32 v72, 16, v6
	v_lshlrev_b32_e32 v120, 16, v7
	v_add_f32_e32 v10, v10, v11
	v_mul_f32_e32 v11, v73, v73
	v_mul_f32_e32 v12, v121, v121
	v_fmac_f32_e32 v11, v72, v72
	v_fmac_f32_e32 v12, v120, v120
	v_and_b32_e32 v123, 0xffff0000, v8
	v_and_b32_e32 v125, 0xffff0000, v9
	v_add_f32_e32 v11, v11, v12
	v_lshlrev_b32_e32 v122, 16, v8
	v_lshlrev_b32_e32 v124, 16, v9
	v_add_f32_e32 v10, v10, v11
	v_mul_f32_e32 v11, v123, v123
	v_mul_f32_e32 v12, v125, v125
	v_fmac_f32_e32 v11, v122, v122
	v_fmac_f32_e32 v12, v124, v124
	v_add_f32_e32 v11, v11, v12
	v_add_f32_e32 v10, v11, v10
	s_lshl_b64 s[36:37], s[24:25], 12
	s_waitcnt vmcnt(4)
	v_lshlrev_b32_e32 v88, 16, v14
	v_add_f32_dpp v10, v10, v10 quad_perm:[1,0,3,2] row_mask:0xf bank_mask:0xf bound_ctrl:1
	v_and_b32_e32 v89, 0xffff0000, v14
	v_lshlrev_b32_e32 v86, 16, v15
	v_add_f32_dpp v10, v10, v10 quad_perm:[2,3,0,1] row_mask:0xf bank_mask:0xf bound_ctrl:1
	v_and_b32_e32 v87, 0xffff0000, v15
	v_lshl_add_u64 v[14:15], v[36:37], 0, s[36:37]
	v_add_f32_dpp v10, v10, v10 row_half_mirror row_mask:0xf bank_mask:0xf bound_ctrl:1
	s_ashr_i32 s36, s26, 12
	s_mul_i32 s29, s36, 0x3000
	v_add_f32_dpp v10, v10, v10 row_mirror row_mask:0xf bank_mask:0xf bound_ctrl:1
	v_mov_b32_e32 v11, v10
	s_nop 1
	v_permlane16_swap_b32_e32 v10, v11
	v_add_f32_e32 v10, v10, v11
	v_mov_b32_e32 v11, v10
	s_nop 1
	v_permlane32_swap_b32_e32 v10, v11
	v_add_f32_e32 v10, v10, v11
	v_fmamk_f32 v10, v10, 0x3a800000, v225
	v_add_u32_e32 v99, s29, v98
	v_lshlrev_b32_e32 v90, 16, v13
	v_and_b32_e32 v91, 0xffff0000, v13
	v_lshlrev_b32_e32 v84, 16, v16
	v_and_b32_e32 v85, 0xffff0000, v16
	v_lshlrev_b32_e32 v82, 16, v17
	v_and_b32_e32 v83, 0xffff0000, v17
	global_load_dwordx4 v[2:5], v[14:15], off offset:48
	global_load_dwordx4 v[6:9], v[14:15], off offset:32
	v_rsq_f32_e32 v126, v10
	ds_read_b128 v[112:115], v99
	global_load_dwordx4 v[10:13], v[14:15], off offset:16
	s_nop 0
	global_load_dwordx4 v[14:17], v[14:15], off
	ds_read_b128 v[116:119], v99 offset:1024
	v_pk_mul_f32 v[50:51], v[126:127], v[50:51] op_sel_hi:[0,1]
	v_pk_mul_f32 v[56:57], v[126:127], v[56:57] op_sel_hi:[0,1]
	v_pk_mul_f32 v[68:69], v[126:127], v[68:69] op_sel_hi:[0,1]
	v_pk_mul_f32 v[62:63], v[126:127], v[62:63] op_sel_hi:[0,1]
	s_waitcnt vmcnt(6) lgkmcnt(1)
	v_pk_fma_f32 v[56:57], v[114:115], v[56:57], v[102:103]
	v_pk_fma_f32 v[50:51], v[112:113], v[50:51], v[100:101]
	ds_read_b128 v[100:103], v99 offset:3072
	s_waitcnt lgkmcnt(1)
	v_pk_fma_f32 v[68:69], v[118:119], v[68:69], v[78:79]
	ds_read_b128 v[78:81], v99 offset:2048
	v_pk_fma_f32 v[62:63], v[116:117], v[62:63], v[76:77]
	v_pk_mul_f32 v[72:73], v[126:127], v[72:73] op_sel_hi:[0,1]
	v_pk_mul_f32 v[76:77], v[126:127], v[120:121] op_sel_hi:[0,1]
	s_waitcnt vmcnt(4) lgkmcnt(0)
	v_pk_fma_f32 v[112:113], v[80:81], v[76:77], v[110:111]
	v_pk_fma_f32 v[114:115], v[78:79], v[72:73], v[108:109]
	v_pk_mul_f32 v[72:73], v[126:127], v[122:123] op_sel_hi:[0,1]
	v_pk_mul_f32 v[76:77], v[126:127], v[124:125] op_sel_hi:[0,1]
	v_pk_fma_f32 v[118:119], v[102:103], v[76:77], v[106:107]
	v_pk_fma_f32 v[120:121], v[100:101], v[72:73], v[104:105]
	v_cvt_pk_bf16_f32 v76, v50, v51
	v_cvt_pk_bf16_f32 v77, v56, v57
	v_cvt_pk_bf16_f32 v78, v62, v63
	v_cvt_pk_bf16_f32 v79, v68, v69
	v_lshl_add_u64 v[72:73], v[38:39], 0, s[38:39]
	global_store_dwordx4 v[72:73], v[76:79], off
	v_cvt_pk_bf16_f32 v100, v114, v115
	v_cvt_pk_bf16_f32 v101, v112, v113
	v_mul_f32_e32 v76, v51, v51
	v_mul_f32_e32 v77, v57, v57
	v_fmac_f32_e32 v76, v50, v50
	v_fmac_f32_e32 v77, v56, v56
	v_add_f32_e32 v76, v76, v77
	v_mul_f32_e32 v77, v63, v63
	v_mul_f32_e32 v78, v69, v69
	v_fmac_f32_e32 v77, v62, v62
	v_fmac_f32_e32 v78, v68, v68
	v_add_f32_e32 v77, v77, v78
	v_add_f32_e32 v76, v76, v77
	v_mul_f32_e32 v77, v115, v115
	v_mul_f32_e32 v78, v113, v113
	v_fmac_f32_e32 v77, v114, v114
	v_fmac_f32_e32 v78, v112, v112
	v_add_f32_e32 v77, v77, v78
	v_add_f32_e32 v76, v77, v76
	v_mul_f32_e32 v77, v121, v121
	v_mul_f32_e32 v78, v119, v119
	v_fmac_f32_e32 v77, v120, v120
	v_fmac_f32_e32 v78, v118, v118
	v_add_f32_e32 v77, v77, v78
	v_add_f32_e32 v76, v77, v76
	v_cvt_pk_bf16_f32 v102, v120, v121
	v_cvt_pk_bf16_f32 v103, v118, v119
	v_add_f32_dpp v76, v76, v76 quad_perm:[1,0,3,2] row_mask:0xf bank_mask:0xf bound_ctrl:1
	global_store_dwordx4 v[72:73], v[100:103], off offset:16
	s_ashr_i32 s38, s24, 12
	v_add_f32_dpp v76, v76, v76 quad_perm:[2,3,0,1] row_mask:0xf bank_mask:0xf bound_ctrl:1
	s_mul_i32 s27, s38, 0x3000
	s_nop 0
	v_add_f32_dpp v76, v76, v76 row_half_mirror row_mask:0xf bank_mask:0xf bound_ctrl:1
	s_nop 1
	v_add_f32_dpp v76, v76, v76 row_mirror row_mask:0xf bank_mask:0xf bound_ctrl:1
	v_mov_b32_e32 v77, v76
	s_nop 1
	v_permlane16_swap_b32_e32 v76, v77
	v_add_f32_e32 v76, v76, v77
	v_mov_b32_e32 v77, v76
	s_nop 1
	v_permlane32_swap_b32_e32 v76, v77
	v_add_f32_e32 v76, v76, v77
	v_fmamk_f32 v76, v76, 0x3a800000, v225
	v_rsq_f32_e32 v122, v76
	ds_read_b128 v[76:79], v99 offset:4096
	ds_read_b128 v[100:103], v99 offset:8192
	ds_read_b128 v[104:107], v99 offset:5120
	ds_read_b128 v[108:111], v99 offset:9216
	v_pk_mul_f32 v[50:51], v[50:51], v[122:123] op_sel_hi:[1,0]
	v_pk_mul_f32 v[56:57], v[56:57], v[122:123] op_sel_hi:[1,0]
	s_waitcnt lgkmcnt(2)
; #define GAS __attribute__((address_space(1)))
; __device__ __forceinline__ float rsq(float x) { return __builtin_amdgcn_rsqf(x); }
; __device__ __forceinline__ void post_mix_front(Frame& F, int l, int m, const f32x4 (&y)[4], f32x4 (&x)[4], const LAS float* PV) {
;     ...
;     roww_store_bf16((GAS bf16*)(F.ws + WS_XR) + (size_t)m * DM, lane, x);
;     const float rstd2 = rsq(row_ss(x, lane) * (1.0f / DM) + EPS);
;     v4u hw;
; #pragma unroll
;     for (int j = 0; j < 4; ++j) { const int c4 = lane + 64 * j; x[j] = x[j] * rstd2 * Bv[c4] + Cv[c4]; hw[j] = pk4_f8(x[j][0], x[j][1], x[j][2], x[j][3]); }
;     ((GAS v4u*)((GAS unsigned char*)(F.ws + WS_HN) + (size_t)m * DM))[lane] = hw;
; }
	v_pk_fma_f32 v[80:81], v[76:77], v[50:51], v[100:101]
	v_mov_b32_e32 v100, v183
	v_med3_f32 v50, v80, s33, v226
	v_med3_f32 v51, v81, s33, v226
	v_cvt_pk_fp8_f32 v100, v50, v51
	v_pk_fma_f32 v[78:79], v[78:79], v[56:57], v[102:103]
	v_pk_mul_f32 v[56:57], v[68:69], v[122:123] op_sel_hi:[1,0]
	v_med3_f32 v50, v78, s33, v226
	v_med3_f32 v51, v79, s33, v226
	v_cvt_pk_fp8_f32 v100, v50, v51 op_sel:[0,0,1]
	v_pk_mul_f32 v[50:51], v[62:63], v[122:123] op_sel_hi:[1,0]
	v_mov_b32_e32 v101, v183
	s_waitcnt lgkmcnt(0)
	v_pk_fma_f32 v[76:77], v[104:105], v[50:51], v[108:109]
	v_pk_fma_f32 v[72:73], v[106:107], v[56:57], v[110:111]
	v_med3_f32 v50, v76, s33, v226
	v_med3_f32 v51, v77, s33, v226
	v_cvt_pk_fp8_f32 v101, v50, v51
	ds_read_b128 v[102:105], v99 offset:6144
	ds_read_b128 v[106:109], v99 offset:10240
	v_med3_f32 v50, v72, s33, v226
	v_med3_f32 v51, v73, s33, v226
	v_cvt_pk_fp8_f32 v101, v50, v51 op_sel:[0,0,1]
	v_pk_mul_f32 v[50:51], v[114:115], v[122:123] op_sel_hi:[1,0]
	v_pk_mul_f32 v[56:57], v[112:113], v[122:123] op_sel_hi:[1,0]
	s_waitcnt lgkmcnt(0)
	v_pk_fma_f32 v[68:69], v[50:51], v[102:103], v[106:107]
	v_mov_b32_e32 v102, v183
	v_med3_f32 v50, v68, s33, v226
	v_med3_f32 v51, v69, s33, v226
	ds_read_b128 v[110:113], v99 offset:7168
	ds_read_b128 v[114:117], v99 offset:11264
	v_cvt_pk_fp8_f32 v102, v50, v51
	v_pk_fma_f32 v[62:63], v[56:57], v[104:105], v[108:109]
	v_mov_b32_e32 v103, v183
	v_med3_f32 v50, v62, s33, v226
	v_med3_f32 v51, v63, s33, v226
	v_cvt_pk_fp8_f32 v102, v50, v51 op_sel:[0,0,1]
	v_pk_mul_f32 v[50:51], v[120:121], v[122:123] op_sel_hi:[1,0]
	v_pk_mul_f32 v[104:105], v[118:119], v[122:123] op_sel_hi:[1,0]
	s_waitcnt lgkmcnt(0)
	v_pk_fma_f32 v[56:57], v[50:51], v[110:111], v[114:115]
	v_lshl_add_u64 v[108:109], v[40:41], 0, s[40:41]
	v_med3_f32 v50, v56, s33, v226
	v_med3_f32 v51, v57, s33, v226
	v_cvt_pk_fp8_f32 v103, v50, v51
	v_pk_fma_f32 v[50:51], v[104:105], v[112:113], v[116:117]
	v_mul_f32_e32 v105, v91, v91
	v_med3_f32 v99, v50, s33, v226
	v_med3_f32 v104, v51, s33, v226
	v_cvt_pk_fp8_f32 v103, v99, v104 op_sel:[0,0,1]
	v_mul_f32_e32 v99, v97, v97
	v_mul_f32_e32 v104, v95, v95
	v_fmac_f32_e32 v99, v96, v96
	v_fmac_f32_e32 v104, v94, v94
	v_add_f32_e32 v99, v99, v104
	v_mul_f32_e32 v104, v93, v93
	v_fmac_f32_e32 v104, v92, v92
	v_fmac_f32_e32 v105, v90, v90
	v_add_f32_e32 v104, v104, v105
	v_add_f32_e32 v99, v99, v104
	v_mul_f32_e32 v104, v89, v89
	v_mul_f32_e32 v105, v87, v87
	v_fmac_f32_e32 v104, v88, v88
	v_fmac_f32_e32 v105, v86, v86
	v_add_f32_e32 v104, v104, v105
	v_add_f32_e32 v99, v99, v104
	v_mul_f32_e32 v104, v85, v85
	v_mul_f32_e32 v105, v83, v83
	v_fmac_f32_e32 v104, v84, v84
	v_fmac_f32_e32 v105, v82, v82
	v_add_f32_e32 v104, v104, v105
	v_add_f32_e32 v99, v104, v99
	global_store_dwordx4 v[108:109], v[100:103], off
	s_lshl_b64 s[40:41], s[24:25], 10
	v_add_f32_dpp v99, v99, v99 quad_perm:[1,0,3,2] row_mask:0xf bank_mask:0xf bound_ctrl:1
	s_nop 1
	v_add_f32_dpp v99, v99, v99 quad_perm:[2,3,0,1] row_mask:0xf bank_mask:0xf bound_ctrl:1
	s_nop 1
	v_add_f32_dpp v99, v99, v99 row_half_mirror row_mask:0xf bank_mask:0xf bound_ctrl:1
	s_nop 1
	v_add_f32_dpp v99, v99, v99 row_mirror row_mask:0xf bank_mask:0xf bound_ctrl:1
	v_mov_b32_e32 v104, v99
	s_nop 1
	v_permlane16_swap_b32_e32 v99, v104
	v_add_f32_e32 v99, v99, v104
	v_mov_b32_e32 v104, v99
	s_nop 1
	v_permlane32_swap_b32_e32 v99, v104
	v_add_f32_e32 v99, v99, v104
	v_fmamk_f32 v99, v99, 0x3a800000, v225
	v_rsq_f32_e32 v110, v99
	v_add_u32_e32 v99, s27, v98
	ds_read_b128 v[104:107], v99
	v_pk_mul_f32 v[100:101], v[110:111], v[96:97] op_sel_hi:[0,1]
	v_pk_mul_f32 v[102:103], v[110:111], v[94:95] op_sel_hi:[0,1]
	ds_read_b128 v[94:97], v99 offset:1024
	s_waitcnt vmcnt(3) lgkmcnt(1)
	v_pk_fma_f32 v[100:101], v[104:105], v[100:101], v[14:15]
	v_pk_mul_f32 v[14:15], v[110:111], v[90:91] op_sel_hi:[0,1]
	v_pk_mul_f32 v[92:93], v[110:111], v[92:93] op_sel_hi:[0,1]
	v_pk_mul_f32 v[90:91], v[110:111], v[88:89] op_sel_hi:[0,1]
	s_waitcnt lgkmcnt(0)
	v_pk_fma_f32 v[96:97], v[96:97], v[14:15], v[12:13]
	ds_read_b128 v[12:15], v99 offset:2048
	v_pk_fma_f32 v[10:11], v[94:95], v[92:93], v[10:11]
	v_pk_mul_f32 v[92:93], v[110:111], v[86:87] op_sel_hi:[0,1]
	ds_read_b128 v[86:89], v99 offset:3072
	v_pk_fma_f32 v[16:17], v[106:107], v[102:103], v[16:17]
	s_waitcnt lgkmcnt(1)
	v_pk_fma_f32 v[104:105], v[12:13], v[90:91], v[6:7]
	v_pk_mul_f32 v[6:7], v[110:111], v[84:85] op_sel_hi:[0,1]
	v_pk_fma_f32 v[102:103], v[14:15], v[92:93], v[8:9]
	s_waitcnt lgkmcnt(0)
	v_pk_fma_f32 v[108:109], v[86:87], v[6:7], v[2:3]
	v_mul_f32_e32 v6, v101, v101
	v_mul_f32_e32 v7, v17, v17
	v_pk_mul_f32 v[8:9], v[110:111], v[82:83] op_sel_hi:[0,1]
	v_fmac_f32_e32 v6, v100, v100
	v_fmac_f32_e32 v7, v16, v16
	v_pk_fma_f32 v[106:107], v[88:89], v[8:9], v[4:5]
	v_add_f32_e32 v6, v6, v7
	v_mul_f32_e32 v7, v11, v11
	v_mul_f32_e32 v8, v97, v97
	v_fmac_f32_e32 v7, v10, v10
	v_fmac_f32_e32 v8, v96, v96
	v_add_f32_e32 v7, v7, v8
	v_add_f32_e32 v6, v6, v7
	v_mul_f32_e32 v7, v105, v105
	v_mul_f32_e32 v8, v103, v103
	v_fmac_f32_e32 v7, v104, v104
	v_fmac_f32_e32 v8, v102, v102
	v_add_f32_e32 v7, v7, v8
	v_add_f32_e32 v6, v7, v6
	v_mul_f32_e32 v7, v109, v109
	v_mul_f32_e32 v8, v107, v107
	v_fmac_f32_e32 v7, v108, v108
	v_fmac_f32_e32 v8, v106, v106
	v_add_f32_e32 v7, v7, v8
	v_add_f32_e32 v6, v7, v6
	v_cvt_pk_bf16_f32 v2, v100, v101
	v_cvt_pk_bf16_f32 v3, v16, v17
	v_add_f32_dpp v6, v6, v6 quad_perm:[1,0,3,2] row_mask:0xf bank_mask:0xf bound_ctrl:1
	v_cvt_pk_bf16_f32 v4, v10, v11
	v_cvt_pk_bf16_f32 v5, v96, v97
	v_add_f32_dpp v6, v6, v6 quad_perm:[2,3,0,1] row_mask:0xf bank_mask:0xf bound_ctrl:1
	v_lshl_add_u64 v[110:111], v[38:39], 0, s[2:3]
	global_store_dwordx4 v[110:111], v[2:5], off
	v_add_f32_dpp v6, v6, v6 row_half_mirror row_mask:0xf bank_mask:0xf bound_ctrl:1
	v_mov_b32_e32 v94, v183
	v_mov_b32_e32 v95, v183
	v_add_f32_dpp v6, v6, v6 row_mirror row_mask:0xf bank_mask:0xf bound_ctrl:1
	v_mov_b32_e32 v7, v6
	s_nop 1
	v_permlane16_swap_b32_e32 v6, v7
	v_add_f32_e32 v6, v6, v7
	v_mov_b32_e32 v7, v6
	s_nop 1
	v_permlane32_swap_b32_e32 v6, v7
	v_add_f32_e32 v6, v6, v7
	v_fmamk_f32 v6, v6, 0x3a800000, v225
	v_rsq_f32_e32 v112, v6
	ds_read_b128 v[2:5], v99 offset:4096
	ds_read_b128 v[6:9], v99 offset:8192
	ds_read_b128 v[86:89], v99 offset:5120
	ds_read_b128 v[90:93], v99 offset:9216
	v_cvt_pk_bf16_f32 v82, v104, v105
	v_pk_mul_f32 v[12:13], v[100:101], v[112:113] op_sel_hi:[1,0]
	v_pk_mul_f32 v[14:15], v[16:17], v[112:113] op_sel_hi:[1,0]
	s_waitcnt lgkmcnt(2)
; #define GAS __attribute__((address_space(1)))
; #define LAS __attribute__((address_space(3)))
; __device__ __forceinline__ float rsq(float x) { return __builtin_amdgcn_rsqf(x); }
; __device__ __forceinline__ void post_mix_front(Frame& F, int l, int m, const f32x4 (&y)[4], f32x4 (&x)[4], const LAS float* PV) {
;     ...
;     const float rstd2 = rsq(row_ss(x, lane) * (1.0f / DM) + EPS);
;     v4u hw;
; #pragma unroll
;     for (int j = 0; j < 4; ++j) { const int c4 = lane + 64 * j; x[j] = x[j] * rstd2 * Bv[c4] + Cv[c4]; hw[j] = pk4_f8(x[j][0], x[j][1], x[j][2], x[j][3]); }
;     ((GAS v4u*)((GAS unsigned char*)(F.ws + WS_HN) + (size_t)m * DM))[lane] = hw;
; __device__ __forceinline__ void phase_post_mix(Frame& F, int l) {
;     ...
;         for (int j = 0; j < 4; ++j) { const LAS float* wg = rws + (lane + 64 * j) * 68;
; #pragma unroll
;             for (int i = 0; i < 4; ++i) { const f32x4 w0 = *(const LAS f32x4*)(wg + 16 * i), w1 = *(const LAS f32x4*)(wg + 16 * i + 4), w2 = *(const LAS f32x4*)(wg + 16 * i + 8), w3 = *(const LAS f32x4*)(wg + 16 * i + 12);
;                 const r_f32x2 wv[8] = {{w0[0], w0[1]}, {w0[2], w0[3]}, {w1[0], w1[1]}, {w1[2], w1[3]}, {w2[0], w2[1]}, {w2[2], w2[3]}, {w3[0], w3[1]}, {w3[2], w3[3]}};
; #pragma unroll
;                 for (int q = 0; q < 4; ++q) { const float h = xx[q][j][i]; const r_f32x2 hh = {h, h};
; #pragma unroll
;                     for (int e = 0; e < 8; ++e) lg2[q][e] = __builtin_elementwise_fma(hh, wv[e], lg2[q][e]); }
	v_pk_fma_f32 v[16:17], v[2:3], v[12:13], v[6:7]
	v_pk_fma_f32 v[14:15], v[4:5], v[14:15], v[8:9]
	v_med3_f32 v2, v16, s33, v226
	v_med3_f32 v3, v17, s33, v226
	v_cvt_pk_fp8_f32 v94, v2, v3
	v_med3_f32 v2, v14, s33, v226
	v_med3_f32 v3, v15, s33, v226
	v_pk_mul_f32 v[4:5], v[96:97], v[112:113] op_sel_hi:[1,0]
	v_cvt_pk_fp8_f32 v94, v2, v3 op_sel:[0,0,1]
	v_pk_mul_f32 v[2:3], v[10:11], v[112:113] op_sel_hi:[1,0]
	s_waitcnt lgkmcnt(0)
	v_pk_fma_f32 v[10:11], v[88:89], v[4:5], v[92:93]
	v_pk_fma_f32 v[12:13], v[86:87], v[2:3], v[90:91]
	v_pk_mul_f32 v[6:7], v[104:105], v[112:113] op_sel_hi:[1,0]
	v_med3_f32 v2, v12, s33, v226
	v_med3_f32 v3, v13, s33, v226
	v_cvt_pk_fp8_f32 v95, v2, v3
	v_med3_f32 v2, v10, s33, v226
	v_med3_f32 v3, v11, s33, v226
	v_mov_b32_e32 v96, v183
	v_cvt_pk_fp8_f32 v95, v2, v3 op_sel:[0,0,1]
	ds_read_b128 v[2:5], v99 offset:6144
	ds_read_b128 v[86:89], v99 offset:10240
	v_cvt_pk_bf16_f32 v83, v102, v103
	v_pk_mul_f32 v[104:105], v[102:103], v[112:113] op_sel_hi:[1,0]
	ds_read_b128 v[90:93], v99 offset:7168
	ds_read_b128 v[100:103], v99 offset:11264
	v_mov_b32_e32 v97, v183
	s_waitcnt lgkmcnt(2)
	v_pk_fma_f32 v[8:9], v[6:7], v[2:3], v[86:87]
	v_pk_fma_f32 v[6:7], v[104:105], v[4:5], v[88:89]
	v_med3_f32 v2, v8, s33, v226
	v_med3_f32 v3, v9, s33, v226
	v_cvt_pk_fp8_f32 v96, v2, v3
	v_med3_f32 v2, v6, s33, v226
	v_med3_f32 v3, v7, s33, v226
	v_pk_mul_f32 v[86:87], v[106:107], v[112:113] op_sel_hi:[1,0]
	v_cvt_pk_fp8_f32 v96, v2, v3 op_sel:[0,0,1]
	v_pk_mul_f32 v[2:3], v[108:109], v[112:113] op_sel_hi:[1,0]
	v_cvt_pk_bf16_f32 v84, v108, v109
	s_waitcnt lgkmcnt(0)
	v_pk_fma_f32 v[4:5], v[2:3], v[90:91], v[100:101]
	v_cvt_pk_bf16_f32 v85, v106, v107
	v_med3_f32 v2, v4, s33, v226
	v_med3_f32 v3, v5, s33, v226
	v_cvt_pk_fp8_f32 v97, v2, v3
	v_pk_fma_f32 v[2:3], v[86:87], v[92:93], v[102:103]
	global_store_dwordx4 v[110:111], v[82:85], off offset:16
	v_med3_f32 v86, v2, s33, v226
	v_med3_f32 v87, v3, s33, v226
	v_cvt_pk_fp8_f32 v97, v86, v87 op_sel:[0,0,1]
	v_lshl_add_u64 v[86:87], v[40:41], 0, s[40:41]
	ds_read_b128 v[82:85], v1
	s_mov_b32 s2, 0xc2ce8ed0
	global_store_dwordx4 v[86:87], v[94:97], off
	ds_read_b128 v[86:89], v1 offset:16
	ds_read_b128 v[90:93], v1 offset:32
	ds_read_b128 v[94:97], v1 offset:48
	s_waitcnt lgkmcnt(3)
	v_pk_fma_f32 v[100:101], v[66:67], v[82:83], 0 op_sel_hi:[0,1,0]
	v_pk_fma_f32 v[102:103], v[66:67], v[84:85], 0 op_sel_hi:[0,1,0]
	s_waitcnt lgkmcnt(2)
	v_pk_fma_f32 v[104:105], v[66:67], v[86:87], 0 op_sel_hi:[0,1,0]
	v_pk_fma_f32 v[106:107], v[66:67], v[88:89], 0 op_sel_hi:[0,1,0]
	s_waitcnt lgkmcnt(1)
	v_pk_fma_f32 v[108:109], v[66:67], v[90:91], 0 op_sel_hi:[0,1,0]
	v_pk_fma_f32 v[110:111], v[66:67], v[92:93], 0 op_sel_hi:[0,1,0]
	s_waitcnt lgkmcnt(0)
	v_pk_fma_f32 v[112:113], v[66:67], v[94:95], 0 op_sel_hi:[0,1,0]
	v_pk_fma_f32 v[114:115], v[66:67], v[96:97], 0 op_sel_hi:[0,1,0]
	v_pk_fma_f32 v[116:117], v[74:75], v[82:83], 0 op_sel_hi:[0,1,0]
	v_pk_fma_f32 v[118:119], v[74:75], v[84:85], 0 op_sel_hi:[0,1,0]
	v_pk_fma_f32 v[120:121], v[74:75], v[86:87], 0 op_sel_hi:[0,1,0]
	v_pk_fma_f32 v[122:123], v[74:75], v[88:89], 0 op_sel_hi:[0,1,0]
	v_pk_fma_f32 v[124:125], v[74:75], v[90:91], 0 op_sel_hi:[0,1,0]
	v_pk_fma_f32 v[126:127], v[74:75], v[92:93], 0 op_sel_hi:[0,1,0]
	v_pk_fma_f32 v[128:129], v[74:75], v[94:95], 0 op_sel_hi:[0,1,0]
	v_pk_fma_f32 v[130:131], v[74:75], v[96:97], 0 op_sel_hi:[0,1,0]
	v_pk_fma_f32 v[132:133], v[80:81], v[82:83], 0 op_sel_hi:[0,1,0]
	v_pk_fma_f32 v[134:135], v[80:81], v[84:85], 0 op_sel_hi:[0,1,0]
	v_pk_fma_f32 v[136:137], v[80:81], v[86:87], 0 op_sel_hi:[0,1,0]
	v_pk_fma_f32 v[138:139], v[80:81], v[88:89], 0 op_sel_hi:[0,1,0]
	v_pk_fma_f32 v[140:141], v[80:81], v[90:91], 0 op_sel_hi:[0,1,0]
	v_pk_fma_f32 v[142:143], v[80:81], v[92:93], 0 op_sel_hi:[0,1,0]
	v_pk_fma_f32 v[144:145], v[80:81], v[94:95], 0 op_sel_hi:[0,1,0]
	v_pk_fma_f32 v[146:147], v[80:81], v[96:97], 0 op_sel_hi:[0,1,0]
	v_pk_fma_f32 v[148:149], v[16:17], v[82:83], 0 op_sel_hi:[0,1,0]
	v_pk_fma_f32 v[150:151], v[16:17], v[84:85], 0 op_sel_hi:[0,1,0]
	v_pk_fma_f32 v[152:153], v[16:17], v[86:87], 0 op_sel_hi:[0,1,0]
	v_pk_fma_f32 v[154:155], v[16:17], v[88:89], 0 op_sel_hi:[0,1,0]
	v_pk_fma_f32 v[156:157], v[16:17], v[90:91], 0 op_sel_hi:[0,1,0]
	v_pk_fma_f32 v[158:159], v[16:17], v[92:93], 0 op_sel_hi:[0,1,0]
	v_pk_fma_f32 v[160:161], v[16:17], v[94:95], 0 op_sel_hi:[0,1,0]
	v_pk_fma_f32 v[162:163], v[16:17], v[96:97], 0 op_sel_hi:[0,1,0]
	ds_read_b128 v[82:85], v1 offset:64
	ds_read_b128 v[86:89], v1 offset:80
	ds_read_b128 v[90:93], v1 offset:96
	ds_read_b128 v[94:97], v1 offset:112
	s_waitcnt lgkmcnt(3)
	v_pk_fma_f32 v[100:101], v[66:67], v[82:83], v[100:101] op_sel:[1,0,0]
	v_pk_fma_f32 v[102:103], v[66:67], v[84:85], v[102:103] op_sel:[1,0,0]
	s_waitcnt lgkmcnt(2)
	v_pk_fma_f32 v[104:105], v[66:67], v[86:87], v[104:105] op_sel:[1,0,0]
	v_pk_fma_f32 v[106:107], v[66:67], v[88:89], v[106:107] op_sel:[1,0,0]
	s_waitcnt lgkmcnt(1)
	v_pk_fma_f32 v[108:109], v[66:67], v[90:91], v[108:109] op_sel:[1,0,0]
	v_pk_fma_f32 v[110:111], v[66:67], v[92:93], v[110:111] op_sel:[1,0,0]
	s_waitcnt lgkmcnt(0)
; #define LAS __attribute__((address_space(3)))
; __device__ __forceinline__ void phase_post_mix(Frame& F, int l) {
;     ...
;         for (int j = 0; j < 4; ++j) { const LAS float* wg = rws + (lane + 64 * j) * 68;
; #pragma unroll
;             for (int i = 0; i < 4; ++i) { const f32x4 w0 = *(const LAS f32x4*)(wg + 16 * i), w1 = *(const LAS f32x4*)(wg + 16 * i + 4), w2 = *(const LAS f32x4*)(wg + 16 * i + 8), w3 = *(const LAS f32x4*)(wg + 16 * i + 12);
;                 const r_f32x2 wv[8] = {{w0[0], w0[1]}, {w0[2], w0[3]}, {w1[0], w1[1]}, {w1[2], w1[3]}, {w2[0], w2[1]}, {w2[2], w2[3]}, {w3[0], w3[1]}, {w3[2], w3[3]}};
; #pragma unroll
;                 for (int q = 0; q < 4; ++q) { const float h = xx[q][j][i]; const r_f32x2 hh = {h, h};
; #pragma unroll
;                     for (int e = 0; e < 8; ++e) lg2[q][e] = __builtin_elementwise_fma(hh, wv[e], lg2[q][e]); }
; #pragma unroll
;                 for (int q = 0; q < 4; ++q)
;                     asm volatile("" : "+v"(lg2[q][0]), "+v"(lg2[q][1]), "+v"(lg2[q][2]), "+v"(lg2[q][3]), "+v"(lg2[q][4]), "+v"(lg2[q][5]), "+v"(lg2[q][6]), "+v"(lg2[q][7]));
;                 } }
	v_pk_fma_f32 v[112:113], v[66:67], v[94:95], v[112:113] op_sel:[1,0,0]
	v_pk_fma_f32 v[66:67], v[66:67], v[96:97], v[114:115] op_sel:[1,0,0]
	v_pk_fma_f32 v[114:115], v[74:75], v[82:83], v[116:117] op_sel:[1,0,0]
	v_pk_fma_f32 v[116:117], v[74:75], v[84:85], v[118:119] op_sel:[1,0,0]
	v_pk_fma_f32 v[118:119], v[74:75], v[86:87], v[120:121] op_sel:[1,0,0]
	v_pk_fma_f32 v[120:121], v[74:75], v[88:89], v[122:123] op_sel:[1,0,0]
	v_pk_fma_f32 v[122:123], v[74:75], v[90:91], v[124:125] op_sel:[1,0,0]
	v_pk_fma_f32 v[124:125], v[74:75], v[92:93], v[126:127] op_sel:[1,0,0]
	v_pk_fma_f32 v[126:127], v[74:75], v[94:95], v[128:129] op_sel:[1,0,0]
	v_pk_fma_f32 v[74:75], v[74:75], v[96:97], v[130:131] op_sel:[1,0,0]
	v_pk_fma_f32 v[128:129], v[80:81], v[82:83], v[132:133] op_sel:[1,0,0]
	v_pk_fma_f32 v[130:131], v[80:81], v[84:85], v[134:135] op_sel:[1,0,0]
	v_pk_fma_f32 v[132:133], v[80:81], v[86:87], v[136:137] op_sel:[1,0,0]
	v_pk_fma_f32 v[134:135], v[80:81], v[88:89], v[138:139] op_sel:[1,0,0]
	v_pk_fma_f32 v[136:137], v[80:81], v[90:91], v[140:141] op_sel:[1,0,0]
	v_pk_fma_f32 v[138:139], v[80:81], v[92:93], v[142:143] op_sel:[1,0,0]
	v_pk_fma_f32 v[140:141], v[80:81], v[94:95], v[144:145] op_sel:[1,0,0]
	v_pk_fma_f32 v[142:143], v[80:81], v[96:97], v[146:147] op_sel:[1,0,0]
	v_pk_fma_f32 v[144:145], v[16:17], v[82:83], v[148:149] op_sel:[1,0,0]
	v_pk_fma_f32 v[146:147], v[16:17], v[84:85], v[150:151] op_sel:[1,0,0]
	v_pk_fma_f32 v[148:149], v[16:17], v[86:87], v[152:153] op_sel:[1,0,0]
	v_pk_fma_f32 v[150:151], v[16:17], v[88:89], v[154:155] op_sel:[1,0,0]
	v_pk_fma_f32 v[152:153], v[16:17], v[90:91], v[156:157] op_sel:[1,0,0]
	v_pk_fma_f32 v[154:155], v[16:17], v[92:93], v[158:159] op_sel:[1,0,0]
	v_pk_fma_f32 v[156:157], v[16:17], v[94:95], v[160:161] op_sel:[1,0,0]
	v_pk_fma_f32 v[16:17], v[16:17], v[96:97], v[162:163] op_sel:[1,0,0]
	s_nop 0
	ds_read_b128 v[80:83], v1 offset:128
	ds_read_b128 v[84:87], v1 offset:144
	ds_read_b128 v[88:91], v1 offset:160
	ds_read_b128 v[92:95], v1 offset:176
	s_waitcnt lgkmcnt(3)
	v_pk_fma_f32 v[96:97], v[60:61], v[80:81], v[100:101] op_sel_hi:[0,1,1]
	v_pk_fma_f32 v[100:101], v[60:61], v[82:83], v[102:103] op_sel_hi:[0,1,1]
	s_waitcnt lgkmcnt(2)
	v_pk_fma_f32 v[102:103], v[60:61], v[84:85], v[104:105] op_sel_hi:[0,1,1]
	v_pk_fma_f32 v[104:105], v[60:61], v[86:87], v[106:107] op_sel_hi:[0,1,1]
	s_waitcnt lgkmcnt(1)
	v_pk_fma_f32 v[106:107], v[60:61], v[88:89], v[108:109] op_sel_hi:[0,1,1]
	v_pk_fma_f32 v[108:109], v[60:61], v[90:91], v[110:111] op_sel_hi:[0,1,1]
	s_waitcnt lgkmcnt(0)
	v_pk_fma_f32 v[110:111], v[60:61], v[92:93], v[112:113] op_sel_hi:[0,1,1]
	v_pk_fma_f32 v[66:67], v[60:61], v[94:95], v[66:67] op_sel_hi:[0,1,1]
	v_pk_fma_f32 v[112:113], v[70:71], v[80:81], v[114:115] op_sel_hi:[0,1,1]
	v_pk_fma_f32 v[114:115], v[70:71], v[82:83], v[116:117] op_sel_hi:[0,1,1]
	v_pk_fma_f32 v[116:117], v[70:71], v[84:85], v[118:119] op_sel_hi:[0,1,1]
	v_pk_fma_f32 v[118:119], v[70:71], v[86:87], v[120:121] op_sel_hi:[0,1,1]
	v_pk_fma_f32 v[120:121], v[70:71], v[88:89], v[122:123] op_sel_hi:[0,1,1]
	v_pk_fma_f32 v[122:123], v[70:71], v[90:91], v[124:125] op_sel_hi:[0,1,1]
	v_pk_fma_f32 v[124:125], v[70:71], v[92:93], v[126:127] op_sel_hi:[0,1,1]
	v_pk_fma_f32 v[74:75], v[70:71], v[94:95], v[74:75] op_sel_hi:[0,1,1]
	v_pk_fma_f32 v[126:127], v[78:79], v[80:81], v[128:129] op_sel_hi:[0,1,1]
	v_pk_fma_f32 v[128:129], v[78:79], v[82:83], v[130:131] op_sel_hi:[0,1,1]
	v_pk_fma_f32 v[130:131], v[78:79], v[84:85], v[132:133] op_sel_hi:[0,1,1]
	v_pk_fma_f32 v[132:133], v[78:79], v[86:87], v[134:135] op_sel_hi:[0,1,1]
	v_pk_fma_f32 v[134:135], v[78:79], v[88:89], v[136:137] op_sel_hi:[0,1,1]
	v_pk_fma_f32 v[136:137], v[78:79], v[90:91], v[138:139] op_sel_hi:[0,1,1]
	v_pk_fma_f32 v[138:139], v[78:79], v[92:93], v[140:141] op_sel_hi:[0,1,1]
	v_pk_fma_f32 v[140:141], v[78:79], v[94:95], v[142:143] op_sel_hi:[0,1,1]
	v_pk_fma_f32 v[142:143], v[14:15], v[80:81], v[144:145] op_sel_hi:[0,1,1]
	v_pk_fma_f32 v[144:145], v[14:15], v[82:83], v[146:147] op_sel_hi:[0,1,1]
	v_pk_fma_f32 v[146:147], v[14:15], v[84:85], v[148:149] op_sel_hi:[0,1,1]
	v_pk_fma_f32 v[148:149], v[14:15], v[86:87], v[150:151] op_sel_hi:[0,1,1]
	v_pk_fma_f32 v[150:151], v[14:15], v[88:89], v[152:153] op_sel_hi:[0,1,1]
	v_pk_fma_f32 v[152:153], v[14:15], v[90:91], v[154:155] op_sel_hi:[0,1,1]
	v_pk_fma_f32 v[154:155], v[14:15], v[92:93], v[156:157] op_sel_hi:[0,1,1]
	v_pk_fma_f32 v[16:17], v[14:15], v[94:95], v[16:17] op_sel_hi:[0,1,1]
	ds_read_b128 v[80:83], v1 offset:192
	ds_read_b128 v[84:87], v1 offset:208
	ds_read_b128 v[88:91], v1 offset:224
	ds_read_b128 v[92:95], v1 offset:240
	s_waitcnt lgkmcnt(3)
	v_pk_fma_f32 v[96:97], v[60:61], v[80:81], v[96:97] op_sel:[1,0,0]
	v_pk_fma_f32 v[100:101], v[60:61], v[82:83], v[100:101] op_sel:[1,0,0]
	s_waitcnt lgkmcnt(2)
	v_pk_fma_f32 v[102:103], v[60:61], v[84:85], v[102:103] op_sel:[1,0,0]
	v_pk_fma_f32 v[104:105], v[60:61], v[86:87], v[104:105] op_sel:[1,0,0]
	s_waitcnt lgkmcnt(1)
	v_pk_fma_f32 v[106:107], v[60:61], v[88:89], v[106:107] op_sel:[1,0,0]
	v_pk_fma_f32 v[108:109], v[60:61], v[90:91], v[108:109] op_sel:[1,0,0]
	s_waitcnt lgkmcnt(0)
; #define LAS __attribute__((address_space(3)))
; __device__ __forceinline__ void phase_post_mix(Frame& F, int l) {
;     ...
;         for (int j = 0; j < 4; ++j) { const LAS float* wg = rws + (lane + 64 * j) * 68;
; #pragma unroll
;             for (int i = 0; i < 4; ++i) { const f32x4 w0 = *(const LAS f32x4*)(wg + 16 * i), w1 = *(const LAS f32x4*)(wg + 16 * i + 4), w2 = *(const LAS f32x4*)(wg + 16 * i + 8), w3 = *(const LAS f32x4*)(wg + 16 * i + 12);
;                 const r_f32x2 wv[8] = {{w0[0], w0[1]}, {w0[2], w0[3]}, {w1[0], w1[1]}, {w1[2], w1[3]}, {w2[0], w2[1]}, {w2[2], w2[3]}, {w3[0], w3[1]}, {w3[2], w3[3]}};
; #pragma unroll
;                 for (int q = 0; q < 4; ++q) { const float h = xx[q][j][i]; const r_f32x2 hh = {h, h};
; #pragma unroll
;                     for (int e = 0; e < 8; ++e) lg2[q][e] = __builtin_elementwise_fma(hh, wv[e], lg2[q][e]); }
; #pragma unroll
;                 for (int q = 0; q < 4; ++q)
;                     asm volatile("" : "+v"(lg2[q][0]), "+v"(lg2[q][1]), "+v"(lg2[q][2]), "+v"(lg2[q][3]), "+v"(lg2[q][4]), "+v"(lg2[q][5]), "+v"(lg2[q][6]), "+v"(lg2[q][7]));
;                 } }
	v_pk_fma_f32 v[110:111], v[60:61], v[92:93], v[110:111] op_sel:[1,0,0]
	v_pk_fma_f32 v[60:61], v[60:61], v[94:95], v[66:67] op_sel:[1,0,0]
	v_pk_fma_f32 v[66:67], v[70:71], v[80:81], v[112:113] op_sel:[1,0,0]
	v_pk_fma_f32 v[112:113], v[70:71], v[82:83], v[114:115] op_sel:[1,0,0]
	v_pk_fma_f32 v[114:115], v[70:71], v[84:85], v[116:117] op_sel:[1,0,0]
	v_pk_fma_f32 v[116:117], v[70:71], v[86:87], v[118:119] op_sel:[1,0,0]
	v_pk_fma_f32 v[118:119], v[70:71], v[88:89], v[120:121] op_sel:[1,0,0]
	v_pk_fma_f32 v[120:121], v[70:71], v[90:91], v[122:123] op_sel:[1,0,0]
	v_pk_fma_f32 v[122:123], v[70:71], v[92:93], v[124:125] op_sel:[1,0,0]
	v_pk_fma_f32 v[70:71], v[70:71], v[94:95], v[74:75] op_sel:[1,0,0]
	v_pk_fma_f32 v[74:75], v[78:79], v[80:81], v[126:127] op_sel:[1,0,0]
	v_pk_fma_f32 v[124:125], v[78:79], v[82:83], v[128:129] op_sel:[1,0,0]
	v_pk_fma_f32 v[126:127], v[78:79], v[84:85], v[130:131] op_sel:[1,0,0]
	v_pk_fma_f32 v[128:129], v[78:79], v[86:87], v[132:133] op_sel:[1,0,0]
	v_pk_fma_f32 v[130:131], v[78:79], v[88:89], v[134:135] op_sel:[1,0,0]
	v_pk_fma_f32 v[132:133], v[78:79], v[90:91], v[136:137] op_sel:[1,0,0]
	v_pk_fma_f32 v[134:135], v[78:79], v[92:93], v[138:139] op_sel:[1,0,0]
	v_pk_fma_f32 v[136:137], v[78:79], v[94:95], v[140:141] op_sel:[1,0,0]
	v_pk_fma_f32 v[138:139], v[14:15], v[80:81], v[142:143] op_sel:[1,0,0]
	v_pk_fma_f32 v[140:141], v[14:15], v[82:83], v[144:145] op_sel:[1,0,0]
	v_pk_fma_f32 v[142:143], v[14:15], v[84:85], v[146:147] op_sel:[1,0,0]
	v_pk_fma_f32 v[144:145], v[14:15], v[86:87], v[148:149] op_sel:[1,0,0]
	v_pk_fma_f32 v[146:147], v[14:15], v[88:89], v[150:151] op_sel:[1,0,0]
	v_pk_fma_f32 v[90:91], v[14:15], v[90:91], v[152:153] op_sel:[1,0,0]
	v_pk_fma_f32 v[92:93], v[14:15], v[92:93], v[154:155] op_sel:[1,0,0]
	v_pk_fma_f32 v[94:95], v[14:15], v[94:95], v[16:17] op_sel:[1,0,0]
	s_nop 0
	ds_read_b128 v[14:17], v1 offset:17408
	ds_read_b128 v[78:81], v1 offset:17424
	ds_read_b128 v[82:85], v1 offset:17440
	ds_read_b128 v[86:89], v1 offset:17456
	s_waitcnt lgkmcnt(3)
	v_pk_fma_f32 v[96:97], v[54:55], v[14:15], v[96:97] op_sel_hi:[0,1,1]
	v_pk_fma_f32 v[100:101], v[54:55], v[16:17], v[100:101] op_sel_hi:[0,1,1]
	s_waitcnt lgkmcnt(2)
	v_pk_fma_f32 v[102:103], v[54:55], v[78:79], v[102:103] op_sel_hi:[0,1,1]
	v_pk_fma_f32 v[104:105], v[54:55], v[80:81], v[104:105] op_sel_hi:[0,1,1]
	s_waitcnt lgkmcnt(1)
	v_pk_fma_f32 v[106:107], v[54:55], v[82:83], v[106:107] op_sel_hi:[0,1,1]
	v_pk_fma_f32 v[108:109], v[54:55], v[84:85], v[108:109] op_sel_hi:[0,1,1]
	s_waitcnt lgkmcnt(0)
	v_pk_fma_f32 v[110:111], v[54:55], v[86:87], v[110:111] op_sel_hi:[0,1,1]
	v_pk_fma_f32 v[60:61], v[54:55], v[88:89], v[60:61] op_sel_hi:[0,1,1]
	v_pk_fma_f32 v[66:67], v[64:65], v[14:15], v[66:67] op_sel_hi:[0,1,1]
	v_pk_fma_f32 v[112:113], v[64:65], v[16:17], v[112:113] op_sel_hi:[0,1,1]
	v_pk_fma_f32 v[114:115], v[64:65], v[78:79], v[114:115] op_sel_hi:[0,1,1]
	v_pk_fma_f32 v[116:117], v[64:65], v[80:81], v[116:117] op_sel_hi:[0,1,1]
	v_pk_fma_f32 v[118:119], v[64:65], v[82:83], v[118:119] op_sel_hi:[0,1,1]
	v_pk_fma_f32 v[120:121], v[64:65], v[84:85], v[120:121] op_sel_hi:[0,1,1]
	v_pk_fma_f32 v[122:123], v[64:65], v[86:87], v[122:123] op_sel_hi:[0,1,1]
	v_pk_fma_f32 v[70:71], v[64:65], v[88:89], v[70:71] op_sel_hi:[0,1,1]
	v_pk_fma_f32 v[74:75], v[76:77], v[14:15], v[74:75] op_sel_hi:[0,1,1]
	v_pk_fma_f32 v[124:125], v[76:77], v[16:17], v[124:125] op_sel_hi:[0,1,1]
	v_pk_fma_f32 v[126:127], v[76:77], v[78:79], v[126:127] op_sel_hi:[0,1,1]
	v_pk_fma_f32 v[128:129], v[76:77], v[80:81], v[128:129] op_sel_hi:[0,1,1]
	v_pk_fma_f32 v[130:131], v[76:77], v[82:83], v[130:131] op_sel_hi:[0,1,1]
	v_pk_fma_f32 v[132:133], v[76:77], v[84:85], v[132:133] op_sel_hi:[0,1,1]
	v_pk_fma_f32 v[134:135], v[76:77], v[86:87], v[134:135] op_sel_hi:[0,1,1]
	v_pk_fma_f32 v[136:137], v[76:77], v[88:89], v[136:137] op_sel_hi:[0,1,1]
	v_pk_fma_f32 v[138:139], v[12:13], v[14:15], v[138:139] op_sel_hi:[0,1,1]
	v_pk_fma_f32 v[140:141], v[12:13], v[16:17], v[140:141] op_sel_hi:[0,1,1]
	v_pk_fma_f32 v[142:143], v[12:13], v[78:79], v[142:143] op_sel_hi:[0,1,1]
	v_pk_fma_f32 v[144:145], v[12:13], v[80:81], v[144:145] op_sel_hi:[0,1,1]
	v_pk_fma_f32 v[146:147], v[12:13], v[82:83], v[146:147] op_sel_hi:[0,1,1]
	v_pk_fma_f32 v[90:91], v[12:13], v[84:85], v[90:91] op_sel_hi:[0,1,1]
	v_pk_fma_f32 v[92:93], v[12:13], v[86:87], v[92:93] op_sel_hi:[0,1,1]
	v_pk_fma_f32 v[94:95], v[12:13], v[88:89], v[94:95] op_sel_hi:[0,1,1]
	ds_read_b128 v[14:17], v1 offset:17472
	ds_read_b128 v[78:81], v1 offset:17488
	ds_read_b128 v[82:85], v1 offset:17504
	ds_read_b128 v[86:89], v1 offset:17520
	s_waitcnt lgkmcnt(3)
	v_pk_fma_f32 v[96:97], v[54:55], v[14:15], v[96:97] op_sel:[1,0,0]
	v_pk_fma_f32 v[100:101], v[54:55], v[16:17], v[100:101] op_sel:[1,0,0]
	s_waitcnt lgkmcnt(2)
	v_pk_fma_f32 v[102:103], v[54:55], v[78:79], v[102:103] op_sel:[1,0,0]
	v_pk_fma_f32 v[104:105], v[54:55], v[80:81], v[104:105] op_sel:[1,0,0]
	s_waitcnt lgkmcnt(1)
	v_pk_fma_f32 v[106:107], v[54:55], v[82:83], v[106:107] op_sel:[1,0,0]
	v_pk_fma_f32 v[108:109], v[54:55], v[84:85], v[108:109] op_sel:[1,0,0]
	s_waitcnt lgkmcnt(0)
; #define LAS __attribute__((address_space(3)))
; __device__ __forceinline__ void phase_post_mix(Frame& F, int l) {
;     ...
;         for (int j = 0; j < 4; ++j) { const LAS float* wg = rws + (lane + 64 * j) * 68;
; #pragma unroll
;             for (int i = 0; i < 4; ++i) { const f32x4 w0 = *(const LAS f32x4*)(wg + 16 * i), w1 = *(const LAS f32x4*)(wg + 16 * i + 4), w2 = *(const LAS f32x4*)(wg + 16 * i + 8), w3 = *(const LAS f32x4*)(wg + 16 * i + 12);
;                 const r_f32x2 wv[8] = {{w0[0], w0[1]}, {w0[2], w0[3]}, {w1[0], w1[1]}, {w1[2], w1[3]}, {w2[0], w2[1]}, {w2[2], w2[3]}, {w3[0], w3[1]}, {w3[2], w3[3]}};
; #pragma unroll
;                 for (int q = 0; q < 4; ++q) { const float h = xx[q][j][i]; const r_f32x2 hh = {h, h};
; #pragma unroll
;                     for (int e = 0; e < 8; ++e) lg2[q][e] = __builtin_elementwise_fma(hh, wv[e], lg2[q][e]); }
; #pragma unroll
;                 for (int q = 0; q < 4; ++q)
;                     asm volatile("" : "+v"(lg2[q][0]), "+v"(lg2[q][1]), "+v"(lg2[q][2]), "+v"(lg2[q][3]), "+v"(lg2[q][4]), "+v"(lg2[q][5]), "+v"(lg2[q][6]), "+v"(lg2[q][7]));
;                 } }
	v_pk_fma_f32 v[110:111], v[54:55], v[86:87], v[110:111] op_sel:[1,0,0]
	v_pk_fma_f32 v[54:55], v[54:55], v[88:89], v[60:61] op_sel:[1,0,0]
	v_pk_fma_f32 v[60:61], v[64:65], v[14:15], v[66:67] op_sel:[1,0,0]
	v_pk_fma_f32 v[112:113], v[64:65], v[16:17], v[112:113] op_sel:[1,0,0]
	v_pk_fma_f32 v[114:115], v[64:65], v[78:79], v[114:115] op_sel:[1,0,0]
	v_pk_fma_f32 v[116:117], v[64:65], v[80:81], v[116:117] op_sel:[1,0,0]
	v_pk_fma_f32 v[118:119], v[64:65], v[82:83], v[118:119] op_sel:[1,0,0]
	v_pk_fma_f32 v[120:121], v[64:65], v[84:85], v[120:121] op_sel:[1,0,0]
	v_pk_fma_f32 v[122:123], v[64:65], v[86:87], v[122:123] op_sel:[1,0,0]
	v_pk_fma_f32 v[70:71], v[64:65], v[88:89], v[70:71] op_sel:[1,0,0]
	v_pk_fma_f32 v[148:149], v[76:77], v[14:15], v[74:75] op_sel:[1,0,0]
	v_pk_fma_f32 v[124:125], v[76:77], v[16:17], v[124:125] op_sel:[1,0,0]
	v_pk_fma_f32 v[126:127], v[76:77], v[78:79], v[126:127] op_sel:[1,0,0]
	v_pk_fma_f32 v[128:129], v[76:77], v[80:81], v[128:129] op_sel:[1,0,0]
	v_pk_fma_f32 v[130:131], v[76:77], v[82:83], v[130:131] op_sel:[1,0,0]
	v_pk_fma_f32 v[132:133], v[76:77], v[84:85], v[132:133] op_sel:[1,0,0]
	v_pk_fma_f32 v[134:135], v[76:77], v[86:87], v[134:135] op_sel:[1,0,0]
	v_pk_fma_f32 v[136:137], v[76:77], v[88:89], v[136:137] op_sel:[1,0,0]
	v_pk_fma_f32 v[138:139], v[12:13], v[14:15], v[138:139] op_sel:[1,0,0]
	v_pk_fma_f32 v[16:17], v[12:13], v[16:17], v[140:141] op_sel:[1,0,0]
	v_pk_fma_f32 v[140:141], v[12:13], v[78:79], v[142:143] op_sel:[1,0,0]
	v_pk_fma_f32 v[142:143], v[12:13], v[80:81], v[144:145] op_sel:[1,0,0]
	v_pk_fma_f32 v[82:83], v[12:13], v[82:83], v[146:147] op_sel:[1,0,0]
	v_pk_fma_f32 v[84:85], v[12:13], v[84:85], v[90:91] op_sel:[1,0,0]
	v_pk_fma_f32 v[86:87], v[12:13], v[86:87], v[92:93] op_sel:[1,0,0]
	v_pk_fma_f32 v[88:89], v[12:13], v[88:89], v[94:95] op_sel:[1,0,0]
	s_nop 0
	ds_read_b128 v[12:15], v1 offset:17536
	ds_read_b128 v[64:67], v1 offset:17552
	ds_read_b128 v[74:77], v1 offset:17568
	ds_read_b128 v[78:81], v1 offset:17584
	s_waitcnt lgkmcnt(3)
	v_pk_fma_f32 v[90:91], v[32:33], v[12:13], v[96:97] op_sel_hi:[0,1,1]
	v_pk_fma_f32 v[92:93], v[32:33], v[14:15], v[100:101] op_sel_hi:[0,1,1]
	s_waitcnt lgkmcnt(2)
	v_pk_fma_f32 v[94:95], v[32:33], v[64:65], v[102:103] op_sel_hi:[0,1,1]
	v_pk_fma_f32 v[96:97], v[32:33], v[66:67], v[104:105] op_sel_hi:[0,1,1]
	s_waitcnt lgkmcnt(1)
	v_pk_fma_f32 v[100:101], v[32:33], v[74:75], v[106:107] op_sel_hi:[0,1,1]
	v_pk_fma_f32 v[102:103], v[32:33], v[76:77], v[108:109] op_sel_hi:[0,1,1]
	s_waitcnt lgkmcnt(0)
	v_pk_fma_f32 v[104:105], v[32:33], v[78:79], v[110:111] op_sel_hi:[0,1,1]
	v_pk_fma_f32 v[54:55], v[32:33], v[80:81], v[54:55] op_sel_hi:[0,1,1]
	v_pk_fma_f32 v[60:61], v[58:59], v[12:13], v[60:61] op_sel_hi:[0,1,1]
	v_pk_fma_f32 v[106:107], v[58:59], v[14:15], v[112:113] op_sel_hi:[0,1,1]
	v_pk_fma_f32 v[108:109], v[58:59], v[64:65], v[114:115] op_sel_hi:[0,1,1]
	v_pk_fma_f32 v[110:111], v[58:59], v[66:67], v[116:117] op_sel_hi:[0,1,1]
	v_pk_fma_f32 v[112:113], v[58:59], v[74:75], v[118:119] op_sel_hi:[0,1,1]
	v_pk_fma_f32 v[114:115], v[58:59], v[76:77], v[120:121] op_sel_hi:[0,1,1]
	v_pk_fma_f32 v[116:117], v[58:59], v[78:79], v[122:123] op_sel_hi:[0,1,1]
	v_pk_fma_f32 v[70:71], v[58:59], v[80:81], v[70:71] op_sel_hi:[0,1,1]
	v_pk_fma_f32 v[118:119], v[72:73], v[12:13], v[148:149] op_sel_hi:[0,1,1]
	v_pk_fma_f32 v[120:121], v[72:73], v[14:15], v[124:125] op_sel_hi:[0,1,1]
	v_pk_fma_f32 v[122:123], v[72:73], v[64:65], v[126:127] op_sel_hi:[0,1,1]
	v_pk_fma_f32 v[124:125], v[72:73], v[66:67], v[128:129] op_sel_hi:[0,1,1]
	v_pk_fma_f32 v[126:127], v[72:73], v[74:75], v[130:131] op_sel_hi:[0,1,1]
	v_pk_fma_f32 v[128:129], v[72:73], v[76:77], v[132:133] op_sel_hi:[0,1,1]
	v_pk_fma_f32 v[130:131], v[72:73], v[78:79], v[134:135] op_sel_hi:[0,1,1]
	v_pk_fma_f32 v[132:133], v[72:73], v[80:81], v[136:137] op_sel_hi:[0,1,1]
	v_pk_fma_f32 v[134:135], v[10:11], v[12:13], v[138:139] op_sel_hi:[0,1,1]
	v_pk_fma_f32 v[16:17], v[10:11], v[14:15], v[16:17] op_sel_hi:[0,1,1]
	v_pk_fma_f32 v[136:137], v[10:11], v[64:65], v[140:141] op_sel_hi:[0,1,1]
	v_pk_fma_f32 v[138:139], v[10:11], v[66:67], v[142:143] op_sel_hi:[0,1,1]
	v_pk_fma_f32 v[82:83], v[10:11], v[74:75], v[82:83] op_sel_hi:[0,1,1]
	v_pk_fma_f32 v[84:85], v[10:11], v[76:77], v[84:85] op_sel_hi:[0,1,1]
	v_pk_fma_f32 v[86:87], v[10:11], v[78:79], v[86:87] op_sel_hi:[0,1,1]
	v_pk_fma_f32 v[88:89], v[10:11], v[80:81], v[88:89] op_sel_hi:[0,1,1]
	ds_read_b128 v[12:15], v1 offset:17600
	ds_read_b128 v[64:67], v1 offset:17616
	ds_read_b128 v[74:77], v1 offset:17632
	ds_read_b128 v[78:81], v1 offset:17648
	s_waitcnt lgkmcnt(3)
	v_pk_fma_f32 v[90:91], v[32:33], v[12:13], v[90:91] op_sel:[1,0,0]
	v_pk_fma_f32 v[92:93], v[32:33], v[14:15], v[92:93] op_sel:[1,0,0]
	s_waitcnt lgkmcnt(2)
	v_pk_fma_f32 v[94:95], v[32:33], v[64:65], v[94:95] op_sel:[1,0,0]
	v_pk_fma_f32 v[96:97], v[32:33], v[66:67], v[96:97] op_sel:[1,0,0]
	s_waitcnt lgkmcnt(1)
	v_pk_fma_f32 v[100:101], v[32:33], v[74:75], v[100:101] op_sel:[1,0,0]
	v_pk_fma_f32 v[102:103], v[32:33], v[76:77], v[102:103] op_sel:[1,0,0]
	s_waitcnt lgkmcnt(0)
; #define LAS __attribute__((address_space(3)))
; __device__ __forceinline__ void phase_post_mix(Frame& F, int l) {
;     ...
;         for (int j = 0; j < 4; ++j) { const LAS float* wg = rws + (lane + 64 * j) * 68;
; #pragma unroll
;             for (int i = 0; i < 4; ++i) { const f32x4 w0 = *(const LAS f32x4*)(wg + 16 * i), w1 = *(const LAS f32x4*)(wg + 16 * i + 4), w2 = *(const LAS f32x4*)(wg + 16 * i + 8), w3 = *(const LAS f32x4*)(wg + 16 * i + 12);
;                 const r_f32x2 wv[8] = {{w0[0], w0[1]}, {w0[2], w0[3]}, {w1[0], w1[1]}, {w1[2], w1[3]}, {w2[0], w2[1]}, {w2[2], w2[3]}, {w3[0], w3[1]}, {w3[2], w3[3]}};
; #pragma unroll
;                 for (int q = 0; q < 4; ++q) { const float h = xx[q][j][i]; const r_f32x2 hh = {h, h};
; #pragma unroll
;                     for (int e = 0; e < 8; ++e) lg2[q][e] = __builtin_elementwise_fma(hh, wv[e], lg2[q][e]); }
; #pragma unroll
;                 for (int q = 0; q < 4; ++q)
;                     asm volatile("" : "+v"(lg2[q][0]), "+v"(lg2[q][1]), "+v"(lg2[q][2]), "+v"(lg2[q][3]), "+v"(lg2[q][4]), "+v"(lg2[q][5]), "+v"(lg2[q][6]), "+v"(lg2[q][7]));
;                 } }
	v_pk_fma_f32 v[104:105], v[32:33], v[78:79], v[104:105] op_sel:[1,0,0]
	v_pk_fma_f32 v[32:33], v[32:33], v[80:81], v[54:55] op_sel:[1,0,0]
	v_pk_fma_f32 v[54:55], v[58:59], v[12:13], v[60:61] op_sel:[1,0,0]
	v_pk_fma_f32 v[106:107], v[58:59], v[14:15], v[106:107] op_sel:[1,0,0]
	v_pk_fma_f32 v[108:109], v[58:59], v[64:65], v[108:109] op_sel:[1,0,0]
	v_pk_fma_f32 v[110:111], v[58:59], v[66:67], v[110:111] op_sel:[1,0,0]
	v_pk_fma_f32 v[112:113], v[58:59], v[74:75], v[112:113] op_sel:[1,0,0]
	v_pk_fma_f32 v[114:115], v[58:59], v[76:77], v[114:115] op_sel:[1,0,0]
	v_pk_fma_f32 v[116:117], v[58:59], v[78:79], v[116:117] op_sel:[1,0,0]
	v_pk_fma_f32 v[70:71], v[58:59], v[80:81], v[70:71] op_sel:[1,0,0]
	v_pk_fma_f32 v[118:119], v[72:73], v[12:13], v[118:119] op_sel:[1,0,0]
	v_pk_fma_f32 v[120:121], v[72:73], v[14:15], v[120:121] op_sel:[1,0,0]
	v_pk_fma_f32 v[122:123], v[72:73], v[64:65], v[122:123] op_sel:[1,0,0]
	v_pk_fma_f32 v[124:125], v[72:73], v[66:67], v[124:125] op_sel:[1,0,0]
	v_pk_fma_f32 v[126:127], v[72:73], v[74:75], v[126:127] op_sel:[1,0,0]
	v_pk_fma_f32 v[128:129], v[72:73], v[76:77], v[128:129] op_sel:[1,0,0]
	v_pk_fma_f32 v[130:131], v[72:73], v[78:79], v[130:131] op_sel:[1,0,0]
	v_pk_fma_f32 v[72:73], v[72:73], v[80:81], v[132:133] op_sel:[1,0,0]
	v_pk_fma_f32 v[132:133], v[10:11], v[12:13], v[134:135] op_sel:[1,0,0]
	v_pk_fma_f32 v[134:135], v[10:11], v[14:15], v[16:17] op_sel:[1,0,0]
	v_pk_fma_f32 v[136:137], v[10:11], v[64:65], v[136:137] op_sel:[1,0,0]
	v_pk_fma_f32 v[138:139], v[10:11], v[66:67], v[138:139] op_sel:[1,0,0]
	v_pk_fma_f32 v[74:75], v[10:11], v[74:75], v[82:83] op_sel:[1,0,0]
	v_pk_fma_f32 v[76:77], v[10:11], v[76:77], v[84:85] op_sel:[1,0,0]
	v_pk_fma_f32 v[78:79], v[10:11], v[78:79], v[86:87] op_sel:[1,0,0]
	v_pk_fma_f32 v[80:81], v[10:11], v[80:81], v[88:89] op_sel:[1,0,0]
	s_nop 0
	ds_read_b128 v[10:13], v1 offset:34816
	ds_read_b128 v[14:17], v1 offset:34832
	ds_read_b128 v[58:61], v1 offset:34848
	ds_read_b128 v[64:67], v1 offset:34864
	s_waitcnt lgkmcnt(3)
	v_pk_fma_f32 v[82:83], v[28:29], v[10:11], v[90:91] op_sel_hi:[0,1,1]
	v_pk_fma_f32 v[84:85], v[28:29], v[12:13], v[92:93] op_sel_hi:[0,1,1]
	s_waitcnt lgkmcnt(2)
	v_pk_fma_f32 v[86:87], v[28:29], v[14:15], v[94:95] op_sel_hi:[0,1,1]
	v_pk_fma_f32 v[88:89], v[28:29], v[16:17], v[96:97] op_sel_hi:[0,1,1]
	s_waitcnt lgkmcnt(1)
	v_pk_fma_f32 v[90:91], v[28:29], v[58:59], v[100:101] op_sel_hi:[0,1,1]
	v_pk_fma_f32 v[92:93], v[28:29], v[60:61], v[102:103] op_sel_hi:[0,1,1]
	s_waitcnt lgkmcnt(0)
	v_pk_fma_f32 v[94:95], v[28:29], v[64:65], v[104:105] op_sel_hi:[0,1,1]
	v_pk_fma_f32 v[32:33], v[28:29], v[66:67], v[32:33] op_sel_hi:[0,1,1]
	v_pk_fma_f32 v[54:55], v[52:53], v[10:11], v[54:55] op_sel_hi:[0,1,1]
	v_pk_fma_f32 v[96:97], v[52:53], v[12:13], v[106:107] op_sel_hi:[0,1,1]
	v_pk_fma_f32 v[100:101], v[52:53], v[14:15], v[108:109] op_sel_hi:[0,1,1]
	v_pk_fma_f32 v[102:103], v[52:53], v[16:17], v[110:111] op_sel_hi:[0,1,1]
	v_pk_fma_f32 v[104:105], v[52:53], v[58:59], v[112:113] op_sel_hi:[0,1,1]
	v_pk_fma_f32 v[106:107], v[52:53], v[60:61], v[114:115] op_sel_hi:[0,1,1]
	v_pk_fma_f32 v[108:109], v[52:53], v[64:65], v[116:117] op_sel_hi:[0,1,1]
	v_pk_fma_f32 v[70:71], v[52:53], v[66:67], v[70:71] op_sel_hi:[0,1,1]
	v_pk_fma_f32 v[110:111], v[68:69], v[10:11], v[118:119] op_sel_hi:[0,1,1]
	v_pk_fma_f32 v[112:113], v[68:69], v[12:13], v[120:121] op_sel_hi:[0,1,1]
	v_pk_fma_f32 v[114:115], v[68:69], v[14:15], v[122:123] op_sel_hi:[0,1,1]
	v_pk_fma_f32 v[116:117], v[68:69], v[16:17], v[124:125] op_sel_hi:[0,1,1]
	v_pk_fma_f32 v[118:119], v[68:69], v[58:59], v[126:127] op_sel_hi:[0,1,1]
	v_pk_fma_f32 v[120:121], v[68:69], v[60:61], v[128:129] op_sel_hi:[0,1,1]
	v_pk_fma_f32 v[122:123], v[68:69], v[64:65], v[130:131] op_sel_hi:[0,1,1]
	v_pk_fma_f32 v[72:73], v[68:69], v[66:67], v[72:73] op_sel_hi:[0,1,1]
	v_pk_fma_f32 v[124:125], v[8:9], v[10:11], v[132:133] op_sel_hi:[0,1,1]
	v_pk_fma_f32 v[126:127], v[8:9], v[12:13], v[134:135] op_sel_hi:[0,1,1]
	v_pk_fma_f32 v[128:129], v[8:9], v[14:15], v[136:137] op_sel_hi:[0,1,1]
	v_pk_fma_f32 v[130:131], v[8:9], v[16:17], v[138:139] op_sel_hi:[0,1,1]
	v_pk_fma_f32 v[74:75], v[8:9], v[58:59], v[74:75] op_sel_hi:[0,1,1]
	v_pk_fma_f32 v[76:77], v[8:9], v[60:61], v[76:77] op_sel_hi:[0,1,1]
	v_pk_fma_f32 v[78:79], v[8:9], v[64:65], v[78:79] op_sel_hi:[0,1,1]
	v_pk_fma_f32 v[80:81], v[8:9], v[66:67], v[80:81] op_sel_hi:[0,1,1]
	ds_read_b128 v[10:13], v1 offset:34880
	ds_read_b128 v[14:17], v1 offset:34896
	ds_read_b128 v[58:61], v1 offset:34912
	ds_read_b128 v[64:67], v1 offset:34928
	s_waitcnt lgkmcnt(3)
	v_pk_fma_f32 v[82:83], v[28:29], v[10:11], v[82:83] op_sel:[1,0,0]
	v_pk_fma_f32 v[84:85], v[28:29], v[12:13], v[84:85] op_sel:[1,0,0]
	s_waitcnt lgkmcnt(2)
	v_pk_fma_f32 v[86:87], v[28:29], v[14:15], v[86:87] op_sel:[1,0,0]
	v_pk_fma_f32 v[88:89], v[28:29], v[16:17], v[88:89] op_sel:[1,0,0]
	s_waitcnt lgkmcnt(1)
	v_pk_fma_f32 v[90:91], v[28:29], v[58:59], v[90:91] op_sel:[1,0,0]
	v_pk_fma_f32 v[92:93], v[28:29], v[60:61], v[92:93] op_sel:[1,0,0]
	s_waitcnt lgkmcnt(0)
; #define LAS __attribute__((address_space(3)))
; __device__ __forceinline__ void phase_post_mix(Frame& F, int l) {
;     ...
;         for (int j = 0; j < 4; ++j) { const LAS float* wg = rws + (lane + 64 * j) * 68;
; #pragma unroll
;             for (int i = 0; i < 4; ++i) { const f32x4 w0 = *(const LAS f32x4*)(wg + 16 * i), w1 = *(const LAS f32x4*)(wg + 16 * i + 4), w2 = *(const LAS f32x4*)(wg + 16 * i + 8), w3 = *(const LAS f32x4*)(wg + 16 * i + 12);
;                 const r_f32x2 wv[8] = {{w0[0], w0[1]}, {w0[2], w0[3]}, {w1[0], w1[1]}, {w1[2], w1[3]}, {w2[0], w2[1]}, {w2[2], w2[3]}, {w3[0], w3[1]}, {w3[2], w3[3]}};
; #pragma unroll
;                 for (int q = 0; q < 4; ++q) { const float h = xx[q][j][i]; const r_f32x2 hh = {h, h};
; #pragma unroll
;                     for (int e = 0; e < 8; ++e) lg2[q][e] = __builtin_elementwise_fma(hh, wv[e], lg2[q][e]); }
; #pragma unroll
;                 for (int q = 0; q < 4; ++q)
;                     asm volatile("" : "+v"(lg2[q][0]), "+v"(lg2[q][1]), "+v"(lg2[q][2]), "+v"(lg2[q][3]), "+v"(lg2[q][4]), "+v"(lg2[q][5]), "+v"(lg2[q][6]), "+v"(lg2[q][7]));
;                 } }
	v_pk_fma_f32 v[94:95], v[28:29], v[64:65], v[94:95] op_sel:[1,0,0]
	v_pk_fma_f32 v[28:29], v[28:29], v[66:67], v[32:33] op_sel:[1,0,0]
	v_pk_fma_f32 v[32:33], v[52:53], v[10:11], v[54:55] op_sel:[1,0,0]
	v_pk_fma_f32 v[96:97], v[52:53], v[12:13], v[96:97] op_sel:[1,0,0]
	v_pk_fma_f32 v[100:101], v[52:53], v[14:15], v[100:101] op_sel:[1,0,0]
	v_pk_fma_f32 v[102:103], v[52:53], v[16:17], v[102:103] op_sel:[1,0,0]
	v_pk_fma_f32 v[104:105], v[52:53], v[58:59], v[104:105] op_sel:[1,0,0]
	v_pk_fma_f32 v[106:107], v[52:53], v[60:61], v[106:107] op_sel:[1,0,0]
	v_pk_fma_f32 v[108:109], v[52:53], v[64:65], v[108:109] op_sel:[1,0,0]
	v_pk_fma_f32 v[70:71], v[52:53], v[66:67], v[70:71] op_sel:[1,0,0]
	v_pk_fma_f32 v[110:111], v[68:69], v[10:11], v[110:111] op_sel:[1,0,0]
	v_pk_fma_f32 v[112:113], v[68:69], v[12:13], v[112:113] op_sel:[1,0,0]
	v_pk_fma_f32 v[114:115], v[68:69], v[14:15], v[114:115] op_sel:[1,0,0]
	v_pk_fma_f32 v[116:117], v[68:69], v[16:17], v[116:117] op_sel:[1,0,0]
	v_pk_fma_f32 v[118:119], v[68:69], v[58:59], v[118:119] op_sel:[1,0,0]
	v_pk_fma_f32 v[120:121], v[68:69], v[60:61], v[120:121] op_sel:[1,0,0]
	v_pk_fma_f32 v[122:123], v[68:69], v[64:65], v[122:123] op_sel:[1,0,0]
	v_pk_fma_f32 v[68:69], v[68:69], v[66:67], v[72:73] op_sel:[1,0,0]
	v_pk_fma_f32 v[72:73], v[8:9], v[10:11], v[124:125] op_sel:[1,0,0]
	v_pk_fma_f32 v[124:125], v[8:9], v[12:13], v[126:127] op_sel:[1,0,0]
	v_pk_fma_f32 v[126:127], v[8:9], v[14:15], v[128:129] op_sel:[1,0,0]
	v_pk_fma_f32 v[16:17], v[8:9], v[16:17], v[130:131] op_sel:[1,0,0]
	v_pk_fma_f32 v[74:75], v[8:9], v[58:59], v[74:75] op_sel:[1,0,0]
	v_pk_fma_f32 v[76:77], v[8:9], v[60:61], v[76:77] op_sel:[1,0,0]
	v_pk_fma_f32 v[64:65], v[8:9], v[64:65], v[78:79] op_sel:[1,0,0]
	v_pk_fma_f32 v[66:67], v[8:9], v[66:67], v[80:81] op_sel:[1,0,0]
	s_nop 0
	ds_read_b128 v[8:11], v1 offset:34944
	ds_read_b128 v[12:15], v1 offset:34960
	ds_read_b128 v[52:55], v1 offset:34976
	ds_read_b128 v[58:61], v1 offset:34992
	s_waitcnt lgkmcnt(3)
	v_pk_fma_f32 v[78:79], v[24:25], v[8:9], v[82:83] op_sel_hi:[0,1,1]
	v_pk_fma_f32 v[80:81], v[24:25], v[10:11], v[84:85] op_sel_hi:[0,1,1]
	s_waitcnt lgkmcnt(2)
	v_pk_fma_f32 v[82:83], v[24:25], v[12:13], v[86:87] op_sel_hi:[0,1,1]
	v_pk_fma_f32 v[84:85], v[24:25], v[14:15], v[88:89] op_sel_hi:[0,1,1]
	s_waitcnt lgkmcnt(1)
	v_pk_fma_f32 v[86:87], v[24:25], v[52:53], v[90:91] op_sel_hi:[0,1,1]
	v_pk_fma_f32 v[88:89], v[24:25], v[54:55], v[92:93] op_sel_hi:[0,1,1]
	s_waitcnt lgkmcnt(0)
	v_pk_fma_f32 v[90:91], v[24:25], v[58:59], v[94:95] op_sel_hi:[0,1,1]
	v_pk_fma_f32 v[28:29], v[24:25], v[60:61], v[28:29] op_sel_hi:[0,1,1]
	v_pk_fma_f32 v[32:33], v[30:31], v[8:9], v[32:33] op_sel_hi:[0,1,1]
	v_pk_fma_f32 v[92:93], v[30:31], v[10:11], v[96:97] op_sel_hi:[0,1,1]
	v_pk_fma_f32 v[94:95], v[30:31], v[12:13], v[100:101] op_sel_hi:[0,1,1]
	v_pk_fma_f32 v[96:97], v[30:31], v[14:15], v[102:103] op_sel_hi:[0,1,1]
	v_pk_fma_f32 v[100:101], v[30:31], v[52:53], v[104:105] op_sel_hi:[0,1,1]
	v_pk_fma_f32 v[102:103], v[30:31], v[54:55], v[106:107] op_sel_hi:[0,1,1]
	v_pk_fma_f32 v[104:105], v[30:31], v[58:59], v[108:109] op_sel_hi:[0,1,1]
	v_pk_fma_f32 v[70:71], v[30:31], v[60:61], v[70:71] op_sel_hi:[0,1,1]
	v_pk_fma_f32 v[106:107], v[62:63], v[8:9], v[110:111] op_sel_hi:[0,1,1]
	v_pk_fma_f32 v[108:109], v[62:63], v[10:11], v[112:113] op_sel_hi:[0,1,1]
	v_pk_fma_f32 v[110:111], v[62:63], v[12:13], v[114:115] op_sel_hi:[0,1,1]
	v_pk_fma_f32 v[112:113], v[62:63], v[14:15], v[116:117] op_sel_hi:[0,1,1]
	v_pk_fma_f32 v[114:115], v[62:63], v[52:53], v[118:119] op_sel_hi:[0,1,1]
	v_pk_fma_f32 v[116:117], v[62:63], v[54:55], v[120:121] op_sel_hi:[0,1,1]
	v_pk_fma_f32 v[118:119], v[62:63], v[58:59], v[122:123] op_sel_hi:[0,1,1]
	v_pk_fma_f32 v[68:69], v[62:63], v[60:61], v[68:69] op_sel_hi:[0,1,1]
	v_pk_fma_f32 v[72:73], v[6:7], v[8:9], v[72:73] op_sel_hi:[0,1,1]
	v_pk_fma_f32 v[120:121], v[6:7], v[10:11], v[124:125] op_sel_hi:[0,1,1]
	v_pk_fma_f32 v[122:123], v[6:7], v[12:13], v[126:127] op_sel_hi:[0,1,1]
	v_pk_fma_f32 v[16:17], v[6:7], v[14:15], v[16:17] op_sel_hi:[0,1,1]
	v_pk_fma_f32 v[74:75], v[6:7], v[52:53], v[74:75] op_sel_hi:[0,1,1]
	v_pk_fma_f32 v[76:77], v[6:7], v[54:55], v[76:77] op_sel_hi:[0,1,1]
	v_pk_fma_f32 v[64:65], v[6:7], v[58:59], v[64:65] op_sel_hi:[0,1,1]
	v_pk_fma_f32 v[66:67], v[6:7], v[60:61], v[66:67] op_sel_hi:[0,1,1]
	ds_read_b128 v[8:11], v1 offset:35008
	ds_read_b128 v[12:15], v1 offset:35024
	ds_read_b128 v[52:55], v1 offset:35040
	ds_read_b128 v[58:61], v1 offset:35056
	s_waitcnt lgkmcnt(3)
	v_pk_fma_f32 v[78:79], v[24:25], v[8:9], v[78:79] op_sel:[1,0,0]
	v_pk_fma_f32 v[80:81], v[24:25], v[10:11], v[80:81] op_sel:[1,0,0]
	s_waitcnt lgkmcnt(2)
	v_pk_fma_f32 v[82:83], v[24:25], v[12:13], v[82:83] op_sel:[1,0,0]
	v_pk_fma_f32 v[84:85], v[24:25], v[14:15], v[84:85] op_sel:[1,0,0]
	s_waitcnt lgkmcnt(1)
	v_pk_fma_f32 v[86:87], v[24:25], v[52:53], v[86:87] op_sel:[1,0,0]
	v_pk_fma_f32 v[88:89], v[24:25], v[54:55], v[88:89] op_sel:[1,0,0]
	s_waitcnt lgkmcnt(0)
; #define LAS __attribute__((address_space(3)))
; __device__ __forceinline__ void phase_post_mix(Frame& F, int l) {
;     ...
;         for (int j = 0; j < 4; ++j) { const LAS float* wg = rws + (lane + 64 * j) * 68;
; #pragma unroll
;             for (int i = 0; i < 4; ++i) { const f32x4 w0 = *(const LAS f32x4*)(wg + 16 * i), w1 = *(const LAS f32x4*)(wg + 16 * i + 4), w2 = *(const LAS f32x4*)(wg + 16 * i + 8), w3 = *(const LAS f32x4*)(wg + 16 * i + 12);
;                 const r_f32x2 wv[8] = {{w0[0], w0[1]}, {w0[2], w0[3]}, {w1[0], w1[1]}, {w1[2], w1[3]}, {w2[0], w2[1]}, {w2[2], w2[3]}, {w3[0], w3[1]}, {w3[2], w3[3]}};
; #pragma unroll
;                 for (int q = 0; q < 4; ++q) { const float h = xx[q][j][i]; const r_f32x2 hh = {h, h};
; #pragma unroll
;                     for (int e = 0; e < 8; ++e) lg2[q][e] = __builtin_elementwise_fma(hh, wv[e], lg2[q][e]); }
; #pragma unroll
;                 for (int q = 0; q < 4; ++q)
;                     asm volatile("" : "+v"(lg2[q][0]), "+v"(lg2[q][1]), "+v"(lg2[q][2]), "+v"(lg2[q][3]), "+v"(lg2[q][4]), "+v"(lg2[q][5]), "+v"(lg2[q][6]), "+v"(lg2[q][7]));
;                 } }
	v_pk_fma_f32 v[90:91], v[24:25], v[58:59], v[90:91] op_sel:[1,0,0]
	v_pk_fma_f32 v[24:25], v[24:25], v[60:61], v[28:29] op_sel:[1,0,0]
	v_pk_fma_f32 v[32:33], v[30:31], v[8:9], v[32:33] op_sel:[1,0,0]
	v_pk_fma_f32 v[92:93], v[30:31], v[10:11], v[92:93] op_sel:[1,0,0]
	v_pk_fma_f32 v[94:95], v[30:31], v[12:13], v[94:95] op_sel:[1,0,0]
	v_pk_fma_f32 v[96:97], v[30:31], v[14:15], v[96:97] op_sel:[1,0,0]
	v_pk_fma_f32 v[100:101], v[30:31], v[52:53], v[100:101] op_sel:[1,0,0]
	v_pk_fma_f32 v[102:103], v[30:31], v[54:55], v[102:103] op_sel:[1,0,0]
	v_pk_fma_f32 v[104:105], v[30:31], v[58:59], v[104:105] op_sel:[1,0,0]
	v_pk_fma_f32 v[70:71], v[30:31], v[60:61], v[70:71] op_sel:[1,0,0]
	v_pk_fma_f32 v[106:107], v[62:63], v[8:9], v[106:107] op_sel:[1,0,0]
	v_pk_fma_f32 v[108:109], v[62:63], v[10:11], v[108:109] op_sel:[1,0,0]
	v_pk_fma_f32 v[110:111], v[62:63], v[12:13], v[110:111] op_sel:[1,0,0]
	v_pk_fma_f32 v[112:113], v[62:63], v[14:15], v[112:113] op_sel:[1,0,0]
	v_pk_fma_f32 v[114:115], v[62:63], v[52:53], v[114:115] op_sel:[1,0,0]
	v_pk_fma_f32 v[116:117], v[62:63], v[54:55], v[116:117] op_sel:[1,0,0]
	v_pk_fma_f32 v[118:119], v[62:63], v[58:59], v[118:119] op_sel:[1,0,0]
	v_pk_fma_f32 v[62:63], v[62:63], v[60:61], v[68:69] op_sel:[1,0,0]
	v_pk_fma_f32 v[68:69], v[6:7], v[8:9], v[72:73] op_sel:[1,0,0]
	v_pk_fma_f32 v[72:73], v[6:7], v[10:11], v[120:121] op_sel:[1,0,0]
	v_pk_fma_f32 v[120:121], v[6:7], v[12:13], v[122:123] op_sel:[1,0,0]
	v_pk_fma_f32 v[122:123], v[6:7], v[14:15], v[16:17] op_sel:[1,0,0]
	v_pk_fma_f32 v[52:53], v[6:7], v[52:53], v[74:75] op_sel:[1,0,0]
	v_pk_fma_f32 v[54:55], v[6:7], v[54:55], v[76:77] op_sel:[1,0,0]
	v_pk_fma_f32 v[58:59], v[6:7], v[58:59], v[64:65] op_sel:[1,0,0]
	v_pk_fma_f32 v[60:61], v[6:7], v[60:61], v[66:67] op_sel:[1,0,0]
	s_nop 0
	ds_read_b128 v[6:9], v1 offset:52224
	ds_read_b128 v[10:13], v1 offset:52240
	ds_read_b128 v[14:17], v1 offset:52256
	ds_read_b128 v[28:31], v1 offset:52272
	s_waitcnt lgkmcnt(3)
	v_pk_fma_f32 v[64:65], v[20:21], v[6:7], v[78:79] op_sel_hi:[0,1,1]
	v_pk_fma_f32 v[66:67], v[20:21], v[8:9], v[80:81] op_sel_hi:[0,1,1]
	s_waitcnt lgkmcnt(2)
	v_pk_fma_f32 v[74:75], v[20:21], v[10:11], v[82:83] op_sel_hi:[0,1,1]
	v_pk_fma_f32 v[76:77], v[20:21], v[12:13], v[84:85] op_sel_hi:[0,1,1]
	s_waitcnt lgkmcnt(1)
	v_pk_fma_f32 v[78:79], v[20:21], v[14:15], v[86:87] op_sel_hi:[0,1,1]
	v_pk_fma_f32 v[80:81], v[20:21], v[16:17], v[88:89] op_sel_hi:[0,1,1]
	s_waitcnt lgkmcnt(0)
	v_pk_fma_f32 v[82:83], v[20:21], v[28:29], v[90:91] op_sel_hi:[0,1,1]
	v_pk_fma_f32 v[24:25], v[20:21], v[30:31], v[24:25] op_sel_hi:[0,1,1]
	v_pk_fma_f32 v[32:33], v[26:27], v[6:7], v[32:33] op_sel_hi:[0,1,1]
	v_pk_fma_f32 v[84:85], v[26:27], v[8:9], v[92:93] op_sel_hi:[0,1,1]
	v_pk_fma_f32 v[86:87], v[26:27], v[10:11], v[94:95] op_sel_hi:[0,1,1]
	v_pk_fma_f32 v[88:89], v[26:27], v[12:13], v[96:97] op_sel_hi:[0,1,1]
	v_pk_fma_f32 v[90:91], v[26:27], v[14:15], v[100:101] op_sel_hi:[0,1,1]
	v_pk_fma_f32 v[92:93], v[26:27], v[16:17], v[102:103] op_sel_hi:[0,1,1]
	v_pk_fma_f32 v[94:95], v[26:27], v[28:29], v[104:105] op_sel_hi:[0,1,1]
	v_pk_fma_f32 v[70:71], v[26:27], v[30:31], v[70:71] op_sel_hi:[0,1,1]
	v_pk_fma_f32 v[96:97], v[56:57], v[6:7], v[106:107] op_sel_hi:[0,1,1]
	v_pk_fma_f32 v[100:101], v[56:57], v[8:9], v[108:109] op_sel_hi:[0,1,1]
	v_pk_fma_f32 v[102:103], v[56:57], v[10:11], v[110:111] op_sel_hi:[0,1,1]
	v_pk_fma_f32 v[104:105], v[56:57], v[12:13], v[112:113] op_sel_hi:[0,1,1]
	v_pk_fma_f32 v[106:107], v[56:57], v[14:15], v[114:115] op_sel_hi:[0,1,1]
	v_pk_fma_f32 v[108:109], v[56:57], v[16:17], v[116:117] op_sel_hi:[0,1,1]
	v_pk_fma_f32 v[110:111], v[56:57], v[28:29], v[118:119] op_sel_hi:[0,1,1]
	v_pk_fma_f32 v[62:63], v[56:57], v[30:31], v[62:63] op_sel_hi:[0,1,1]
	v_pk_fma_f32 v[68:69], v[4:5], v[6:7], v[68:69] op_sel_hi:[0,1,1]
	v_pk_fma_f32 v[72:73], v[4:5], v[8:9], v[72:73] op_sel_hi:[0,1,1]
	v_pk_fma_f32 v[112:113], v[4:5], v[10:11], v[120:121] op_sel_hi:[0,1,1]
	v_pk_fma_f32 v[114:115], v[4:5], v[12:13], v[122:123] op_sel_hi:[0,1,1]
	v_pk_fma_f32 v[52:53], v[4:5], v[14:15], v[52:53] op_sel_hi:[0,1,1]
	v_pk_fma_f32 v[54:55], v[4:5], v[16:17], v[54:55] op_sel_hi:[0,1,1]
	v_pk_fma_f32 v[58:59], v[4:5], v[28:29], v[58:59] op_sel_hi:[0,1,1]
	v_pk_fma_f32 v[60:61], v[4:5], v[30:31], v[60:61] op_sel_hi:[0,1,1]
	ds_read_b128 v[6:9], v1 offset:52288
	ds_read_b128 v[10:13], v1 offset:52304
	ds_read_b128 v[14:17], v1 offset:52320
	ds_read_b128 v[28:31], v1 offset:52336
	s_waitcnt lgkmcnt(3)
	v_pk_fma_f32 v[64:65], v[20:21], v[6:7], v[64:65] op_sel:[1,0,0]
	v_pk_fma_f32 v[66:67], v[20:21], v[8:9], v[66:67] op_sel:[1,0,0]
	s_waitcnt lgkmcnt(2)
	v_pk_fma_f32 v[74:75], v[20:21], v[10:11], v[74:75] op_sel:[1,0,0]
	v_pk_fma_f32 v[76:77], v[20:21], v[12:13], v[76:77] op_sel:[1,0,0]
	s_waitcnt lgkmcnt(1)
	v_pk_fma_f32 v[78:79], v[20:21], v[14:15], v[78:79] op_sel:[1,0,0]
	v_pk_fma_f32 v[80:81], v[20:21], v[16:17], v[80:81] op_sel:[1,0,0]
	s_waitcnt lgkmcnt(0)
; #define LAS __attribute__((address_space(3)))
; __device__ __forceinline__ void phase_post_mix(Frame& F, int l) {
;     ...
;         for (int j = 0; j < 4; ++j) { const LAS float* wg = rws + (lane + 64 * j) * 68;
; #pragma unroll
;             for (int i = 0; i < 4; ++i) { const f32x4 w0 = *(const LAS f32x4*)(wg + 16 * i), w1 = *(const LAS f32x4*)(wg + 16 * i + 4), w2 = *(const LAS f32x4*)(wg + 16 * i + 8), w3 = *(const LAS f32x4*)(wg + 16 * i + 12);
;                 const r_f32x2 wv[8] = {{w0[0], w0[1]}, {w0[2], w0[3]}, {w1[0], w1[1]}, {w1[2], w1[3]}, {w2[0], w2[1]}, {w2[2], w2[3]}, {w3[0], w3[1]}, {w3[2], w3[3]}};
; #pragma unroll
;                 for (int q = 0; q < 4; ++q) { const float h = xx[q][j][i]; const r_f32x2 hh = {h, h};
; #pragma unroll
;                     for (int e = 0; e < 8; ++e) lg2[q][e] = __builtin_elementwise_fma(hh, wv[e], lg2[q][e]); }
; #pragma unroll
;                 for (int q = 0; q < 4; ++q)
;                     asm volatile("" : "+v"(lg2[q][0]), "+v"(lg2[q][1]), "+v"(lg2[q][2]), "+v"(lg2[q][3]), "+v"(lg2[q][4]), "+v"(lg2[q][5]), "+v"(lg2[q][6]), "+v"(lg2[q][7]));
;                 } }
	v_pk_fma_f32 v[82:83], v[20:21], v[28:29], v[82:83] op_sel:[1,0,0]
	v_pk_fma_f32 v[20:21], v[20:21], v[30:31], v[24:25] op_sel:[1,0,0]
	v_pk_fma_f32 v[32:33], v[26:27], v[6:7], v[32:33] op_sel:[1,0,0]
	v_pk_fma_f32 v[84:85], v[26:27], v[8:9], v[84:85] op_sel:[1,0,0]
	v_pk_fma_f32 v[86:87], v[26:27], v[10:11], v[86:87] op_sel:[1,0,0]
	v_pk_fma_f32 v[88:89], v[26:27], v[12:13], v[88:89] op_sel:[1,0,0]
	v_pk_fma_f32 v[90:91], v[26:27], v[14:15], v[90:91] op_sel:[1,0,0]
	v_pk_fma_f32 v[92:93], v[26:27], v[16:17], v[92:93] op_sel:[1,0,0]
	v_pk_fma_f32 v[94:95], v[26:27], v[28:29], v[94:95] op_sel:[1,0,0]
	v_pk_fma_f32 v[70:71], v[26:27], v[30:31], v[70:71] op_sel:[1,0,0]
	v_pk_fma_f32 v[96:97], v[56:57], v[6:7], v[96:97] op_sel:[1,0,0]
	v_pk_fma_f32 v[100:101], v[56:57], v[8:9], v[100:101] op_sel:[1,0,0]
	v_pk_fma_f32 v[102:103], v[56:57], v[10:11], v[102:103] op_sel:[1,0,0]
	v_pk_fma_f32 v[104:105], v[56:57], v[12:13], v[104:105] op_sel:[1,0,0]
	v_pk_fma_f32 v[106:107], v[56:57], v[14:15], v[106:107] op_sel:[1,0,0]
	v_pk_fma_f32 v[108:109], v[56:57], v[16:17], v[108:109] op_sel:[1,0,0]
	v_pk_fma_f32 v[110:111], v[56:57], v[28:29], v[110:111] op_sel:[1,0,0]
	v_pk_fma_f32 v[56:57], v[56:57], v[30:31], v[62:63] op_sel:[1,0,0]
	v_pk_fma_f32 v[62:63], v[4:5], v[6:7], v[68:69] op_sel:[1,0,0]
	v_pk_fma_f32 v[68:69], v[4:5], v[8:9], v[72:73] op_sel:[1,0,0]
	v_pk_fma_f32 v[72:73], v[4:5], v[10:11], v[112:113] op_sel:[1,0,0]
	v_pk_fma_f32 v[112:113], v[4:5], v[12:13], v[114:115] op_sel:[1,0,0]
	v_pk_fma_f32 v[52:53], v[4:5], v[14:15], v[52:53] op_sel:[1,0,0]
	v_pk_fma_f32 v[16:17], v[4:5], v[16:17], v[54:55] op_sel:[1,0,0]
	v_pk_fma_f32 v[28:29], v[4:5], v[28:29], v[58:59] op_sel:[1,0,0]
	v_pk_fma_f32 v[30:31], v[4:5], v[30:31], v[60:61] op_sel:[1,0,0]
	s_nop 0
	ds_read_b128 v[4:7], v1 offset:52352
	ds_read_b128 v[8:11], v1 offset:52368
	ds_read_b128 v[12:15], v1 offset:52384
	ds_read_b128 v[24:27], v1 offset:52400
	s_waitcnt lgkmcnt(3)
	v_pk_fma_f32 v[54:55], v[18:19], v[4:5], v[64:65] op_sel_hi:[0,1,1]
	v_pk_fma_f32 v[58:59], v[18:19], v[6:7], v[66:67] op_sel_hi:[0,1,1]
	s_waitcnt lgkmcnt(2)
	v_pk_fma_f32 v[60:61], v[18:19], v[8:9], v[74:75] op_sel_hi:[0,1,1]
	v_pk_fma_f32 v[64:65], v[18:19], v[10:11], v[76:77] op_sel_hi:[0,1,1]
	s_waitcnt lgkmcnt(1)
	v_pk_fma_f32 v[66:67], v[18:19], v[12:13], v[78:79] op_sel_hi:[0,1,1]
	v_pk_fma_f32 v[80:81], v[18:19], v[14:15], v[80:81] op_sel_hi:[0,1,1]
	s_waitcnt lgkmcnt(0)
	v_pk_fma_f32 v[82:83], v[18:19], v[24:25], v[82:83] op_sel_hi:[0,1,1]
	v_pk_fma_f32 v[20:21], v[18:19], v[26:27], v[20:21] op_sel_hi:[0,1,1]
	v_pk_fma_f32 v[32:33], v[22:23], v[4:5], v[32:33] op_sel_hi:[0,1,1]
	v_pk_fma_f32 v[84:85], v[22:23], v[6:7], v[84:85] op_sel_hi:[0,1,1]
	v_pk_fma_f32 v[86:87], v[22:23], v[8:9], v[86:87] op_sel_hi:[0,1,1]
	v_pk_fma_f32 v[88:89], v[22:23], v[10:11], v[88:89] op_sel_hi:[0,1,1]
	v_pk_fma_f32 v[90:91], v[22:23], v[12:13], v[90:91] op_sel_hi:[0,1,1]
	v_pk_fma_f32 v[92:93], v[22:23], v[14:15], v[92:93] op_sel_hi:[0,1,1]
	v_pk_fma_f32 v[94:95], v[22:23], v[24:25], v[94:95] op_sel_hi:[0,1,1]
	v_pk_fma_f32 v[114:115], v[22:23], v[26:27], v[70:71] op_sel_hi:[0,1,1]
	v_pk_fma_f32 v[96:97], v[50:51], v[4:5], v[96:97] op_sel_hi:[0,1,1]
	v_pk_fma_f32 v[100:101], v[50:51], v[6:7], v[100:101] op_sel_hi:[0,1,1]
	v_pk_fma_f32 v[102:103], v[50:51], v[8:9], v[102:103] op_sel_hi:[0,1,1]
	v_pk_fma_f32 v[104:105], v[50:51], v[10:11], v[104:105] op_sel_hi:[0,1,1]
	v_pk_fma_f32 v[106:107], v[50:51], v[12:13], v[106:107] op_sel_hi:[0,1,1]
	v_pk_fma_f32 v[108:109], v[50:51], v[14:15], v[108:109] op_sel_hi:[0,1,1]
	v_pk_fma_f32 v[110:111], v[50:51], v[24:25], v[110:111] op_sel_hi:[0,1,1]
	v_pk_fma_f32 v[116:117], v[50:51], v[26:27], v[56:57] op_sel_hi:[0,1,1]
	v_pk_fma_f32 v[118:119], v[2:3], v[4:5], v[62:63] op_sel_hi:[0,1,1]
	v_pk_fma_f32 v[120:121], v[2:3], v[6:7], v[68:69] op_sel_hi:[0,1,1]
	v_pk_fma_f32 v[8:9], v[2:3], v[8:9], v[72:73] op_sel_hi:[0,1,1]
	v_pk_fma_f32 v[112:113], v[2:3], v[10:11], v[112:113] op_sel_hi:[0,1,1]
	v_pk_fma_f32 v[12:13], v[2:3], v[12:13], v[52:53] op_sel_hi:[0,1,1]
	v_pk_fma_f32 v[122:123], v[2:3], v[14:15], v[16:17] op_sel_hi:[0,1,1]
	v_pk_fma_f32 v[124:125], v[2:3], v[24:25], v[28:29] op_sel_hi:[0,1,1]
	v_pk_fma_f32 v[126:127], v[2:3], v[26:27], v[30:31] op_sel_hi:[0,1,1]
	ds_read_b128 v[4:7], v1 offset:52416
	ds_read_b128 v[68:71], v1 offset:52432
	ds_read_b128 v[72:75], v1 offset:52448
	ds_read_b128 v[76:79], v1 offset:52464
	s_waitcnt lgkmcnt(3)
	v_pk_fma_f32 v[128:129], v[18:19], v[4:5], v[54:55] op_sel:[1,0,0]
	v_pk_fma_f32 v[130:131], v[18:19], v[6:7], v[58:59] op_sel:[1,0,0]
	s_waitcnt lgkmcnt(2)
	v_pk_fma_f32 v[132:133], v[18:19], v[68:69], v[60:61] op_sel:[1,0,0]
	v_pk_fma_f32 v[134:135], v[18:19], v[70:71], v[64:65] op_sel:[1,0,0]
	s_waitcnt lgkmcnt(1)
	v_pk_fma_f32 v[136:137], v[18:19], v[72:73], v[66:67] op_sel:[1,0,0]
	v_pk_fma_f32 v[80:81], v[18:19], v[74:75], v[80:81] op_sel:[1,0,0]
	s_waitcnt lgkmcnt(0)
; #define GAS __attribute__((address_space(1)))
; __device__ __forceinline__ void post_mix_route(Frame& F, int m, float (&lg)[16]) {
;     const int lane = F.lane, b = m >> 12, t = m & (SEQ - 1);
;     const bool b5 = (lane & 32) != 0, b4 = (lane & 16) != 0, b3 = (lane & 8) != 0, b2 = (lane & 4) != 0;
;     float a8[8], a4[4], a2[2];
; #pragma unroll
;     for (int e = 0; e < 8; ++e) a8[e] = swap32_sum(lg[e], lg[8 + e]);
; #pragma unroll
;     for (int e = 0; e < 4; ++e) a4[e] = swap16_sum(a8[e], a8[4 + e]);
; #pragma unroll
;     for (int e = 0; e < 2; ++e) { const float keep = b3 ? a4[2 + e] : a4[e], send = b3 ? a4[e] : a4[2 + e]; a2[e] = keep + dpp_f<DPP_ROR8>(send); }
;     float v = (b2 ? a2[1] : a2[0]) + dpp_f<DPP_HMIR>(b2 ? a2[0] : a2[1]);
;     v += dpp_f<DPP_X2>(v); v += dpp_f<DPP_X1>(v);
;     float mx = fmaxf(v, dpp_f<DPP_HMIR>(v)); mx = fmaxf(mx, dpp_f<DPP_ROR8>(mx)); mx = swap16_max(mx); mx = swap32_max(mx);
;     const float ex = expf(v - mx); float den = ex + dpp_f<DPP_HMIR>(ex); den += dpp_f<DPP_ROR8>(den); den = swap16_sum(den, den); den = swap32_sum(den, den);
;     const int e = (b5 ? 8 : 0) + (b4 ? 4 : 0) + (b3 ? 2 : 0) + (b2 ? 1 : 0);
;     if ((lane & 3) == 0) ((GAS float*)(F.ws + WS_AFF))[((size_t)b * NEXP + e) * SEQ + t] = ex / den;
; __device__ __forceinline__ void phase_post_mix(Frame& F, int l) {
;     ...
;         for (int j = 0; j < 4; ++j) { const LAS float* wg = rws + (lane + 64 * j) * 68;
; #pragma unroll
;             for (int i = 0; i < 4; ++i) { const f32x4 w0 = *(const LAS f32x4*)(wg + 16 * i), w1 = *(const LAS f32x4*)(wg + 16 * i + 4), w2 = *(const LAS f32x4*)(wg + 16 * i + 8), w3 = *(const LAS f32x4*)(wg + 16 * i + 12);
;                 const r_f32x2 wv[8] = {{w0[0], w0[1]}, {w0[2], w0[3]}, {w1[0], w1[1]}, {w1[2], w1[3]}, {w2[0], w2[1]}, {w2[2], w2[3]}, {w3[0], w3[1]}, {w3[2], w3[3]}};
; #pragma unroll
;                 for (int q = 0; q < 4; ++q) { const float h = xx[q][j][i]; const r_f32x2 hh = {h, h};
; #pragma unroll
;                     for (int e = 0; e < 8; ++e) lg2[q][e] = __builtin_elementwise_fma(hh, wv[e], lg2[q][e]); }
; #pragma unroll
;                 for (int q = 0; q < 4; ++q)
;                     asm volatile("" : "+v"(lg2[q][0]), "+v"(lg2[q][1]), "+v"(lg2[q][2]), "+v"(lg2[q][3]), "+v"(lg2[q][4]), "+v"(lg2[q][5]), "+v"(lg2[q][6]), "+v"(lg2[q][7]));
;                 } }
	v_pk_fma_f32 v[82:83], v[18:19], v[76:77], v[82:83] op_sel:[1,0,0]
	v_pk_fma_f32 v[138:139], v[18:19], v[78:79], v[20:21] op_sel:[1,0,0]
	v_pk_fma_f32 v[64:65], v[22:23], v[4:5], v[32:33] op_sel:[1,0,0]
	v_pk_fma_f32 v[60:61], v[22:23], v[6:7], v[84:85] op_sel:[1,0,0]
	v_permlane32_swap_b32_e32 v128, v136
	v_permlane32_swap_b32_e32 v129, v137
	v_permlane32_swap_b32_e32 v130, v80
	v_permlane32_swap_b32_e32 v131, v81
	v_permlane32_swap_b32_e32 v132, v82
	v_permlane32_swap_b32_e32 v133, v83
	v_permlane32_swap_b32_e32 v134, v138
	v_permlane32_swap_b32_e32 v135, v139
	v_pk_fma_f32 v[56:57], v[22:23], v[68:69], v[86:87] op_sel:[1,0,0]
	v_pk_fma_f32 v[52:53], v[22:23], v[70:71], v[88:89] op_sel:[1,0,0]
	v_pk_fma_f32 v[66:67], v[22:23], v[72:73], v[90:91] op_sel:[1,0,0]
	v_pk_fma_f32 v[62:63], v[22:23], v[74:75], v[92:93] op_sel:[1,0,0]
	v_pk_fma_f32 v[58:59], v[22:23], v[76:77], v[94:95] op_sel:[1,0,0]
	v_pk_fma_f32 v[54:55], v[22:23], v[78:79], v[114:115] op_sel:[1,0,0]
	v_pk_fma_f32 v[30:31], v[50:51], v[4:5], v[96:97] op_sel:[1,0,0]
	v_pk_fma_f32 v[26:27], v[50:51], v[6:7], v[100:101] op_sel:[1,0,0]
	v_pk_fma_f32 v[22:23], v[50:51], v[68:69], v[102:103] op_sel:[1,0,0]
	v_pk_fma_f32 v[18:19], v[50:51], v[70:71], v[104:105] op_sel:[1,0,0]
	v_pk_fma_f32 v[32:33], v[50:51], v[72:73], v[106:107] op_sel:[1,0,0]
	v_pk_fma_f32 v[28:29], v[50:51], v[74:75], v[108:109] op_sel:[1,0,0]
	v_pk_fma_f32 v[24:25], v[50:51], v[76:77], v[110:111] op_sel:[1,0,0]
	v_pk_fma_f32 v[20:21], v[50:51], v[78:79], v[116:117] op_sel:[1,0,0]
	v_pk_fma_f32 v[14:15], v[2:3], v[4:5], v[118:119] op_sel:[1,0,0]
	v_pk_fma_f32 v[10:11], v[2:3], v[6:7], v[120:121] op_sel:[1,0,0]
	v_pk_fma_f32 v[6:7], v[2:3], v[68:69], v[8:9] op_sel:[1,0,0]
	v_pk_fma_f32 v[4:5], v[2:3], v[70:71], v[112:113] op_sel:[1,0,0]
	v_pk_fma_f32 v[16:17], v[2:3], v[72:73], v[12:13] op_sel:[1,0,0]
	v_add_f32_e32 v50, v128, v136
	v_add_f32_e32 v51, v129, v137
	v_add_f32_e32 v68, v130, v80
	v_add_f32_e32 v69, v131, v81
	v_add_f32_e32 v70, v132, v82
	v_add_f32_e32 v71, v133, v83
	v_add_f32_e32 v72, v134, v138
	v_add_f32_e32 v73, v135, v139
	v_permlane16_swap_b32_e32 v50, v70
	v_permlane16_swap_b32_e32 v51, v71
	v_permlane16_swap_b32_e32 v68, v72
	v_permlane16_swap_b32_e32 v69, v73
	v_add_f32_e32 v50, v50, v70
	v_add_f32_e32 v51, v51, v71
	v_add_f32_e32 v68, v68, v72
	v_add_f32_e32 v69, v69, v73
	v_cndmask_b32_e64 v70, v68, v50, s[4:5]
	v_cndmask_b32_e64 v50, v50, v68, s[4:5]
	v_cndmask_b32_e64 v68, v69, v51, s[4:5]
	v_cndmask_b32_e64 v51, v51, v69, s[4:5]
	v_add_f32_dpp v50, v50, v70 row_ror:8 row_mask:0xf bank_mask:0xf bound_ctrl:1
	v_pk_fma_f32 v[12:13], v[2:3], v[74:75], v[122:123] op_sel:[1,0,0]
	v_add_f32_dpp v51, v51, v68 row_ror:8 row_mask:0xf bank_mask:0xf bound_ctrl:1
	v_cndmask_b32_e64 v68, v51, v50, s[6:7]
	v_cndmask_b32_e64 v50, v50, v51, s[6:7]
	v_pk_fma_f32 v[8:9], v[2:3], v[76:77], v[124:125] op_sel:[1,0,0]
	v_pk_fma_f32 v[2:3], v[2:3], v[78:79], v[126:127] op_sel:[1,0,0]
	v_add_f32_dpp v50, v50, v68 row_half_mirror row_mask:0xf bank_mask:0xf bound_ctrl:1
	s_nop 1
	v_add_f32_dpp v50, v50, v50 quad_perm:[2,3,0,1] row_mask:0xf bank_mask:0xf bound_ctrl:1
	s_nop 1
	v_add_f32_dpp v50, v50, v50 quad_perm:[1,0,3,2] row_mask:0xf bank_mask:0xf bound_ctrl:1
	s_nop 1
	v_mov_b32_dpp v51, v50 row_half_mirror row_mask:0xf bank_mask:0xf bound_ctrl:1
	v_max_f32_e32 v51, v51, v51
	v_max_f32_e32 v51, v50, v51
	s_nop 1
	v_mov_b32_dpp v68, v51 row_ror:8 row_mask:0xf bank_mask:0xf bound_ctrl:1
	v_max_f32_e32 v68, v68, v68
	v_max_f32_e32 v51, v51, v68
	v_mov_b32_e32 v68, v51
	s_nop 1
	v_permlane16_swap_b32_e32 v51, v68
	v_max_f32_e32 v68, v68, v68
	v_max_f32_e32 v51, v51, v51
	v_max_f32_e32 v51, v51, v68
	v_mov_b32_e32 v68, v51
	s_nop 1
	v_permlane32_swap_b32_e32 v51, v68
	v_max_f32_e32 v68, v68, v68
	v_max_f32_e32 v51, v51, v51
	v_max_f32_e32 v51, v51, v68
	v_sub_f32_e32 v50, v50, v51
	v_mul_f32_e32 v51, 0x3fb8aa3b, v50
	v_fma_f32 v68, v50, s78, -v51
	v_rndne_f32_e32 v69, v51
	v_fmac_f32_e32 v68, 0x32a5705f, v50
	v_sub_f32_e32 v51, v51, v69
	v_add_f32_e32 v51, v51, v68
	v_exp_f32_e32 v51, v51
	v_cvt_i32_f32_e32 v68, v69
	v_cmp_ngt_f32_e32 vcc, s2, v50
	s_mov_b32 s2, 0x42b17218
	v_ldexp_f32 v51, v51, v68
	v_cndmask_b32_e32 v51, 0, v51, vcc
	v_cmp_nlt_f32_e32 vcc, s2, v50
	s_nop 1
	v_cndmask_b32_e32 v50, v242, v51, vcc
	s_nop 1
	v_add_f32_dpp v51, v50, v50 row_half_mirror row_mask:0xf bank_mask:0xf bound_ctrl:1
	s_nop 1
	v_add_f32_dpp v51, v51, v51 row_ror:8 row_mask:0xf bank_mask:0xf bound_ctrl:1
	v_mov_b32_e32 v68, v51
	s_nop 1
	v_permlane16_swap_b32_e32 v51, v68
	v_add_f32_e32 v51, v51, v68
	v_mov_b32_e32 v68, v51
	s_nop 1
	v_permlane32_swap_b32_e32 v51, v68
	s_and_saveexec_b64 s[2:3], s[8:9]
	s_cbranch_execnz .LBB0_1253
	s_or_b64 exec, exec, s[2:3]
	s_cmp_eq_u32 s14, s28
	s_cbranch_scc0 .LBB0_1254

; #define GAS __attribute__((address_space(1)))
; #define LAS __attribute__((address_space(3)))
; __device__ __forceinline__ void phase_topk(Frame& F) {
;     const int tid = F.tid, lane = F.lane, wave = F.wave;
;     LAS unsigned* hist = (LAS unsigned*)F.lds;
;     LAS unsigned* ctl = hist + 256;
;     LAS unsigned* lst = hist + 512;
;     const GAS float* aff = (const GAS float*)(F.ws + WS_AFF); GAS int* slotp = (GAS int*)(F.ws + WS_SLOT); GAS float* gate = (GAS float*)(F.ws + WS_GATE);
;     const GAS unsigned char* hn8 = (const GAS unsigned char*)(F.ws + WS_HN); GAS unsigned char* xg8 = (GAS unsigned char*)(F.ws + WS_XG);
;     for (int it = F.vcu; it < BATCH * NEXP * 4; it += F.G) { const int be = it >> 2, qu = it & 3, b = be >> 4, e = be & 15;
;         const GAS f32x4* ap = (const GAS f32x4*)(aff + (size_t)be * SEQ + 8 * tid); const f32x4 v0 = ap[0], v1 = ap[1];
;         unsigned key[8];
; #pragma unroll
;         for (int j = 0; j < 4; ++j) { key[j] = __float_as_uint(v0[j]); key[4 + j] = __float_as_uint(v1[j]); }
.LBB0_1387:
	v_mov_b32_e32 v2, v0
	s_nop 0
	v_readfirstlane_b32 s0, v2
	s_ashr_i32 s89, s0, 6
	s_cmpk_gt_i32 s93, 0xff
	v_and_b32_e32 v186, 63, v2
	s_cbranch_scc1 .LBB0_1506
	s_add_u32 s84, s80, 0x400000
	s_addc_u32 s85, s81, 0
	s_cmp_lt_u32 s0, 64
	s_cselect_b64 s[66:67], -1, 0
	s_lshl_b32 s0, s89, 2
	s_add_i32 s64, s0, 0
	s_cmp_gt_i32 s89, 0
	s_mov_b32 s8, s89
	s_cselect_b64 s[88:89], -1, 0
	s_cmp_gt_i32 s8, 1
	s_cselect_b64 s[76:77], -1, 0
	s_cmp_gt_i32 s8, 2
	v_lshlrev_b32_e32 v30, 3, v2
	s_cselect_b64 s[72:73], -1, 0
	s_cmp_gt_i32 s8, 3
	v_writelane_b32 v255, s24, 6
	v_ashrrev_i32_e32 v31, 31, v30
	s_movk_i32 s1, 0x100
	s_cselect_b64 s[74:75], -1, 0
	s_cmp_gt_i32 s8, 4
	v_writelane_b32 v255, s25, 7
	v_lshl_add_u64 v[4:5], v[30:31], 2, s[80:81]
	v_cmp_gt_i32_e64 s[6:7], s1, v2
	v_lshlrev_b32_e32 v182, 4, v186
	s_cselect_b64 s[82:83], -1, 0
	s_cmp_gt_i32 s8, 5
	s_mov_b64 s[22:23], s[80:81]
	s_mov_b64 s[0:1], 0x300000
	v_cmp_eq_u32_e64 s[4:5], 0, v2
	v_lshl_add_u32 v1, v2, 2, 0
	s_cselect_b64 s[2:3], -1, 0
	s_cmp_gt_i32 s8, 6
	v_ashrrev_i32_e32 v49, 7, v2
	v_lshl_add_u64 v[34:35], v[4:5], 0, s[0:1]
	v_writelane_b32 v255, s22, 8
	s_mov_b64 s[0:1], 0xac00000
	s_cselect_b64 s[80:81], -1, 0
	v_lshl_add_u64 v[2:3], s[22:23], 0, v[182:183]
	s_cmp_gt_i32 s8, 7
	v_lshl_add_u64 v[36:37], v[2:3], 0, s[0:1]
	s_mov_b64 s[0:1], 0x4400000
	s_cselect_b64 s[70:71], -1, 0
	v_lshl_add_u64 v[38:39], v[2:3], 0, s[0:1]
	s_lshl_b32 s0, s8, 5
	v_lshlrev_b32_e32 v31, 2, v186
	v_writelane_b32 v255, s23, 9
	s_add_i32 s69, s0, 0
	v_lshl_add_u64 v[32:33], v[4:5], 0, s[96:97]
	v_add_u32_e32 v42, 0, v182
	v_add_u32_e32 v43, -4, v31
	v_cmp_eq_u32_e64 s[10:11], 0, v186
	v_add_u32_e32 v44, -8, v31
	v_cmp_gt_u32_e64 s[96:97], 2, v186
	v_add_u32_e32 v45, -16, v31
	v_cmp_gt_u32_e64 s[12:13], 4, v186
	v_subrev_u32_e32 v46, 32, v31
	v_cmp_gt_u32_e64 s[14:15], 8, v186
	v_subrev_u32_e32 v47, 64, v31
	v_cmp_gt_u32_e64 s[16:17], 16, v186
	v_add_u32_e32 v48, 0xffffff80, v31
	v_cmp_gt_u32_e64 s[18:19], 32, v186
	v_cmp_eq_u32_e64 s[20:21], 63, v186
	s_lshl_b32 s65, s8, 3
	v_add_u32_e32 v50, 4, v31
	v_add_u32_e32 v51, 8, v31
	v_cmp_gt_u32_e64 s[22:23], 62, v186
	v_add_u32_e32 v52, 16, v31
	v_cmp_gt_u32_e64 s[24:25], 60, v186
	v_add_u32_e32 v53, 32, v31
	v_cmp_gt_u32_e64 s[26:27], 56, v186
	v_add_u32_e32 v54, 64, v31
	v_cmp_gt_u32_e64 s[28:29], 48, v186
	v_add_u32_e32 v55, 0x80, v31
	v_or_b32_e32 v56, 1, v30
	v_or_b32_e32 v57, 2, v30
	v_or_b32_e32 v58, 3, v30
	v_or_b32_e32 v59, 4, v30
	v_or_b32_e32 v60, 5, v30
	v_or_b32_e32 v61, 6, v30
	v_or_b32_e32 v62, 7, v30
	v_writelane_b32 v255, s8, 10
	s_addk_i32 s69, 0x800
	s_branch .LBB0_1390

; template <class Epi, class Sched, bool ALIGN_EPI = false, bool SP2 = false, bool F8 = false, bool BTILED = false, bool ATILED = false>
; __device__ __forceinline__ void gemm_phase(PG8_LAS unsigned char* lds, const Gemm g, const Sched& S, const Epi& E) {
;     ...
;     for (int i = 0; i < 2; ++i) { int R, C; stage_rc(tid * 16 + i * 8192, R, C); const int Rb = Epi::PERM ? ((R & ~31) + perm32(R & 31)) : R;
;         voffA[i] = ATILED ? (unsigned)((C >> 5) * 16384 + R * 64 + (C & 31) * 2) : (unsigned)(R * K + C) * 2u; voffB[i] = BTILED ? (unsigned)((C >> 5) * 16384 + Rb * 64 + (C & 31) * 2) : (unsigned)(Rb * K + C) * 2u; }
;     const size_t kstep = (size_t)(BK * 2);
;     const size_t hstep = (size_t)HALF * K * 2;
;     const size_t tstep = 2 * hstep;
;     const size_t kstepB = BTILED ? (size_t)32768 : kstep, hstepB = BTILED ? (size_t)8192 : hstep;
;     const size_t kstepA = ATILED ? (size_t)32768 : kstep, hstepA = ATILED ? (size_t)8192 : hstep;
;     const unsigned ldsw = (unsigned)wid * 1024u;
;     const int aoff = lds_byte(wr * 64 + fr, fq * 8), boff = lds_byte(wc * 32 + fr, fq * 8);
;     ...
;     Unit cur, nxt; int ui = 0;
;     if (!S.next(0, cur)) return;
;     f32x4 acc[2][2][4][2];
; #pragma unroll
;     for (int a = 0; a < 2; ++a)
; #pragma unroll
;         for (int b = 0; b < 2; ++b)
; #pragma unroll
;             for (int m = 0; m < 4; ++m)
; #pragma unroll
;                 for (int n = 0; n < 2; ++n) acc[a][b][m][n] = (f32x4){0.f, 0.f, 0.f, 0.f};
;     bf16x8 At[4][2], B0[2][2], B1[2][2];
;     const char* cA = (const char*)g.A + (size_t)cur.pm * tstep; const char* cB = (const char*)g.Bt + (size_t)cur.pn * tstep;
;     S.a_ready(cur);
;     if constexpr (SP2) {
;         PG8_STAGE(PG8_SB(0, 0), cB, voffB); PG8_STAGE(PG8_SB(0, 1), cB + hstepB, voffB); PG8_STAGE(PG8_SA(0, 0), cA, voffA); PG8_STAGE(PG8_SA(0, 1), cA + hstepA, voffA);
;         if (wr == 1) PG8_BAR;
;         PG8_WAIT_V(2); PG8_BAR;
;         PG8_STAGE(PG8_SB(1, 0), cB + kstepB, voffB); PG8_STAGE(PG8_SA(1, 0), cA + kstepA, voffA); PG8_STAGE(PG8_SB(1, 1), cB + hstepB + kstepB, voffB);
;         PG8_WAIT_V(6); PG8_BAR;
;     } else {
;         PG8_STAGE(PG8_SB(0, 0), cB, voffB); PG8_STAGE(PG8_SA(0, 0), cA, voffA); PG8_STAGE(PG8_SB(0, 1), cB + hstepB, voffB); PG8_STAGE(PG8_SA(0, 1), cA + hstepA, voffA);
;         if (wr == 1) PG8_BAR;
;         PG8_WAIT_V(4); PG8_BAR;
.LBB0_1648:
	v_mov_b32_e32 v1, v0
	s_waitcnt vmcnt(0)
	v_mov_b32_e32 v8, v0
	s_cmpk_gt_i32 s25, 0xaff
	v_readfirstlane_b32 s26, v1
	v_readfirstlane_b32 s4, v8
	s_cbranch_scc1 .LBB0_1664
	v_lshlrev_b32_e32 v2, 4, v8
	v_add_u32_e32 v3, 0x2000, v2
	v_ashrrev_i32_e32 v4, 31, v3
	v_lshrrev_b32_e32 v4, 22, v4
	v_add_u32_e32 v4, v3, v4
	v_ashrrev_i32_e32 v6, 10, v4
	v_mul_i32_i24_e32 v4, 0x400, v6
	v_sub_u32_e32 v3, v3, v4
	v_lshrrev_b32_e32 v4, 4, v3
	v_bitop3_b32 v3, v4, v3, 32 bitop3:0x6c
	v_ashrrev_i32_e32 v4, 31, v3
	s_add_u32 s27, s80, 0x4400000
	v_lshrrev_b32_e32 v4, 26, v4
	s_mul_i32 s2, s54, 0x5800000
	s_addc_u32 s28, s81, 0
	v_add_u32_e32 v4, v3, v4
	v_lshlrev_b32_e32 v5, 3, v6
	s_add_u32 s2, s80, s2
	v_ashrrev_i32_e32 v7, 6, v4
	v_and_b32_e32 v5, -16, v5
	s_addc_u32 s3, s81, 0
	v_add_u32_e32 v5, v7, v5
	s_add_u32 s29, s2, 0x2b400000
	v_and_b32_e32 v9, 3, v7
	s_mov_b32 s2, 0x3ffffe0
	v_lshrrev_b32_e32 v10, 2, v5
	v_lshlrev_b32_e32 v11, 1, v5
	v_and_b32_e32 v4, 0xc0, v4
	v_and_or_b32 v9, v5, s2, v9
	v_and_b32_e32 v10, 4, v10
	v_and_b32_e32 v11, 24, v11
	v_sub_u32_e32 v3, v3, v4
	v_or3_b32 v10, v9, v10, v11
	v_lshlrev_b32_e32 v9, 5, v6
	v_ashrrev_i16_sdwa v3, v224, sext(v3) dst_sel:DWORD dst_unused:UNUSED_PAD src0_sel:DWORD src1_sel:BYTE_0
	v_and_b32_e32 v11, 32, v9
	v_bfe_i32 v9, v3, 0, 16
	v_add_u32_e32 v3, v11, v9
	v_lshlrev_b32_e32 v4, 9, v3
	v_and_b32_e32 v4, 0xffffc000, v4
	v_lshl_add_u32 v4, v10, 6, v4
	v_lshlrev_b32_e32 v3, 1, v3
	v_and_or_b32 v162, v3, 62, v4
	v_lshl_add_u32 v164, v5, 10, v3
	v_bfe_i32 v3, v8, 27, 1
	v_lshrrev_b32_e32 v3, 22, v3
	v_add_u32_e32 v3, v2, v3
	v_and_b32_e32 v3, 0xfffffc00, v3
	v_sub_u32_e32 v2, v2, v3
	v_lshrrev_b32_e32 v3, 4, v2
	v_ashrrev_i32_e32 v4, 31, v8
	v_bitop3_b32 v2, v3, v2, 32 bitop3:0x6c
	v_lshrrev_b32_e32 v4, 26, v4
	v_ashrrev_i32_e32 v3, 31, v2
	v_add_u32_e32 v4, v8, v4
	v_lshrrev_b32_e32 v3, 26, v3
	v_ashrrev_i32_e32 v11, 6, v4
	v_add_u32_e32 v3, v2, v3
	v_lshlrev_b32_e32 v4, 3, v11
	v_ashrrev_i32_e32 v10, 6, v3
	v_and_b32_e32 v4, -16, v4
	v_add_u32_e32 v4, v10, v4
	v_and_b32_e32 v5, 3, v10
	v_and_or_b32 v5, v4, s2, v5
	s_mul_hi_i32 s2, s25, 0x2e8ba2e9
	s_addc_u32 s30, s3, 0
	s_lshr_b32 s3, s2, 31
	s_ashr_i32 s2, s2, 5
	s_add_i32 s2, s2, s3
	v_lshrrev_b32_e32 v12, 2, v4
	v_lshlrev_b32_e32 v13, 1, v4
	v_and_b32_e32 v3, 0xc0, v3
	s_mul_i32 s3, s2, 0xb0
	v_and_b32_e32 v12, 4, v12
	v_and_b32_e32 v13, 24, v13
	v_sub_u32_e32 v2, v2, v3
	s_sub_i32 s3, s25, s3
	v_or3_b32 v5, v5, v12, v13
	v_lshlrev_b32_e32 v12, 5, v11
	v_ashrrev_i16_sdwa v2, v224, sext(v2) dst_sel:DWORD dst_unused:UNUSED_PAD src0_sel:DWORD src1_sel:BYTE_0
	s_lshl_b32 s6, s2, 3
	s_and_b32 s7, s3, 7
	s_ashr_i32 s43, s3, 3
	s_mul_i32 s2, s2, 22
	v_and_b32_e32 v13, 32, v12
	v_bfe_i32 v12, v2, 0, 16
	s_or_b32 s18, s7, s6
	s_add_i32 s2, s2, s43
	s_ashr_i32 s5, s4, 6
	v_add_u32_e32 v2, v13, v12
	s_ashr_i32 s3, s2, 31
	s_ashr_i32 s19, s18, 31
	s_ashr_i32 s8, s4, 8
	s_lshl_b32 s31, s5, 10
	v_lshlrev_b32_e32 v3, 9, v2
	s_lshl_b64 s[2:3], s[2:3], 18
	s_lshl_b64 s[6:7], s[18:19], 18
	v_and_b32_e32 v3, 0xffffc000, v3
	s_add_u32 s2, s29, s2
	v_lshl_add_u32 v3, v5, 6, v3
	v_lshlrev_b32_e32 v2, 1, v2
	s_addc_u32 s3, s30, s3
	s_add_i32 s19, s31, 0
	v_and_or_b32 v166, v2, 62, v3
	s_add_i32 m0, s19, 0x10000
	v_lshl_add_u32 v182, v4, 10, v2
	global_load_lds_dwordx4 v166, s[2:3]
	s_add_i32 m0, s19, 0x12000
	s_add_u32 s10, s2, 0x2000
	global_load_lds_dwordx4 v162, s[2:3]
	s_addc_u32 s11, s3, 0
	s_add_i32 m0, s19, 0x14000
	v_mov_b32_e32 v165, v183
	global_load_lds_dwordx4 v166, s[10:11]
	s_add_i32 m0, s19, 0x16000
	s_add_u32 s20, s27, s6
	s_addc_u32 s21, s28, s7
	s_add_i32 s34, s19, 0x2000
	global_load_lds_dwordx4 v162, s[10:11]
	s_mov_b32 m0, s19
	s_add_u32 s6, s20, 0x20000
	global_load_lds_dwordx4 v182, s[20:21]
	s_mov_b32 m0, s34
	s_addc_u32 s7, s21, 0
	s_add_i32 s35, s19, 0x4000
	global_load_lds_dwordx4 v164, s[20:21]
	s_mov_b32 m0, s35
	s_add_i32 s36, s19, 0x6000
	global_load_lds_dwordx4 v182, s[6:7]
	s_mov_b32 m0, s36
	s_cmp_eq_u32 s8, 1
	global_load_lds_dwordx4 v164, s[6:7]
	v_lshl_add_u64 v[2:3], s[20:21], 0, v[182:183]
	s_cselect_b64 s[6:7], -1, 0
	s_cmp_lg_u32 s8, 1
	v_lshl_add_u64 v[4:5], s[20:21], 0, v[164:165]
	s_cbranch_scc1 .LBB0_1651
	s_barrier

; #define PG8_STAGE(bufoff, gbase, voff) do { _Pragma("unroll") for (int _i = 0; _i < 2; ++_i) \
;         __builtin_amdgcn_global_load_lds((const unsigned*)((const char*)(gbase) + (voff)[_i]), (PG8_LAS unsigned*)(lds + (bufoff) + ldsw + _i * 8192), 16, 0, 0); } while (0)
; #define PG8_WAIT_V(n) asm volatile("s_waitcnt vmcnt(" #n ")" ::: "memory")
; #define PG8_BAR __builtin_amdgcn_s_barrier()
; template <class Epi, class Sched, bool ALIGN_EPI = false, bool SP2 = false, bool F8 = false, bool BTILED = false, bool ATILED = false>
; __device__ __forceinline__ void gemm_phase(PG8_LAS unsigned char* lds, const Gemm g, const Sched& S, const Epi& E) {
;     ...
;         PG8_STAGE(PG8_SB(0, 0), cB, voffB); PG8_STAGE(PG8_SB(0, 1), cB + hstepB, voffB); PG8_STAGE(PG8_SA(0, 0), cA, voffA); PG8_STAGE(PG8_SA(0, 1), cA + hstepA, voffA);
;         if (wr == 1) PG8_BAR;
;         PG8_WAIT_V(2); PG8_BAR;
;         PG8_STAGE(PG8_SB(1, 0), cB + kstepB, voffB); PG8_STAGE(PG8_SA(1, 0), cA + kstepA, voffA); PG8_STAGE(PG8_SB(1, 1), cB + hstepB + kstepB, voffB);
;         PG8_WAIT_V(6); PG8_BAR;
; __global__ void __launch_bounds__(NTHR, 2) fwd_kernel(Args args) {
;     ...
;             pg8::Gemm g{(const pg8::bf16_t*)(F.ws + WS_H), (const pg8::bf16_t*)(F.ws + WS_WD + (size_t)l * NEXP * DM * FF), NEXP * EROWS, NEXP * DM, FF / 2};
;             pg8::MoeOrder S; S.init(4, F.G, F.vcu);
;             pg8::EpiBf16Row E{(pg8::bf16_t*)(F.ws + WS_YE), DM, (const float*)(F.ws + WS_GATE), 1.0f / W8_SCALE};
;             pg8::gemm_phase<pg8::EpiBf16Row, pg8::MoeOrder, true, true, true, true, true>(F.lds, g, S, E);
.LBB0_1793:
	s_add_u32 s12, s80, 0x4400000
	s_addc_u32 s13, s81, 0
	s_add_u32 s14, s80, 0x400000
	s_addc_u32 s15, s81, 0
	s_lshl_b32 s0, s16, 5
	s_and_b32 s20, s0, 0x60
	s_lshl_b32 s17, s5, 13
	s_lshl_b32 s16, s20, 7
	s_add_u32 s0, s2, 0x8000
	s_addc_u32 s1, s3, 0
	s_add_i32 m0, s38, 0x18000
	v_lshl_add_u64 v[12:13], s[0:1], 0, v[182:183]
	v_mov_b32_e32 v167, v183
	s_waitcnt vmcnt(2)
	s_barrier
	global_load_lds_dwordx4 v[12:13], off
	s_add_i32 m0, s38, 0x1a000
	v_lshl_add_u64 v[12:13], s[0:1], 0, v[166:167]
	s_add_u32 s0, s6, 0x8000
	v_mov_b32_e32 v163, v183
	s_addc_u32 s1, s7, 0
	s_add_i32 s42, s38, 0x8000
	v_mov_b32_e32 v165, v183
	global_load_lds_dwordx4 v[12:13], off
	v_lshl_add_u64 v[12:13], s[0:1], 0, v[162:163]
	s_mov_b32 m0, s42
	s_add_i32 s43, s38, 0xa000
	global_load_lds_dwordx4 v[12:13], off
	v_lshl_add_u64 v[12:13], s[0:1], 0, v[164:165]
	s_add_u32 s0, s2, 0xa000
	s_mov_b32 m0, s43
	s_addc_u32 s1, s3, 0
	global_load_lds_dwordx4 v[12:13], off
	s_add_i32 m0, s38, 0x1c000
	v_lshl_add_u64 v[12:13], s[0:1], 0, v[182:183]
	global_load_lds_dwordx4 v[12:13], off
	v_lshl_add_u64 v[12:13], s[0:1], 0, v[166:167]
	s_add_i32 m0, s38, 0x1e000
	v_and_b32_e32 v11, 15, v2
	global_load_lds_dwordx4 v[12:13], off
	v_lshrrev_b32_e32 v12, 1, v2
	v_and_b32_e32 v12, 24, v12
	v_lshlrev_b32_e32 v13, 1, v12
	v_lshlrev_b32_e32 v2, 2, v2
	v_lshl_or_b32 v172, s5, 6, v11
	v_lshl_or_b32 v11, v11, 6, v13
	v_and_b32_e32 v2, 32, v2
	v_bitop3_b32 v13, v11, s17, v2 bitop3:0xde
	v_bitop3_b32 v173, v11, s16, v2 bitop3:0xde
	v_lshlrev_b32_e32 v2, 9, v3
	v_and_b32_e32 v2, 0xfffffc00, v2
	v_add_u32_e32 v2, v5, v2
	v_add3_u32 v2, v2, v4, v6
	v_mov_b32_e32 v3, v183
	s_mov_b64 s[0:1], 0xa000
	v_lshl_add_u64 v[168:169], v[2:3], 0, s[0:1]
	v_lshlrev_b32_e32 v2, 9, v7
	s_cmpk_lt_u32 s4, 0x100
	v_and_b32_e32 v2, 0xfffffc00, v2
	s_waitcnt vmcnt(6)
	s_cselect_b64 s[16:17], -1, 0
	s_ashr_i32 s44, s28, 31
	s_ashr_i32 s45, s30, 31
	v_add_u32_e32 v2, v9, v2
	s_cmp_lg_u64 s[80:81], 0
	v_add3_u32 v2, v2, v8, v10
	s_cselect_b64 s[18:19], -1, 0
	v_or_b32_e32 v174, s20, v12
	v_lshl_add_u64 v[170:171], v[2:3], 0, s[0:1]
	s_mov_b32 s46, 0
	v_add_u32_e32 v175, 0, v13
	s_barrier
	s_branch .LBB0_1796

; #define GAS __attribute__((address_space(1)))
; #define LAS __attribute__((address_space(3)))
; __device__ __forceinline__ void phase_combine(Frame& F, int l) {
;     const int gw = F.vcu * NWAVES + F.wave, NGW = F.G * NWAVES, lane = F.lane;
;     const GAS float* modl = (const GAS float*)(F.ws + WS_MOD) + (size_t)l * 4 * 6144;
;     const GAS int* slot = (const GAS int*)(F.ws + WS_SLOT); const GAS bf16* ye = (const GAS bf16*)(F.ws + WS_YE);
;     LAS float* PV = (LAS float*)F.lds;
;     for (int i = F.tid; i < 4 * 256; i += NTHR) { const int b = i >> 8, c4 = i & 255; const GAS float* mb = modl + (size_t)b * 6144;
;         const f32x4 gf = ((const GAS f32x4*)(mb + 5120))[c4], pg = ((const GAS f32x4*)(INP(F, I_FPOST) + l * DM))[c4];
;         LAS f32x4* pv = (LAS f32x4*)(PV + b * 3072) + ((c4 >> 2) + 64 * (c4 & 3)); pv[0] = gf * pg;
;         if (l + 1 < DEPTH) { const GAS float* mn = modl + 4 * 6144 + (size_t)b * 6144; const f32x4 gg = ((const GAS f32x4*)(INP(F, I_MPRE) + (l + 1) * DM))[c4], s1 = ((const GAS f32x4*)(mn + 1024))[c4], s0 = ((const GAS f32x4*)mn)[c4];
;             pv[256] = gg * (1.0f + s1); pv[512] = s0; } }
;     __syncthreads();
;     for (int m0 = gw; m0 < M; m0 += 2 * NGW) {
;         int mm[2]; mm[0] = m0; mm[1] = (m0 + NGW < M) ? m0 + NGW : m0;
;         int sl[2]; unsigned long long mask[2]; f32x4 y[2][4], x[2][4];
; #pragma unroll
;         for (int q = 0; q < 2; ++q) { const int b = mm[q] >> 12, t = mm[q] & (SEQ - 1); sl[q] = -1; if (lane < 16) sl[q] = slot[((size_t)b * NEXP + lane) * SEQ + t];
;             roww_load_bf16((const GAS bf16*)(F.ws + WS_XR) + (size_t)mm[q] * DM, lane, x[q]);
.LBB0_1956:
	s_or_b64 exec, exec, s[0:1]
	s_ashr_i32 s89, s14, 6
	s_add_i32 s0, s89, s13
	v_and_b32_e32 v186, 63, v1
	s_cmpk_gt_i32 s0, 0x3fff
	s_waitcnt lgkmcnt(0)
	s_barrier
	s_cbranch_scc1 .LBB0_1995
	v_lshlrev_b32_e32 v182, 14, v186
	v_lshl_add_u64 v[2:3], s[58:59], 0, v[182:183]
	s_mov_b64 s[2:3], 0x300000
	v_lshlrev_b32_e32 v182, 5, v186
	v_lshl_add_u64 v[58:59], v[2:3], 0, s[2:3]
	v_lshl_add_u64 v[2:3], s[58:59], 0, v[182:183]
	s_mov_b64 s[2:3], 0x4400000
	v_lshl_add_u64 v[60:61], v[2:3], 0, s[2:3]
	s_mov_b64 s[2:3], 0x27400000
	v_lshl_add_u64 v[62:63], v[2:3], 0, s[2:3]
	v_lshlrev_b32_e32 v182, 6, v186
	s_mov_b64 s[2:3], 0x18400000
	s_lshl_b32 s20, s12, 3
	v_cmp_gt_u32_e64 s[6:7], 16, v186
	s_lshl_b32 s21, s12, 4
	v_lshl_add_u32 v100, v186, 4, 0
	v_lshl_add_u64 v[64:65], s[56:57], 0, v[182:183]
	v_lshl_add_u64 v[66:67], v[2:3], 0, s[2:3]
	s_branch .LBB0_1959
